# row phases P1/P5/P13: all per-column-group gate loads (g/shift/scale) hoisted to the row head into idle VGPRs, per-group vmcnt waits removed (stores no longer serialise the next group's loads); on top
# speedup vs baseline: 1.0274x; 1.0274x over previous
; template <bool COMBINE, bool ROUTE, bool FINAL, bool OUT8 = false, bool DUMMY = false> ...
;     ...
;     for (int m = blockIdx.x * 8 + wave; m < M; m += gridDim.x * 8) {
;         const int b = m / T;
;         f32x4 xv[8];
; #pragma unroll
;         for (int j = 0; j < 8; ++j) xv[j] = *(const f32x4*)(xin + (size_t)m * D + 4 * lane + 256 * j);
;         if (mres) { const float* gta = modl + (size_t)b * 12288 + 2 * D;
; #pragma unroll
;             for (int j = 0; j < 8; ++j) { const int c = 4 * lane + 256 * j; const u32x2 mm = *(const u32x2*)(mres + (size_t)m * D + c); const f32x4 gv = *(const f32x4*)(gta + c);
;                 xv[j].x += gv.x * __uint_as_float(mm.x << 16); xv[j].y += gv.y * __uint_as_float(mm.x & 0xffff0000u); xv[j].z += gv.z * __uint_as_float(mm.y << 16); xv[j].w += gv.w * __uint_as_float(mm.y & 0xffff0000u); } }
;         if (COMBINE) {
;             const int e0 = tok_e[2 * m], e1 = tok_e[2 * m + 1];
;             const size_t r0 = (size_t)(base[e0] + tok_pos[2 * m]), r1 = (size_t)(base[e1] + tok_pos[2 * m + 1]);
;             const float* gt = modprev + (size_t)b * 12288 + 5 * D;
; #pragma unroll
;             for (int j = 0; j < 8; ++j) {
;                 const int c = 4 * lane + 256 * j;
;                 const u32x2 a = *(const u32x2*)(Y + r0 * D + c), bb = *(const u32x2*)(Y + r1 * D + c);
;                 const f32x4 gv = *(const f32x4*)(gt + c);
;                 xv[j].x += gv.x * (__uint_as_float(a.x << 16) + __uint_as_float(bb.x << 16));
;                 xv[j].y += gv.y * (__uint_as_float(a.x & 0xffff0000u) + __uint_as_float(bb.x & 0xffff0000u));
;                 xv[j].z += gv.z * (__uint_as_float(a.y << 16) + __uint_as_float(bb.y << 16));
;                 xv[j].w += gv.w * (__uint_as_float(a.y & 0xffff0000u) + __uint_as_float(bb.y & 0xffff0000u));
;                 if (!FINAL) *(f32x4*)(xnew + (size_t)m * D + c) = xv[j];
;             }
;         }
;         float ss = 0.f;
; #pragma unroll
;         for (int j = 0; j < 8; ++j) ss += xv[j].x * xv[j].x + xv[j].y * xv[j].y + xv[j].z * xv[j].z + xv[j].w * xv[j].w;
;         ss = wave_sum(ss);
;         const float rstd = 1.0f / sqrtf(ss * (1.f / D) + EPS);
;         if (FINAL) {
; #pragma unroll
;             for (int j = 0; j < 8; ++j) { const int c = 4 * lane + 256 * j; const f32x4 gv = *(const f32x4*)(g + c); *(f32x4*)(fout + (size_t)m * D + c) = xv[j] * rstd * gv; }
.LBB0_90:
	v_ashrrev_i32_e32 v35, 31, v34
	v_lshlrev_b64 v[2:3], 13, v[34:35]
	v_lshl_add_u64 v[2:3], v[38:39], 0, v[2:3]
	global_load_dwordx4 v[30:33], v[2:3], off
	global_load_dwordx4 v[26:29], v[2:3], off offset:1024
	global_load_dwordx4 v[22:25], v[2:3], off offset:2048
	global_load_dwordx4 v[18:21], v[2:3], off offset:3072
	v_add_co_u32_e32 v66, vcc, s3, v2
	v_lshrrev_b32_e32 v0, 21, v35
	s_nop 0
	v_addc_co_u32_e32 v67, vcc, 0, v3, vcc
	global_load_dwordx4 v[14:17], v[66:67], off
	global_load_dwordx4 v[10:13], v[66:67], off offset:1024
	global_load_dwordx4 v[6:9], v[66:67], off offset:2048
	global_load_dwordx4 v[2:5], v[66:67], off offset:3072
	global_load_dwordx4 v[78:81], v[40:41], off
	v_add_u32_e32 v0, v34, v0
	v_ashrrev_i32_e32 v0, 11, v0
	v_mul_hi_i32_i24_e32 v67, 0xc000, v0
	v_mul_i32_i24_e32 v66, 0xc000, v0
	v_lshl_add_u64 v[66:67], s[24:25], 0, v[66:67]
	v_lshl_add_u64 v[68:69], v[66:67], 0, s[10:11]
	v_lshl_add_u64 v[92:93], v[68:69], 0, v[36:37]
	v_lshl_add_u64 v[90:91], v[66:67], 0, v[36:37]
	global_load_dwordx4 v[82:85], v[92:93], off
	global_load_dwordx4 v[86:89], v[90:91], off
	global_load_dwordx4 v[104:107], v[40:41], off offset:1024
	v_mov_b32_e32 v108, v52
	v_mov_b32_e32 v109, 0
	v_lshl_add_u64 v[108:109], v[68:69], 0, v[108:109]
	global_load_dwordx4 v[108:111], v[108:109], off
	global_load_dwordx4 v[112:115], v[90:91], off offset:1024
	global_load_dwordx4 v[116:119], v[40:41], off offset:2048
	v_mov_b32_e32 v120, v54
	v_mov_b32_e32 v121, 0
	v_lshl_add_u64 v[120:121], v[68:69], 0, v[120:121]
	global_load_dwordx4 v[120:123], v[120:121], off
	global_load_dwordx4 v[124:127], v[90:91], off offset:2048
	global_load_dwordx4 v[128:131], v[40:41], off offset:3072
	v_mov_b32_e32 v132, v56
	v_mov_b32_e32 v133, 0
	v_lshl_add_u64 v[132:133], v[68:69], 0, v[132:133]
	global_load_dwordx4 v[132:135], v[132:133], off
	global_load_dwordx4 v[136:139], v[90:91], off offset:3072
	global_load_dwordx4 v[140:143], v[42:43], off
	v_mov_b32_e32 v144, v58
	v_mov_b32_e32 v145, 0
	v_lshl_add_u64 v[144:145], v[68:69], 0, v[144:145]
	global_load_dwordx4 v[144:147], v[144:145], off
	v_mov_b32_e32 v148, v58
	v_mov_b32_e32 v149, 0
	v_lshl_add_u64 v[148:149], v[66:67], 0, v[148:149]
	global_load_dwordx4 v[148:151], v[148:149], off
	global_load_dwordx4 v[152:155], v[44:45], off
	v_mov_b32_e32 v156, v60
	v_mov_b32_e32 v157, 0
	v_lshl_add_u64 v[156:157], v[68:69], 0, v[156:157]
	global_load_dwordx4 v[156:159], v[156:157], off
	v_mov_b32_e32 v160, v60
	v_mov_b32_e32 v161, 0
	v_lshl_add_u64 v[160:161], v[66:67], 0, v[160:161]
	global_load_dwordx4 v[160:163], v[160:161], off
	global_load_dwordx4 v[164:167], v[46:47], off
	v_mov_b32_e32 v168, v62
	v_mov_b32_e32 v169, 0
	v_lshl_add_u64 v[168:169], v[68:69], 0, v[168:169]
	global_load_dwordx4 v[168:171], v[168:169], off
	v_mov_b32_e32 v172, v62
	v_mov_b32_e32 v173, 0
	v_lshl_add_u64 v[172:173], v[66:67], 0, v[172:173]
	global_load_dwordx4 v[172:175], v[172:173], off
	global_load_dwordx4 v[176:179], v[48:49], off
	v_mov_b32_e32 v180, v64
	v_mov_b32_e32 v181, 0
	v_lshl_add_u64 v[180:181], v[68:69], 0, v[180:181]
	global_load_dwordx4 v[180:183], v[180:181], off
	v_mov_b32_e32 v184, v64
	v_mov_b32_e32 v185, 0
	v_lshl_add_u64 v[184:185], v[66:67], 0, v[184:185]
	global_load_dwordx4 v[184:187], v[184:185], off
	s_waitcnt vmcnt(0)
	v_mul_f32_e32 v0, v31, v31
	v_mul_f32_e32 v70, v27, v27
	v_mul_f32_e32 v100, v23, v23
	v_fmac_f32_e32 v0, v30, v30
	v_fmac_f32_e32 v70, v26, v26
	v_mul_f32_e32 v101, v19, v19
	v_fmac_f32_e32 v100, v22, v22
	v_fmac_f32_e32 v0, v32, v32
	v_fmac_f32_e32 v70, v28, v28
	v_fmac_f32_e32 v101, v18, v18
	v_fmac_f32_e32 v100, v24, v24
	v_mul_f32_e32 v102, v15, v15
	v_fmac_f32_e32 v0, v33, v33
	v_fmac_f32_e32 v70, v29, v29
	v_fmac_f32_e32 v101, v20, v20
	v_mul_f32_e32 v103, v11, v11
	v_mov_b32_e32 v94, v7
	v_mov_b32_e32 v95, v3
	v_fmac_f32_e32 v100, v25, v25
	v_fmac_f32_e32 v102, v14, v14
	v_add_f32_e32 v0, v0, v70
	v_mov_b32_e32 v92, v6
	v_mov_b32_e32 v93, v2
	v_fmac_f32_e32 v101, v21, v21
	v_fmac_f32_e32 v103, v10, v10
	v_pk_mul_f32 v[94:95], v[94:95], v[94:95]
	v_fmac_f32_e32 v102, v16, v16
	v_add_f32_e32 v0, v0, v100
	v_mov_b32_e32 v96, v8
	v_mov_b32_e32 v97, v4
	v_fmac_f32_e32 v103, v12, v12
	v_pk_fma_f32 v[92:93], v[92:93], v[92:93], v[94:95]
	v_fmac_f32_e32 v102, v17, v17
	v_add_f32_e32 v0, v0, v101
	v_mov_b32_e32 v98, v9
	v_mov_b32_e32 v99, v5
	v_fmac_f32_e32 v103, v13, v13
	v_pk_fma_f32 v[92:93], v[96:97], v[96:97], v[92:93]
	v_add_f32_e32 v0, v0, v102
	v_pk_fma_f32 v[92:93], v[98:99], v[98:99], v[92:93]
	v_add_f32_e32 v0, v0, v103
	v_add_f32_e32 v0, v0, v92
	v_add_f32_e32 v0, v0, v93
	ds_bpermute_b32 v70, v1, v0
	v_pk_add_f32 v[82:83], v[82:83], 1.0 op_sel_hi:[1,0]
	v_mov_b32_e32 v92, 0
	v_pk_add_f32 v[84:85], v[84:85], 1.0 op_sel_hi:[1,0]
	s_waitcnt lgkmcnt(0)
	v_add_f32_e32 v0, v0, v70
	ds_bpermute_b32 v70, v71, v0
	s_waitcnt lgkmcnt(0)
	v_add_f32_e32 v0, v0, v70
	ds_bpermute_b32 v70, v72, v0
	s_waitcnt lgkmcnt(0)
	v_add_f32_e32 v0, v0, v70
	ds_bpermute_b32 v70, v73, v0
	s_waitcnt lgkmcnt(0)
	v_add_f32_e32 v0, v0, v70
	ds_bpermute_b32 v70, v74, v0
	s_waitcnt lgkmcnt(0)
	v_add_f32_e32 v0, v0, v70
	ds_bpermute_b32 v70, v75, v0
	s_waitcnt lgkmcnt(0)
; __device__ __forceinline__ unsigned pk2(float a, float b) { f32x2 v = {a, b}; bf16x2_t r = __builtin_convertvector(v, bf16x2_t); return __builtin_bit_cast(unsigned, r); }
; __device__ __forceinline__ unsigned pk4_fp8(float a, float b, float c, float d) { unsigned w = 0u; w = __builtin_amdgcn_cvt_pk_fp8_f32(a, b, w, false); w = __builtin_amdgcn_cvt_pk_fp8_f32(c, d, w, true); return w; }
; template <bool COMBINE, bool ROUTE, bool FINAL, bool OUT8 = false, bool DUMMY = false> ...
;     ...
;         const float rstd = 1.0f / sqrtf(ss * (1.f / D) + EPS);
;         if (FINAL) {
; #pragma unroll
;             for (int j = 0; j < 8; ++j) { const int c = 4 * lane + 256 * j; const f32x4 gv = *(const f32x4*)(g + c); *(f32x4*)(fout + (size_t)m * D + c) = xv[j] * rstd * gv; }
;         } else {
;             const float* sh = modl + (size_t)b * 12288 + sh_off; const float* sc = modl + (size_t)b * 12288 + sc_off;
; #pragma unroll
;             for (int j = 0; j < 8; ++j) {
;                 const int c = 4 * lane + 256 * j;
;                 const f32x4 gv = *(const f32x4*)(g + c), shv = *(const f32x4*)(sh + c), scv = *(const f32x4*)(sc + c);
;                 xv[j] = xv[j] * rstd * gv * (1.f + scv) + shv;
;                 if (OUT8) *(unsigned*)((unsigned char*)hout + (size_t)m * D + c) = pk4_fp8(xv[j].x * F8_SA, xv[j].y * F8_SA, xv[j].z * F8_SA, xv[j].w * F8_SA);
;                 else { u32x2 o; o.x = pk2(xv[j].x, xv[j].y); o.y = pk2(xv[j].z, xv[j].w); *(u32x2*)(hout + (size_t)m * D + c) = o; }
	v_add_f32_e32 v0, v0, v70
	v_fmamk_f32 v0, v0, 0x3a000000, v76
	v_mul_f32_e32 v70, 0x4f800000, v0
	v_cmp_gt_f32_e32 vcc, s12, v0
	s_nop 1
	v_cndmask_b32_e32 v0, v0, v70, vcc
	v_sqrt_f32_e32 v70, v0
	s_nop 0
	v_add_u32_e32 v93, -1, v70
	v_add_u32_e32 v94, 1, v70
	v_fma_f32 v95, -v93, v70, v0
	v_fma_f32 v96, -v94, v70, v0
	v_cmp_ge_f32_e64 s[4:5], 0, v95
	s_nop 1
	v_cndmask_b32_e64 v70, v70, v93, s[4:5]
	v_cmp_lt_f32_e64 s[4:5], 0, v96
	s_nop 1
	v_cndmask_b32_e64 v70, v70, v94, s[4:5]
	v_mul_f32_e32 v93, 0x37800000, v70
	v_cndmask_b32_e32 v70, v70, v93, vcc
	v_cmp_class_f32_e32 vcc, v0, v77
	s_nop 1
	v_cndmask_b32_e32 v0, v70, v0, vcc
	v_div_scale_f32 v70, s[4:5], v0, v0, 1.0
	v_rcp_f32_e32 v93, v70
	v_div_scale_f32 v94, vcc, 1.0, v0, 1.0
	v_fma_f32 v95, -v70, v93, 1.0
	v_fmac_f32_e32 v93, v95, v93
	v_mul_f32_e32 v95, v94, v93
	v_fma_f32 v96, -v70, v95, v94
	v_fmac_f32_e32 v95, v96, v93
	v_fma_f32 v70, -v70, v95, v94
	v_div_fmas_f32 v70, v70, v93, v95
	v_div_fixup_f32 v70, v70, v0, 1.0
	v_pk_mul_f32 v[30:31], v[30:31], v[70:71] op_sel_hi:[1,0]
	v_pk_mul_f32 v[32:33], v[32:33], v[70:71] op_sel_hi:[1,0]
	v_pk_mul_f32 v[30:31], v[78:79], v[30:31]
	v_pk_mul_f32 v[32:33], v[80:81], v[32:33]
	v_pk_fma_f32 v[30:31], v[82:83], v[30:31], v[86:87]
	v_pk_mul_f32 v[26:27], v[26:27], v[70:71] op_sel_hi:[1,0]
	v_mul_f32_e32 v0, 0x41800000, v30
	v_mul_f32_e32 v30, 0x41800000, v31
	v_cvt_pk_fp8_f32 v92, v0, v30
	v_pk_fma_f32 v[30:31], v[84:85], v[32:33], v[88:89]
	v_lshl_add_u64 v[32:33], v[68:69], 0, v[52:53]
	v_mul_f32_e32 v0, 0x41800000, v30
	v_mul_f32_e32 v30, 0x41800000, v31
	v_cvt_pk_fp8_f32 v92, v0, v30 op_sel:[0,0,1]
	v_lshlrev_b64 v[30:31], 11, v[34:35]
	v_lshl_add_u64 v[30:31], v[50:51], 0, v[30:31]
	v_mov_b32_e32 v0, 0
	global_store_dword v[30:31], v92, off
	v_pk_mul_f32 v[28:29], v[28:29], v[70:71] op_sel_hi:[1,0]
	v_pk_mul_f32 v[24:25], v[24:25], v[70:71] op_sel_hi:[1,0]
	v_pk_mul_f32 v[22:23], v[22:23], v[70:71] op_sel_hi:[1,0]
	v_pk_mul_f32 v[20:21], v[20:21], v[70:71] op_sel_hi:[1,0]
	v_pk_mul_f32 v[18:19], v[18:19], v[70:71] op_sel_hi:[1,0]
	v_pk_mul_f32 v[16:17], v[16:17], v[70:71] op_sel_hi:[1,0]
	v_pk_mul_f32 v[14:15], v[14:15], v[70:71] op_sel_hi:[1,0]
	v_pk_mul_f32 v[12:13], v[12:13], v[70:71] op_sel_hi:[1,0]
	v_pk_mul_f32 v[10:11], v[10:11], v[70:71] op_sel_hi:[1,0]
	v_pk_mul_f32 v[8:9], v[8:9], v[70:71] op_sel_hi:[1,0]
	v_pk_mul_f32 v[6:7], v[6:7], v[70:71] op_sel_hi:[1,0]
	v_pk_mul_f32 v[4:5], v[4:5], v[70:71] op_sel_hi:[1,0]
	v_pk_mul_f32 v[2:3], v[2:3], v[70:71] op_sel_hi:[1,0]
	v_add_u32_e32 v34, s60, v34
	v_cmp_lt_i32_e32 vcc, s13, v34
	s_or_b64 s[8:9], vcc, s[8:9]
	v_pk_add_f32 v[32:33], v[110:111], 1.0 op_sel_hi:[1,0]
	v_pk_mul_f32 v[26:27], v[104:105], v[26:27]
	v_pk_add_f32 v[78:79], v[108:109], 1.0 op_sel_hi:[1,0]
	v_pk_mul_f32 v[28:29], v[106:107], v[28:29]
	v_pk_fma_f32 v[26:27], v[78:79], v[26:27], v[112:113]
	s_nop 0
	v_mul_f32_e32 v26, 0x41800000, v26
	v_mul_f32_e32 v27, 0x41800000, v27
	v_cvt_pk_fp8_f32 v0, v26, v27
	v_pk_fma_f32 v[26:27], v[32:33], v[28:29], v[114:115]
	v_lshl_add_u64 v[32:33], v[68:69], 0, v[54:55]
	v_mul_f32_e32 v26, 0x41800000, v26
	v_mul_f32_e32 v27, 0x41800000, v27
	v_cvt_pk_fp8_f32 v0, v26, v27 op_sel:[0,0,1]
	global_store_dword v[30:31], v0, off offset:256
	v_mov_b32_e32 v0, 0
	v_lshl_add_u64 v[32:33], v[68:69], 0, v[56:57]
	v_pk_mul_f32 v[22:23], v[22:23], v[116:117]
	v_pk_mul_f32 v[24:25], v[24:25], v[118:119]
	v_pk_add_f32 v[28:29], v[120:121], 1.0 op_sel_hi:[1,0]
	v_pk_add_f32 v[26:27], v[122:123], 1.0 op_sel_hi:[1,0]
	v_pk_fma_f32 v[22:23], v[22:23], v[28:29], v[124:125]
	s_nop 0
	v_mul_f32_e32 v22, 0x41800000, v22
	v_mul_f32_e32 v23, 0x41800000, v23
; __device__ __forceinline__ unsigned pk2(float a, float b) { f32x2 v = {a, b}; bf16x2_t r = __builtin_convertvector(v, bf16x2_t); return __builtin_bit_cast(unsigned, r); }
; __device__ __forceinline__ unsigned pk4_fp8(float a, float b, float c, float d) { unsigned w = 0u; w = __builtin_amdgcn_cvt_pk_fp8_f32(a, b, w, false); w = __builtin_amdgcn_cvt_pk_fp8_f32(c, d, w, true); return w; }
; template <bool COMBINE, bool ROUTE, bool FINAL, bool OUT8 = false, bool DUMMY = false> ...
;     ...
;             const float* sh = modl + (size_t)b * 12288 + sh_off; const float* sc = modl + (size_t)b * 12288 + sc_off;
; #pragma unroll
;             for (int j = 0; j < 8; ++j) {
;                 const int c = 4 * lane + 256 * j;
;                 const f32x4 gv = *(const f32x4*)(g + c), shv = *(const f32x4*)(sh + c), scv = *(const f32x4*)(sc + c);
;                 xv[j] = xv[j] * rstd * gv * (1.f + scv) + shv;
;                 if (OUT8) *(unsigned*)((unsigned char*)hout + (size_t)m * D + c) = pk4_fp8(xv[j].x * F8_SA, xv[j].y * F8_SA, xv[j].z * F8_SA, xv[j].w * F8_SA);
;                 else { u32x2 o; o.x = pk2(xv[j].x, xv[j].y); o.y = pk2(xv[j].z, xv[j].w); *(u32x2*)(hout + (size_t)m * D + c) = o; }
;             }
	v_cvt_pk_fp8_f32 v0, v22, v23
	v_pk_fma_f32 v[22:23], v[24:25], v[26:27], v[126:127]
	s_nop 0
	v_mul_f32_e32 v22, 0x41800000, v22
	v_mul_f32_e32 v23, 0x41800000, v23
	v_cvt_pk_fp8_f32 v0, v22, v23 op_sel:[0,0,1]
	global_store_dword v[30:31], v0, off offset:512
	v_mov_b32_e32 v0, 0
	v_pk_mul_f32 v[18:19], v[18:19], v[128:129]
	v_pk_mul_f32 v[20:21], v[20:21], v[130:131]
	v_pk_add_f32 v[24:25], v[132:133], 1.0 op_sel_hi:[1,0]
	v_pk_add_f32 v[22:23], v[134:135], 1.0 op_sel_hi:[1,0]
	v_pk_fma_f32 v[18:19], v[18:19], v[24:25], v[136:137]
	v_lshl_add_u64 v[26:27], v[66:67], 0, v[58:59]
	v_mul_f32_e32 v18, 0x41800000, v18
	v_mul_f32_e32 v19, 0x41800000, v19
	v_cvt_pk_fp8_f32 v0, v18, v19
	v_pk_fma_f32 v[18:19], v[20:21], v[22:23], v[138:139]
	v_lshl_add_u64 v[22:23], v[68:69], 0, v[58:59]
	v_mul_f32_e32 v18, 0x41800000, v18
	v_mul_f32_e32 v19, 0x41800000, v19
	v_cvt_pk_fp8_f32 v0, v18, v19 op_sel:[0,0,1]
	global_store_dword v[30:31], v0, off offset:768
	v_mov_b32_e32 v0, 0
	v_pk_mul_f32 v[14:15], v[14:15], v[140:141]
	v_pk_mul_f32 v[16:17], v[16:17], v[142:143]
	v_pk_add_f32 v[20:21], v[144:145], 1.0 op_sel_hi:[1,0]
	v_pk_add_f32 v[18:19], v[146:147], 1.0 op_sel_hi:[1,0]
	v_lshl_add_u64 v[22:23], v[66:67], 0, v[60:61]
	v_pk_fma_f32 v[14:15], v[14:15], v[20:21], v[148:149]
	s_nop 0
	v_mul_f32_e32 v14, 0x41800000, v14
	v_mul_f32_e32 v15, 0x41800000, v15
	v_cvt_pk_fp8_f32 v0, v14, v15
	v_pk_fma_f32 v[14:15], v[16:17], v[18:19], v[150:151]
	v_lshl_add_u64 v[18:19], v[68:69], 0, v[60:61]
	v_mul_f32_e32 v14, 0x41800000, v14
	v_mul_f32_e32 v15, 0x41800000, v15
	v_cvt_pk_fp8_f32 v0, v14, v15 op_sel:[0,0,1]
	global_store_dword v[30:31], v0, off offset:1024
	v_mov_b32_e32 v0, 0
	v_pk_mul_f32 v[10:11], v[10:11], v[152:153]
	v_pk_mul_f32 v[12:13], v[12:13], v[154:155]
	v_pk_add_f32 v[16:17], v[156:157], 1.0 op_sel_hi:[1,0]
	v_pk_add_f32 v[14:15], v[158:159], 1.0 op_sel_hi:[1,0]
	v_lshl_add_u64 v[18:19], v[66:67], 0, v[62:63]
	v_pk_fma_f32 v[10:11], v[10:11], v[16:17], v[160:161]
	s_nop 0
	v_mul_f32_e32 v10, 0x41800000, v10
	v_mul_f32_e32 v11, 0x41800000, v11
	v_cvt_pk_fp8_f32 v0, v10, v11
	v_pk_fma_f32 v[10:11], v[12:13], v[14:15], v[162:163]
	v_lshl_add_u64 v[14:15], v[68:69], 0, v[62:63]
	v_mul_f32_e32 v10, 0x41800000, v10
	v_mul_f32_e32 v11, 0x41800000, v11
	v_cvt_pk_fp8_f32 v0, v10, v11 op_sel:[0,0,1]
	global_store_dword v[30:31], v0, off offset:1280
	v_mov_b32_e32 v0, 0
	v_pk_mul_f32 v[6:7], v[6:7], v[164:165]
	v_pk_mul_f32 v[8:9], v[8:9], v[166:167]
	v_pk_add_f32 v[12:13], v[168:169], 1.0 op_sel_hi:[1,0]
	v_pk_add_f32 v[10:11], v[170:171], 1.0 op_sel_hi:[1,0]
	v_lshl_add_u64 v[14:15], v[66:67], 0, v[64:65]
	v_pk_fma_f32 v[6:7], v[6:7], v[12:13], v[172:173]
	s_nop 0
	v_mul_f32_e32 v6, 0x41800000, v6
	v_mul_f32_e32 v7, 0x41800000, v7
	v_cvt_pk_fp8_f32 v0, v6, v7
	v_pk_fma_f32 v[6:7], v[8:9], v[10:11], v[174:175]
	v_lshl_add_u64 v[10:11], v[68:69], 0, v[64:65]
	v_mul_f32_e32 v6, 0x41800000, v6
	v_mul_f32_e32 v7, 0x41800000, v7
	v_cvt_pk_fp8_f32 v0, v6, v7 op_sel:[0,0,1]
	global_store_dword v[30:31], v0, off offset:1536
	v_pk_mul_f32 v[2:3], v[2:3], v[176:177]
	v_pk_mul_f32 v[4:5], v[4:5], v[178:179]
	v_pk_add_f32 v[8:9], v[180:181], 1.0 op_sel_hi:[1,0]
	v_pk_add_f32 v[6:7], v[182:183], 1.0 op_sel_hi:[1,0]
	v_pk_fma_f32 v[2:3], v[2:3], v[8:9], v[184:185]
	v_mov_b32_e32 v8, 0
	v_mul_f32_e32 v0, 0x41800000, v2
	v_mul_f32_e32 v2, 0x41800000, v3
	v_cvt_pk_fp8_f32 v8, v0, v2
	v_pk_fma_f32 v[2:3], v[4:5], v[6:7], v[186:187]
	s_nop 0
	v_mul_f32_e32 v0, 0x41800000, v2
	v_mul_f32_e32 v2, 0x41800000, v3
	v_cvt_pk_fp8_f32 v8, v0, v2 op_sel:[0,0,1]
	global_store_dword v[30:31], v8, off offset:1792
	s_andn2_b64 exec, exec, s[8:9]
	s_cbranch_execnz .LBB0_90

; template <bool COMBINE, bool ROUTE, bool FINAL, bool OUT8 = false, bool DUMMY = false> ...
;     ...
;         float ss = 0.f;
; #pragma unroll
;         for (int j = 0; j < 8; ++j) ss += xv[j].x * xv[j].x + xv[j].y * xv[j].y + xv[j].z * xv[j].z + xv[j].w * xv[j].w;
;         ss = wave_sum(ss);
;         const float rstd = 1.0f / sqrtf(ss * (1.f / D) + EPS);
;         if (FINAL) {
; #pragma unroll
;             for (int j = 0; j < 8; ++j) { const int c = 4 * lane + 256 * j; const f32x4 gv = *(const f32x4*)(g + c); *(f32x4*)(fout + (size_t)m * D + c) = xv[j] * rstd * gv; }
;         } else {
;             const float* sh = modl + (size_t)b * 12288 + sh_off; const float* sc = modl + (size_t)b * 12288 + sc_off;
; #pragma unroll
;             for (int j = 0; j < 8; ++j) {
;                 const int c = 4 * lane + 256 * j;
;                 const f32x4 gv = *(const f32x4*)(g + c), shv = *(const f32x4*)(sh + c), scv = *(const f32x4*)(sc + c);
.LBB0_523:
	s_waitcnt vmcnt(7)
	v_mul_f32_e32 v0, v33, v33
	s_waitcnt vmcnt(6)
	v_mul_f32_e32 v1, v29, v29
	v_fmac_f32_e32 v0, v32, v32
	v_fmac_f32_e32 v1, v28, v28
	v_fmac_f32_e32 v0, v34, v34
	v_fmac_f32_e32 v1, v30, v30
	v_fmac_f32_e32 v0, v35, v35
	v_fmac_f32_e32 v1, v31, v31
	v_add_f32_e32 v0, v0, v1
	s_waitcnt vmcnt(5)
	v_mul_f32_e32 v1, v25, v25
	v_fmac_f32_e32 v1, v24, v24
	v_fmac_f32_e32 v1, v26, v26
	v_fmac_f32_e32 v1, v27, v27
	v_add_f32_e32 v0, v0, v1
	s_waitcnt vmcnt(4)
	v_mul_f32_e32 v1, v21, v21
	v_fmac_f32_e32 v1, v20, v20
	v_fmac_f32_e32 v1, v22, v22
	v_fmac_f32_e32 v1, v23, v23
	v_add_f32_e32 v0, v0, v1
	s_waitcnt vmcnt(3)
	v_mul_f32_e32 v1, v17, v17
	v_fmac_f32_e32 v1, v16, v16
	v_fmac_f32_e32 v1, v18, v18
	v_fmac_f32_e32 v1, v19, v19
	v_add_f32_e32 v0, v0, v1
	s_waitcnt vmcnt(2)
	v_mul_f32_e32 v1, v13, v13
	v_fmac_f32_e32 v1, v12, v12
	v_fmac_f32_e32 v1, v14, v14
	v_fmac_f32_e32 v1, v15, v15
	s_waitcnt vmcnt(1)
	v_mov_b32_e32 v74, v9
	s_waitcnt vmcnt(0)
	v_mov_b32_e32 v75, v5
	v_add_f32_e32 v59, v0, v1
	v_mov_b32_e32 v0, v8
	v_mov_b32_e32 v1, v4
	v_pk_mul_f32 v[74:75], v[74:75], v[74:75]
	v_lshl_add_u64 v[76:77], v[72:73], 0, s[54:55]
	v_pk_fma_f32 v[0:1], v[0:1], v[0:1], v[74:75]
	v_mov_b32_e32 v74, v10
	v_mov_b32_e32 v75, v6
	v_pk_fma_f32 v[0:1], v[74:75], v[74:75], v[0:1]
	v_mov_b32_e32 v74, v11
	v_mov_b32_e32 v75, v7
	v_pk_fma_f32 v[0:1], v[74:75], v[74:75], v[0:1]
	v_lshl_add_u64 v[74:75], v[72:73], 0, s[52:53]
	v_lshl_add_u64 v[72:73], v[74:75], 0, v[40:41]
	v_lshl_add_u64 v[164:165], v[76:77], 0, v[40:41]
	global_load_dwordx4 v[156:159], v[44:45], off
	global_load_dwordx4 v[160:163], v[72:73], off
	s_nop 0
	global_load_dwordx4 v[164:167], v[164:165], off
	global_load_dwordx4 v[168:171], v[44:45], off offset:1024
	v_mov_b32_e32 v172, v58
	v_mov_b32_e32 v173, 0
	v_lshl_add_u64 v[172:173], v[76:77], 0, v[172:173]
	global_load_dwordx4 v[172:175], v[172:173], off
	v_mov_b32_e32 v176, v58
	v_mov_b32_e32 v177, 0
	v_lshl_add_u64 v[176:177], v[74:75], 0, v[176:177]
	global_load_dwordx4 v[176:179], v[176:177], off
	global_load_dwordx4 v[180:183], v[44:45], off offset:2048
	v_mov_b32_e32 v184, v60
	v_mov_b32_e32 v185, 0
	v_lshl_add_u64 v[184:185], v[76:77], 0, v[184:185]
	global_load_dwordx4 v[184:187], v[184:185], off
	v_mov_b32_e32 v188, v60
	v_mov_b32_e32 v189, 0
	v_lshl_add_u64 v[188:189], v[74:75], 0, v[188:189]
	global_load_dwordx4 v[188:191], v[188:189], off
	global_load_dwordx4 v[192:195], v[44:45], off offset:3072
	v_mov_b32_e32 v196, v62
	v_mov_b32_e32 v197, 0
	v_lshl_add_u64 v[196:197], v[76:77], 0, v[196:197]
	global_load_dwordx4 v[196:199], v[196:197], off
	v_mov_b32_e32 v200, v62
	v_mov_b32_e32 v201, 0
	v_lshl_add_u64 v[200:201], v[74:75], 0, v[200:201]
	global_load_dwordx4 v[200:203], v[200:201], off
	global_load_dwordx4 v[204:207], v[46:47], off
	v_mov_b32_e32 v208, v64
	v_mov_b32_e32 v209, 0
	v_lshl_add_u64 v[208:209], v[76:77], 0, v[208:209]
	global_load_dwordx4 v[208:211], v[208:209], off
	v_mov_b32_e32 v212, v64
	v_mov_b32_e32 v213, 0
	v_lshl_add_u64 v[212:213], v[74:75], 0, v[212:213]
	global_load_dwordx4 v[212:215], v[212:213], off
	global_load_dwordx4 v[216:219], v[48:49], off
	v_mov_b32_e32 v220, v66
	v_mov_b32_e32 v221, 0
	v_lshl_add_u64 v[220:221], v[76:77], 0, v[220:221]
	global_load_dwordx4 v[220:223], v[220:221], off
	v_mov_b32_e32 v224, v66
	v_mov_b32_e32 v225, 0
	v_lshl_add_u64 v[224:225], v[74:75], 0, v[224:225]
	global_load_dwordx4 v[224:227], v[224:225], off
	global_load_dwordx4 v[228:231], v[50:51], off
	v_mov_b32_e32 v246, v68
	v_mov_b32_e32 v247, 0
	v_lshl_add_u64 v[246:247], v[76:77], 0, v[246:247]
	global_load_dwordx4 v[246:249], v[246:247], off
	v_mov_b32_e32 v250, v68
	v_mov_b32_e32 v251, 0
	v_lshl_add_u64 v[250:251], v[74:75], 0, v[250:251]
	global_load_dwordx4 v[250:253], v[250:251], off
	global_load_dwordx4 v[232:235], v[52:53], off
	v_mov_b32_e32 v236, v70
	v_mov_b32_e32 v237, 0
	v_lshl_add_u64 v[236:237], v[74:75], 0, v[236:237]
	global_load_dwordx4 v[236:239], v[236:237], off
	v_mov_b32_e32 v242, v70
	v_mov_b32_e32 v243, 0
	v_lshl_add_u64 v[242:243], v[76:77], 0, v[242:243]
	global_load_dwordx4 v[242:245], v[242:243], off
	v_add_f32_e32 v0, v59, v0
	v_add_f32_e32 v0, v0, v1
	ds_bpermute_b32 v1, v78, v0
	v_mov_b32_e32 v65, v41
	v_mov_b32_e32 v67, v41
	v_mov_b32_e32 v69, v41
	v_mov_b32_e32 v71, v41
	s_waitcnt lgkmcnt(0)
	v_add_f32_e32 v0, v0, v1
	ds_bpermute_b32 v1, v79, v0
	s_waitcnt lgkmcnt(0)
	v_add_f32_e32 v0, v0, v1
	ds_bpermute_b32 v1, v80, v0
	s_waitcnt lgkmcnt(0)
	v_add_f32_e32 v0, v0, v1
	ds_bpermute_b32 v1, v81, v0
	s_waitcnt lgkmcnt(0)
	v_add_f32_e32 v0, v0, v1
	ds_bpermute_b32 v1, v82, v0
	s_waitcnt lgkmcnt(0)
	v_add_f32_e32 v0, v0, v1
	ds_bpermute_b32 v1, v83, v0
	s_waitcnt lgkmcnt(0)
	v_add_f32_e32 v0, v0, v1
	v_fmamk_f32 v0, v0, 0x3a000000, v39
	v_mul_f32_e32 v1, 0x4f800000, v0
	v_cmp_gt_f32_e32 vcc, s3, v0
	s_waitcnt vmcnt(0)
; __device__ __forceinline__ unsigned pk2(float a, float b) { f32x2 v = {a, b}; bf16x2_t r = __builtin_convertvector(v, bf16x2_t); return __builtin_bit_cast(unsigned, r); }
; __device__ __forceinline__ unsigned pk4_fp8(float a, float b, float c, float d) { unsigned w = 0u; w = __builtin_amdgcn_cvt_pk_fp8_f32(a, b, w, false); w = __builtin_amdgcn_cvt_pk_fp8_f32(c, d, w, true); return w; }
; template <bool COMBINE, bool ROUTE, bool FINAL, bool OUT8 = false, bool DUMMY = false> ...
;     ...
;         const float rstd = 1.0f / sqrtf(ss * (1.f / D) + EPS);
;         if (FINAL) {
; #pragma unroll
;             for (int j = 0; j < 8; ++j) { const int c = 4 * lane + 256 * j; const f32x4 gv = *(const f32x4*)(g + c); *(f32x4*)(fout + (size_t)m * D + c) = xv[j] * rstd * gv; }
;         } else {
;             const float* sh = modl + (size_t)b * 12288 + sh_off; const float* sc = modl + (size_t)b * 12288 + sc_off;
; #pragma unroll
;             for (int j = 0; j < 8; ++j) {
;                 const int c = 4 * lane + 256 * j;
;                 const f32x4 gv = *(const f32x4*)(g + c), shv = *(const f32x4*)(sh + c), scv = *(const f32x4*)(sc + c);
;                 xv[j] = xv[j] * rstd * gv * (1.f + scv) + shv;
;                 if (OUT8) *(unsigned*)((unsigned char*)hout + (size_t)m * D + c) = pk4_fp8(xv[j].x * F8_SA, xv[j].y * F8_SA, xv[j].z * F8_SA, xv[j].w * F8_SA);
;                 else { u32x2 o; o.x = pk2(xv[j].x, xv[j].y); o.y = pk2(xv[j].z, xv[j].w); *(u32x2*)(hout + (size_t)m * D + c) = o; }
;             }
	v_pk_add_f32 v[72:73], v[164:165], 1.0 op_sel_hi:[1,0]
	v_cndmask_b32_e32 v0, v0, v1, vcc
	v_sqrt_f32_e32 v1, v0
	s_nop 0
	v_add_u32_e32 v40, -1, v1
	v_fma_f32 v59, -v40, v1, v0
	v_cmp_ge_f32_e64 s[6:7], 0, v59
	v_add_u32_e32 v59, 1, v1
	s_nop 0
	v_cndmask_b32_e64 v40, v1, v40, s[6:7]
	v_fma_f32 v1, -v59, v1, v0
	v_cmp_lt_f32_e64 s[6:7], 0, v1
	s_nop 1
	v_cndmask_b32_e64 v1, v40, v59, s[6:7]
	v_mul_f32_e32 v40, 0x37800000, v1
	v_cndmask_b32_e32 v1, v1, v40, vcc
	v_cmp_class_f32_e32 vcc, v0, v150
	s_nop 1
	v_cndmask_b32_e32 v0, v1, v0, vcc
	v_div_scale_f32 v1, s[6:7], v0, v0, 1.0
	v_rcp_f32_e32 v40, v1
	s_nop 0
	v_fma_f32 v59, -v1, v40, 1.0
	v_fmac_f32_e32 v40, v59, v40
	v_div_scale_f32 v59, vcc, 1.0, v0, 1.0
	v_mul_f32_e32 v61, v59, v40
	v_fma_f32 v63, -v1, v61, v59
	v_fmac_f32_e32 v61, v63, v40
	v_fma_f32 v1, -v1, v61, v59
	v_div_fmas_f32 v1, v1, v40, v61
	v_div_fixup_f32 v40, v1, v0, 1.0
	v_pk_mul_f32 v[32:33], v[32:33], v[40:41] op_sel_hi:[1,0]
	v_mov_b32_e32 v59, v41
	v_pk_mul_f32 v[32:33], v[156:157], v[32:33]
	v_pk_mul_f32 v[0:1], v[34:35], v[40:41] op_sel_hi:[1,0]
	v_pk_fma_f32 v[72:73], v[72:73], v[32:33], v[160:161]
	v_pk_mul_f32 v[0:1], v[158:159], v[0:1]
	v_mul_f32_e32 v32, 0x41800000, v72
	v_mul_f32_e32 v33, 0x41800000, v73
	v_cvt_pk_fp8_f32 v59, v32, v33
	v_pk_add_f32 v[34:35], v[166:167], 1.0 op_sel_hi:[1,0]
	v_pk_mul_f32 v[28:29], v[28:29], v[40:41] op_sel_hi:[1,0]
	v_pk_fma_f32 v[32:33], v[34:35], v[0:1], v[162:163]
	v_mov_b32_e32 v61, v41
	v_mul_f32_e32 v0, 0x41800000, v32
	v_mul_f32_e32 v1, 0x41800000, v33
	v_cvt_pk_fp8_f32 v59, v0, v1 op_sel:[0,0,1]
	v_lshlrev_b64 v[0:1], 11, v[2:3]
	v_lshl_add_u64 v[34:35], v[56:57], 0, v[0:1]
	v_mov_b32_e32 v3, v41
	global_store_dword v[34:35], v59, off
	v_mov_b32_e32 v59, v41
	v_lshl_add_u64 v[0:1], v[76:77], 0, v[58:59]
	v_lshl_add_u64 v[0:1], v[74:75], 0, v[58:59]
	v_pk_mul_f32 v[0:1], v[30:31], v[40:41] op_sel_hi:[1,0]
	v_pk_mul_f32 v[24:25], v[24:25], v[40:41] op_sel_hi:[1,0]
	v_mov_b32_e32 v63, v41
	v_pk_mul_f32 v[20:21], v[20:21], v[40:41] op_sel_hi:[1,0]
	v_pk_mul_f32 v[16:17], v[16:17], v[40:41] op_sel_hi:[1,0]
	v_pk_mul_f32 v[12:13], v[12:13], v[40:41] op_sel_hi:[1,0]
	v_pk_mul_f32 v[8:9], v[8:9], v[40:41] op_sel_hi:[1,0]
	v_pk_mul_f32 v[6:7], v[6:7], v[40:41] op_sel_hi:[1,0]
	v_pk_mul_f32 v[4:5], v[4:5], v[40:41] op_sel_hi:[1,0]
	v_pk_mul_f32 v[28:29], v[168:169], v[28:29]
	v_pk_add_f32 v[30:31], v[172:173], 1.0 op_sel_hi:[1,0]
	v_pk_mul_f32 v[0:1], v[170:171], v[0:1]
	v_pk_fma_f32 v[30:31], v[30:31], v[28:29], v[176:177]
	v_pk_add_f32 v[156:157], v[174:175], 1.0 op_sel_hi:[1,0]
	v_mul_f32_e32 v28, 0x41800000, v30
	v_mul_f32_e32 v29, 0x41800000, v31
	v_cvt_pk_fp8_f32 v3, v28, v29
	v_pk_fma_f32 v[28:29], v[156:157], v[0:1], v[178:179]
	s_nop 0
	v_mul_f32_e32 v0, 0x41800000, v28
	v_mul_f32_e32 v1, 0x41800000, v29
	v_cvt_pk_fp8_f32 v3, v0, v1 op_sel:[0,0,1]
	v_lshl_add_u64 v[0:1], v[76:77], 0, v[60:61]
	global_store_dword v[34:35], v3, off offset:256
	v_lshl_add_u64 v[0:1], v[74:75], 0, v[60:61]
	v_pk_mul_f32 v[0:1], v[26:27], v[40:41] op_sel_hi:[1,0]
	v_mov_b32_e32 v3, v41
	v_pk_mul_f32 v[24:25], v[180:181], v[24:25]
	v_pk_add_f32 v[26:27], v[184:185], 1.0 op_sel_hi:[1,0]
	v_pk_mul_f32 v[0:1], v[182:183], v[0:1]
	v_pk_fma_f32 v[26:27], v[24:25], v[26:27], v[188:189]
	v_pk_add_f32 v[156:157], v[186:187], 1.0 op_sel_hi:[1,0]
	v_mul_f32_e32 v24, 0x41800000, v26
	v_mul_f32_e32 v25, 0x41800000, v27
	v_cvt_pk_fp8_f32 v3, v24, v25
	v_pk_fma_f32 v[24:25], v[0:1], v[156:157], v[190:191]
	s_nop 0
	v_mul_f32_e32 v0, 0x41800000, v24
	v_mul_f32_e32 v1, 0x41800000, v25
	v_cvt_pk_fp8_f32 v3, v0, v1 op_sel:[0,0,1]
	v_lshl_add_u64 v[0:1], v[76:77], 0, v[62:63]
	global_store_dword v[34:35], v3, off offset:512
	v_lshl_add_u64 v[0:1], v[74:75], 0, v[62:63]
	v_pk_mul_f32 v[0:1], v[22:23], v[40:41] op_sel_hi:[1,0]
	v_mov_b32_e32 v3, v41
	v_pk_mul_f32 v[20:21], v[20:21], v[192:193]
	v_pk_add_f32 v[22:23], v[196:197], 1.0 op_sel_hi:[1,0]
	v_pk_mul_f32 v[0:1], v[0:1], v[194:195]
	v_pk_fma_f32 v[22:23], v[20:21], v[22:23], v[200:201]
	v_pk_add_f32 v[156:157], v[198:199], 1.0 op_sel_hi:[1,0]
	v_mul_f32_e32 v20, 0x41800000, v22
	v_mul_f32_e32 v21, 0x41800000, v23
	v_cvt_pk_fp8_f32 v3, v20, v21
	v_pk_fma_f32 v[20:21], v[0:1], v[156:157], v[202:203]
	s_nop 0
	v_mul_f32_e32 v0, 0x41800000, v20
	v_mul_f32_e32 v1, 0x41800000, v21
	v_cvt_pk_fp8_f32 v3, v0, v1 op_sel:[0,0,1]
	v_lshl_add_u64 v[0:1], v[76:77], 0, v[64:65]
	global_store_dword v[34:35], v3, off offset:768
	v_lshl_add_u64 v[0:1], v[74:75], 0, v[64:65]
	v_pk_mul_f32 v[0:1], v[18:19], v[40:41] op_sel_hi:[1,0]
	v_mov_b32_e32 v3, v41
	v_pk_mul_f32 v[16:17], v[16:17], v[204:205]
	v_pk_add_f32 v[18:19], v[208:209], 1.0 op_sel_hi:[1,0]
	v_pk_mul_f32 v[0:1], v[0:1], v[206:207]
	v_pk_fma_f32 v[18:19], v[16:17], v[18:19], v[212:213]
	v_pk_add_f32 v[156:157], v[210:211], 1.0 op_sel_hi:[1,0]
	v_mul_f32_e32 v16, 0x41800000, v18
	v_mul_f32_e32 v17, 0x41800000, v19
	v_cvt_pk_fp8_f32 v3, v16, v17
	v_pk_fma_f32 v[16:17], v[0:1], v[156:157], v[214:215]
	s_nop 0
	v_mul_f32_e32 v0, 0x41800000, v16
	v_mul_f32_e32 v1, 0x41800000, v17
	v_cvt_pk_fp8_f32 v3, v0, v1 op_sel:[0,0,1]
	v_lshl_add_u64 v[0:1], v[76:77], 0, v[66:67]
	global_store_dword v[34:35], v3, off offset:1024
	v_lshl_add_u64 v[0:1], v[74:75], 0, v[66:67]
	v_pk_mul_f32 v[0:1], v[14:15], v[40:41] op_sel_hi:[1,0]
	v_mov_b32_e32 v3, v41
	v_pk_mul_f32 v[12:13], v[12:13], v[216:217]
	v_pk_add_f32 v[14:15], v[220:221], 1.0 op_sel_hi:[1,0]
	v_pk_mul_f32 v[0:1], v[0:1], v[218:219]
	v_pk_fma_f32 v[14:15], v[12:13], v[14:15], v[224:225]
	v_pk_add_f32 v[156:157], v[222:223], 1.0 op_sel_hi:[1,0]
	v_mul_f32_e32 v12, 0x41800000, v14
; __device__ __forceinline__ unsigned pk2(float a, float b) { f32x2 v = {a, b}; bf16x2_t r = __builtin_convertvector(v, bf16x2_t); return __builtin_bit_cast(unsigned, r); }
; __device__ __forceinline__ unsigned pk4_fp8(float a, float b, float c, float d) { unsigned w = 0u; w = __builtin_amdgcn_cvt_pk_fp8_f32(a, b, w, false); w = __builtin_amdgcn_cvt_pk_fp8_f32(c, d, w, true); return w; }
; template <bool COMBINE, bool ROUTE, bool FINAL, bool OUT8 = false, bool DUMMY = false> ...
;     ...
;                 xv[j] = xv[j] * rstd * gv * (1.f + scv) + shv;
;                 if (OUT8) *(unsigned*)((unsigned char*)hout + (size_t)m * D + c) = pk4_fp8(xv[j].x * F8_SA, xv[j].y * F8_SA, xv[j].z * F8_SA, xv[j].w * F8_SA);
;                 else { u32x2 o; o.x = pk2(xv[j].x, xv[j].y); o.y = pk2(xv[j].z, xv[j].w); *(u32x2*)(hout + (size_t)m * D + c) = o; }
;             }
;             if (ROUTE) {
;                 float lg[16];
; #pragma unroll
;                 for (int e = 0; e < 16; ++e) lg[e] = 0.f;
; #pragma unroll
;                 for (int j = 0; j < 8; ++j) {
; #pragma unroll
;                     for (int cc = 0; cc < 4; ++cc) {
;                         const float hv = xv[j][cc];
;                         const f32x4 w0 = WT[((j * 4 + cc) * 4 + 0) * 64 + lane], w1 = WT[((j * 4 + cc) * 4 + 1) * 64 + lane], w2 = WT[((j * 4 + cc) * 4 + 2) * 64 + lane], w3 = WT[((j * 4 + cc) * 4 + 3) * 64 + lane];
;                         lg[0] += hv * w0.x; lg[1] += hv * w0.y; lg[2] += hv * w0.z; lg[3] += hv * w0.w;
;                         lg[4] += hv * w1.x; lg[5] += hv * w1.y; lg[6] += hv * w1.z; lg[7] += hv * w1.w;
;                         lg[8] += hv * w2.x; lg[9] += hv * w2.y; lg[10] += hv * w2.z; lg[11] += hv * w2.w;
;                         lg[12] += hv * w3.x; lg[13] += hv * w3.y; lg[14] += hv * w3.z; lg[15] += hv * w3.w;
;                     }
	v_mul_f32_e32 v13, 0x41800000, v15
	v_cvt_pk_fp8_f32 v3, v12, v13
	v_pk_fma_f32 v[12:13], v[0:1], v[156:157], v[226:227]
	s_nop 0
	v_mul_f32_e32 v0, 0x41800000, v12
	v_mul_f32_e32 v1, 0x41800000, v13
	v_cvt_pk_fp8_f32 v3, v0, v1 op_sel:[0,0,1]
	v_lshl_add_u64 v[0:1], v[76:77], 0, v[68:69]
	global_store_dword v[34:35], v3, off offset:1280
	v_lshl_add_u64 v[0:1], v[74:75], 0, v[68:69]
	v_pk_mul_f32 v[0:1], v[10:11], v[40:41] op_sel_hi:[1,0]
	v_mov_b32_e32 v3, v41
	v_pk_mul_f32 v[8:9], v[8:9], v[228:229]
	v_pk_add_f32 v[10:11], v[246:247], 1.0 op_sel_hi:[1,0]
	v_pk_mul_f32 v[0:1], v[0:1], v[230:231]
	v_pk_fma_f32 v[10:11], v[8:9], v[10:11], v[250:251]
	v_pk_add_f32 v[156:157], v[248:249], 1.0 op_sel_hi:[1,0]
	v_mul_f32_e32 v8, 0x41800000, v10
	v_mul_f32_e32 v9, 0x41800000, v11
	v_cvt_pk_fp8_f32 v3, v8, v9
	v_pk_fma_f32 v[8:9], v[0:1], v[156:157], v[252:253]
	v_mov_b32_e32 v157, v41
	v_mul_f32_e32 v0, 0x41800000, v8
	v_mul_f32_e32 v1, 0x41800000, v9
	v_cvt_pk_fp8_f32 v3, v0, v1 op_sel:[0,0,1]
	v_lshl_add_u64 v[0:1], v[74:75], 0, v[70:71]
	v_lshl_add_u64 v[74:75], v[76:77], 0, v[70:71]
	global_store_dword v[34:35], v3, off offset:1536
	ds_read_b128 v[74:77], v84
	ds_read_b128 v[170:173], v84 offset:1024
	ds_read_b128 v[174:177], v84 offset:2048
	ds_read_b128 v[178:181], v84 offset:3072
	ds_read_b128 v[182:185], v84 offset:4096
	ds_read_b128 v[186:189], v84 offset:5120
	ds_read_b128 v[190:193], v84 offset:6144
	ds_read_b128 v[194:197], v84 offset:7168
	ds_read_b128 v[198:201], v84 offset:8192
	ds_read_b128 v[202:205], v84 offset:9216
	ds_read_b128 v[206:209], v84 offset:10240
	ds_read_b128 v[210:213], v84 offset:11264
	ds_read_b128 v[214:217], v84 offset:12288
	ds_read_b128 v[218:221], v84 offset:13312
	ds_read_b128 v[224:227], v84 offset:14336
	ds_read_b128 v[228:231], v84 offset:15360
	s_waitcnt lgkmcnt(14)
	v_fma_f32 v156, v72, v74, 0
	v_fma_f32 v155, v72, v75, 0
	v_fma_f32 v67, v72, v76, 0
	v_fma_f32 v65, v72, v77, 0
	v_fma_f32 v77, v72, v170, 0
	v_fma_f32 v76, v72, v171, 0
	v_fma_f32 v63, v72, v172, 0
	v_fma_f32 v61, v72, v173, 0
	s_waitcnt lgkmcnt(13)
	v_fma_f32 v75, v72, v174, 0
	v_fma_f32 v74, v72, v175, 0
	v_fma_f32 v59, v72, v176, 0
	v_fma_f32 v40, v72, v177, 0
	s_waitcnt lgkmcnt(12)
	v_fma_f32 v71, v72, v178, 0
	v_fma_f32 v69, v72, v179, 0
	v_fma_f32 v3, v72, v180, 0
	v_fma_f32 v1, v72, v181, 0
	s_waitcnt lgkmcnt(11)
	v_fmac_f32_e32 v156, v73, v182
	v_fmac_f32_e32 v155, v73, v183
	v_fmac_f32_e32 v67, v73, v184
	v_fmac_f32_e32 v65, v73, v185
	s_waitcnt lgkmcnt(10)
	v_fmac_f32_e32 v77, v73, v186
	v_fmac_f32_e32 v76, v73, v187
	v_fmac_f32_e32 v63, v73, v188
	v_fmac_f32_e32 v61, v73, v189
	s_waitcnt lgkmcnt(9)
	v_fmac_f32_e32 v75, v73, v190
	v_fmac_f32_e32 v74, v73, v191
	v_fmac_f32_e32 v59, v73, v192
	v_fmac_f32_e32 v40, v73, v193
	s_waitcnt lgkmcnt(8)
	v_fmac_f32_e32 v71, v73, v194
	v_fmac_f32_e32 v69, v73, v195
	v_fmac_f32_e32 v3, v73, v196
	v_fmac_f32_e32 v1, v73, v197
	s_waitcnt lgkmcnt(7)
	v_fmac_f32_e32 v156, v32, v198
	v_fmac_f32_e32 v155, v32, v199
	v_fmac_f32_e32 v67, v32, v200
	v_fmac_f32_e32 v65, v32, v201
	s_waitcnt lgkmcnt(6)
	v_fmac_f32_e32 v77, v32, v202
	v_fmac_f32_e32 v76, v32, v203
	v_fmac_f32_e32 v63, v32, v204
	v_fmac_f32_e32 v61, v32, v205
	s_waitcnt lgkmcnt(5)
	v_fmac_f32_e32 v75, v32, v206
	v_fmac_f32_e32 v74, v32, v207
	v_fmac_f32_e32 v59, v32, v208
	v_fmac_f32_e32 v40, v32, v209
	s_waitcnt lgkmcnt(4)
	v_fmac_f32_e32 v71, v32, v210
	v_fmac_f32_e32 v69, v32, v211
	v_fmac_f32_e32 v3, v32, v212
	v_fmac_f32_e32 v1, v32, v213
	s_waitcnt lgkmcnt(1)
	v_fmac_f32_e32 v59, v33, v226
	v_fmac_f32_e32 v40, v33, v227
	s_waitcnt lgkmcnt(0)
	v_fmac_f32_e32 v3, v33, v230
	v_fmac_f32_e32 v1, v33, v231
	v_fmac_f32_e32 v156, v33, v214
	v_fmac_f32_e32 v155, v33, v215
	v_fmac_f32_e32 v67, v33, v216
	v_fmac_f32_e32 v65, v33, v217
	v_fmac_f32_e32 v77, v33, v218
	v_fmac_f32_e32 v76, v33, v219
	v_fmac_f32_e32 v63, v33, v220
	v_fmac_f32_e32 v61, v33, v221
	v_fmac_f32_e32 v75, v33, v224
	v_fmac_f32_e32 v74, v33, v225
	v_fmac_f32_e32 v71, v33, v228
	v_fmac_f32_e32 v69, v33, v229
	v_pk_mul_f32 v[4:5], v[4:5], v[232:233]
	v_pk_mul_f32 v[72:73], v[6:7], v[234:235]
	v_pk_add_f32 v[6:7], v[242:243], 1.0 op_sel_hi:[1,0]
	v_pk_add_f32 v[158:159], v[244:245], 1.0 op_sel_hi:[1,0]
	v_pk_fma_f32 v[6:7], v[4:5], v[6:7], v[236:237]
	s_nop 0
	v_mul_f32_e32 v0, 0x41800000, v6
	v_mul_f32_e32 v4, 0x41800000, v7
	v_cvt_pk_fp8_f32 v157, v0, v4
	v_pk_fma_f32 v[4:5], v[72:73], v[158:159], v[238:239]
	s_nop 0
	v_mul_f32_e32 v0, 0x41800000, v4
	v_mul_f32_e32 v32, 0x41800000, v5
	v_cvt_pk_fp8_f32 v157, v0, v32 op_sel:[0,0,1]
	global_store_dword v[34:35], v157, off offset:1792
	ds_read_b128 v[32:35], v84 offset:16384
	ds_read_b128 v[158:161], v84 offset:17408
	ds_read_b128 v[162:165], v84 offset:18432
	ds_read_b128 v[166:169], v84 offset:19456
	s_waitcnt lgkmcnt(3)
	v_fmac_f32_e32 v156, v30, v32
	v_fmac_f32_e32 v155, v30, v33
	v_fmac_f32_e32 v67, v30, v34
	v_fmac_f32_e32 v65, v30, v35
	s_waitcnt lgkmcnt(2)
	v_fmac_f32_e32 v77, v30, v158
	v_fmac_f32_e32 v76, v30, v159
	v_fmac_f32_e32 v63, v30, v160
	v_fmac_f32_e32 v61, v30, v161
	s_waitcnt lgkmcnt(1)
	v_fmac_f32_e32 v75, v30, v162
	v_fmac_f32_e32 v74, v30, v163
	v_fmac_f32_e32 v59, v30, v164
	v_fmac_f32_e32 v40, v30, v165
	s_waitcnt lgkmcnt(0)
	v_fmac_f32_e32 v71, v30, v166
	v_fmac_f32_e32 v69, v30, v167
	v_fmac_f32_e32 v3, v30, v168
	ds_read_b128 v[32:35], v84 offset:20480
	v_fmac_f32_e32 v1, v30, v169
	ds_read_b128 v[158:161], v84 offset:21504
	ds_read_b128 v[162:165], v84 offset:22528
	ds_read_b128 v[166:169], v84 offset:23552
	s_waitcnt lgkmcnt(3)
; template <bool COMBINE, bool ROUTE, bool FINAL, bool OUT8 = false, bool DUMMY = false> ...
;     ...
; #pragma unroll
;                 for (int j = 0; j < 8; ++j) {
; #pragma unroll
;                     for (int cc = 0; cc < 4; ++cc) {
;                         const float hv = xv[j][cc];
;                         const f32x4 w0 = WT[((j * 4 + cc) * 4 + 0) * 64 + lane], w1 = WT[((j * 4 + cc) * 4 + 1) * 64 + lane], w2 = WT[((j * 4 + cc) * 4 + 2) * 64 + lane], w3 = WT[((j * 4 + cc) * 4 + 3) * 64 + lane];
;                         lg[0] += hv * w0.x; lg[1] += hv * w0.y; lg[2] += hv * w0.z; lg[3] += hv * w0.w;
;                         lg[4] += hv * w1.x; lg[5] += hv * w1.y; lg[6] += hv * w1.z; lg[7] += hv * w1.w;
;                         lg[8] += hv * w2.x; lg[9] += hv * w2.y; lg[10] += hv * w2.z; lg[11] += hv * w2.w;
;                         lg[12] += hv * w3.x; lg[13] += hv * w3.y; lg[14] += hv * w3.z; lg[15] += hv * w3.w;
;                     }
	v_fmac_f32_e32 v156, v31, v32
	v_fmac_f32_e32 v155, v31, v33
	v_fmac_f32_e32 v67, v31, v34
	v_fmac_f32_e32 v65, v31, v35
	s_waitcnt lgkmcnt(2)
	v_fmac_f32_e32 v77, v31, v158
	v_fmac_f32_e32 v76, v31, v159
	v_fmac_f32_e32 v63, v31, v160
	v_fmac_f32_e32 v61, v31, v161
	s_waitcnt lgkmcnt(1)
	v_fmac_f32_e32 v75, v31, v162
	v_fmac_f32_e32 v74, v31, v163
	v_fmac_f32_e32 v59, v31, v164
	v_fmac_f32_e32 v40, v31, v165
	s_waitcnt lgkmcnt(0)
	v_fmac_f32_e32 v71, v31, v166
	v_fmac_f32_e32 v69, v31, v167
	v_fmac_f32_e32 v3, v31, v168
	ds_read_b128 v[32:35], v84 offset:24576
	v_fmac_f32_e32 v1, v31, v169
	ds_read_b128 v[158:161], v84 offset:25600
	ds_read_b128 v[162:165], v84 offset:26624
	ds_read_b128 v[166:169], v84 offset:27648
	s_waitcnt lgkmcnt(3)
	v_fmac_f32_e32 v156, v28, v32
	v_fmac_f32_e32 v155, v28, v33
	s_waitcnt lgkmcnt(2)
	v_fmac_f32_e32 v77, v28, v158
	v_fmac_f32_e32 v76, v28, v159
	v_fmac_f32_e32 v63, v28, v160
	v_fmac_f32_e32 v61, v28, v161
	s_waitcnt lgkmcnt(1)
	v_fmac_f32_e32 v75, v28, v162
	v_fmac_f32_e32 v74, v28, v163
	v_fmac_f32_e32 v59, v28, v164
	v_fmac_f32_e32 v40, v28, v165
	s_waitcnt lgkmcnt(0)
	v_fmac_f32_e32 v71, v28, v166
	v_fmac_f32_e32 v69, v28, v167
	v_fmac_f32_e32 v3, v28, v168
	ds_read_b128 v[30:33], v84 offset:28672
	v_fmac_f32_e32 v1, v28, v169
	ds_read_b128 v[158:161], v84 offset:29696
	ds_read_b128 v[162:165], v84 offset:30720
	ds_read_b128 v[166:169], v84 offset:31744
	v_fmac_f32_e32 v67, v28, v34
	v_fmac_f32_e32 v65, v28, v35
	s_waitcnt lgkmcnt(3)
	v_fmac_f32_e32 v156, v29, v30
	s_waitcnt lgkmcnt(1)
	v_fmac_f32_e32 v59, v29, v164
	v_fmac_f32_e32 v40, v29, v165
	s_waitcnt lgkmcnt(0)
	v_fmac_f32_e32 v3, v29, v168
	v_fmac_f32_e32 v1, v29, v169
	v_fmac_f32_e32 v155, v29, v31
	v_fmac_f32_e32 v67, v29, v32
	v_fmac_f32_e32 v65, v29, v33
	v_fmac_f32_e32 v77, v29, v158
	v_fmac_f32_e32 v76, v29, v159
	v_fmac_f32_e32 v63, v29, v160
	v_fmac_f32_e32 v61, v29, v161
	v_fmac_f32_e32 v75, v29, v162
	v_fmac_f32_e32 v74, v29, v163
	v_fmac_f32_e32 v71, v29, v166
	v_fmac_f32_e32 v69, v29, v167
	ds_read_b128 v[28:31], v84 offset:32768
	ds_read_b128 v[32:35], v84 offset:33792
	ds_read_b128 v[158:161], v84 offset:34816
	ds_read_b128 v[162:165], v84 offset:35840
	s_waitcnt lgkmcnt(3)
	v_fmac_f32_e32 v156, v26, v28
	v_fmac_f32_e32 v155, v26, v29
	v_fmac_f32_e32 v67, v26, v30
	v_fmac_f32_e32 v65, v26, v31
	s_waitcnt lgkmcnt(2)
	v_fmac_f32_e32 v77, v26, v32
	v_fmac_f32_e32 v76, v26, v33
	v_fmac_f32_e32 v63, v26, v34
	v_fmac_f32_e32 v61, v26, v35
	s_waitcnt lgkmcnt(1)
	v_fmac_f32_e32 v75, v26, v158
	v_fmac_f32_e32 v74, v26, v159
	v_fmac_f32_e32 v59, v26, v160
	v_fmac_f32_e32 v40, v26, v161
	s_waitcnt lgkmcnt(0)
	v_fmac_f32_e32 v71, v26, v162
	v_fmac_f32_e32 v69, v26, v163
	v_fmac_f32_e32 v3, v26, v164
	ds_read_b128 v[28:31], v84 offset:36864
	v_fmac_f32_e32 v1, v26, v165
	ds_read_b128 v[32:35], v84 offset:37888
	ds_read_b128 v[158:161], v84 offset:38912
	ds_read_b128 v[162:165], v84 offset:39936
	s_waitcnt lgkmcnt(3)
	v_fmac_f32_e32 v156, v27, v28
	v_fmac_f32_e32 v155, v27, v29
	v_fmac_f32_e32 v67, v27, v30
	v_fmac_f32_e32 v65, v27, v31
	s_waitcnt lgkmcnt(2)
	v_fmac_f32_e32 v77, v27, v32
	v_fmac_f32_e32 v76, v27, v33
	v_fmac_f32_e32 v63, v27, v34
	v_fmac_f32_e32 v61, v27, v35
	s_waitcnt lgkmcnt(1)
	v_fmac_f32_e32 v75, v27, v158
	v_fmac_f32_e32 v74, v27, v159
	v_fmac_f32_e32 v59, v27, v160
	v_fmac_f32_e32 v40, v27, v161
	s_waitcnt lgkmcnt(0)
	v_fmac_f32_e32 v71, v27, v162
	v_fmac_f32_e32 v69, v27, v163
	v_fmac_f32_e32 v3, v27, v164
	ds_read_b128 v[28:31], v84 offset:40960
	v_fmac_f32_e32 v1, v27, v165
	ds_read_b128 v[32:35], v84 offset:41984
	ds_read_b128 v[158:161], v84 offset:43008
	ds_read_b128 v[162:165], v84 offset:44032
	s_waitcnt lgkmcnt(3)
	v_fmac_f32_e32 v156, v24, v28
	v_fmac_f32_e32 v155, v24, v29
	v_fmac_f32_e32 v67, v24, v30
	v_fmac_f32_e32 v65, v24, v31
	s_waitcnt lgkmcnt(2)
	v_fmac_f32_e32 v77, v24, v32
	v_fmac_f32_e32 v76, v24, v33
	s_waitcnt lgkmcnt(1)
	v_fmac_f32_e32 v75, v24, v158
	v_fmac_f32_e32 v74, v24, v159
	v_fmac_f32_e32 v59, v24, v160
	v_fmac_f32_e32 v40, v24, v161
	s_waitcnt lgkmcnt(0)
	v_fmac_f32_e32 v71, v24, v162
	v_fmac_f32_e32 v69, v24, v163
	v_fmac_f32_e32 v3, v24, v164
	ds_read_b128 v[26:29], v84 offset:45056
	v_fmac_f32_e32 v1, v24, v165
	ds_read_b128 v[30:33], v84 offset:46080
	ds_read_b128 v[158:161], v84 offset:47104
	ds_read_b128 v[162:165], v84 offset:48128
	v_fmac_f32_e32 v63, v24, v34
	v_fmac_f32_e32 v61, v24, v35
	s_waitcnt lgkmcnt(3)
	v_fmac_f32_e32 v156, v25, v26
	s_waitcnt lgkmcnt(1)
	v_fmac_f32_e32 v59, v25, v160
	v_fmac_f32_e32 v40, v25, v161
	s_waitcnt lgkmcnt(0)
	v_fmac_f32_e32 v3, v25, v164
	v_fmac_f32_e32 v1, v25, v165
	v_fmac_f32_e32 v155, v25, v27
	v_fmac_f32_e32 v67, v25, v28
	v_fmac_f32_e32 v65, v25, v29
	v_fmac_f32_e32 v77, v25, v30
	v_fmac_f32_e32 v76, v25, v31
	v_fmac_f32_e32 v63, v25, v32
	v_fmac_f32_e32 v61, v25, v33
	v_fmac_f32_e32 v75, v25, v158
	v_fmac_f32_e32 v74, v25, v159
	v_fmac_f32_e32 v71, v25, v162
	v_fmac_f32_e32 v69, v25, v163
	ds_read_b128 v[24:27], v84 offset:49152
	ds_read_b128 v[28:31], v84 offset:50176
	ds_read_b128 v[32:35], v84 offset:51200
	ds_read_b128 v[158:161], v84 offset:52224
	s_waitcnt lgkmcnt(3)
	v_fmac_f32_e32 v156, v22, v24
	v_fmac_f32_e32 v155, v22, v25
	v_fmac_f32_e32 v67, v22, v26
	v_fmac_f32_e32 v65, v22, v27
	s_waitcnt lgkmcnt(2)
	v_fmac_f32_e32 v77, v22, v28
	v_fmac_f32_e32 v76, v22, v29
	v_fmac_f32_e32 v63, v22, v30
	v_fmac_f32_e32 v61, v22, v31
	s_waitcnt lgkmcnt(1)
	v_fmac_f32_e32 v75, v22, v32
	v_fmac_f32_e32 v74, v22, v33
	v_fmac_f32_e32 v59, v22, v34
	v_fmac_f32_e32 v40, v22, v35
	s_waitcnt lgkmcnt(0)
; template <bool COMBINE, bool ROUTE, bool FINAL, bool OUT8 = false, bool DUMMY = false> ...
;     ...
; #pragma unroll
;                 for (int j = 0; j < 8; ++j) {
; #pragma unroll
;                     for (int cc = 0; cc < 4; ++cc) {
;                         const float hv = xv[j][cc];
;                         const f32x4 w0 = WT[((j * 4 + cc) * 4 + 0) * 64 + lane], w1 = WT[((j * 4 + cc) * 4 + 1) * 64 + lane], w2 = WT[((j * 4 + cc) * 4 + 2) * 64 + lane], w3 = WT[((j * 4 + cc) * 4 + 3) * 64 + lane];
;                         lg[0] += hv * w0.x; lg[1] += hv * w0.y; lg[2] += hv * w0.z; lg[3] += hv * w0.w;
;                         lg[4] += hv * w1.x; lg[5] += hv * w1.y; lg[6] += hv * w1.z; lg[7] += hv * w1.w;
;                         lg[8] += hv * w2.x; lg[9] += hv * w2.y; lg[10] += hv * w2.z; lg[11] += hv * w2.w;
;                         lg[12] += hv * w3.x; lg[13] += hv * w3.y; lg[14] += hv * w3.z; lg[15] += hv * w3.w;
;                     }
	v_fmac_f32_e32 v71, v22, v158
	v_fmac_f32_e32 v69, v22, v159
	v_fmac_f32_e32 v3, v22, v160
	ds_read_b128 v[24:27], v84 offset:53248
	v_fmac_f32_e32 v1, v22, v161
	ds_read_b128 v[28:31], v84 offset:54272
	ds_read_b128 v[32:35], v84 offset:55296
	ds_read_b128 v[158:161], v84 offset:56320
	s_waitcnt lgkmcnt(3)
	v_fmac_f32_e32 v156, v23, v24
	v_fmac_f32_e32 v155, v23, v25
	v_fmac_f32_e32 v67, v23, v26
	v_fmac_f32_e32 v65, v23, v27
	s_waitcnt lgkmcnt(2)
	v_fmac_f32_e32 v77, v23, v28
	v_fmac_f32_e32 v76, v23, v29
	v_fmac_f32_e32 v63, v23, v30
	v_fmac_f32_e32 v61, v23, v31
	s_waitcnt lgkmcnt(1)
	v_fmac_f32_e32 v75, v23, v32
	v_fmac_f32_e32 v74, v23, v33
	v_fmac_f32_e32 v59, v23, v34
	v_fmac_f32_e32 v40, v23, v35
	s_waitcnt lgkmcnt(0)
	v_fmac_f32_e32 v71, v23, v158
	v_fmac_f32_e32 v69, v23, v159
	v_fmac_f32_e32 v3, v23, v160
	ds_read_b128 v[24:27], v84 offset:57344
	v_fmac_f32_e32 v1, v23, v161
	ds_read_b128 v[28:31], v84 offset:58368
	ds_read_b128 v[32:35], v84 offset:59392
	ds_read_b128 v[158:161], v84 offset:60416
	s_waitcnt lgkmcnt(3)
	v_fmac_f32_e32 v156, v20, v24
	v_fmac_f32_e32 v155, v20, v25
	v_fmac_f32_e32 v67, v20, v26
	v_fmac_f32_e32 v65, v20, v27
	s_waitcnt lgkmcnt(2)
	v_fmac_f32_e32 v77, v20, v28
	v_fmac_f32_e32 v76, v20, v29
	v_fmac_f32_e32 v63, v20, v30
	v_fmac_f32_e32 v61, v20, v31
	s_waitcnt lgkmcnt(1)
	v_fmac_f32_e32 v75, v20, v32
	v_fmac_f32_e32 v74, v20, v33
	s_waitcnt lgkmcnt(0)
	v_fmac_f32_e32 v71, v20, v158
	v_fmac_f32_e32 v69, v20, v159
	v_fmac_f32_e32 v3, v20, v160
	ds_read_b128 v[22:25], v84 offset:61440
	v_fmac_f32_e32 v1, v20, v161
	ds_read_b128 v[26:29], v84 offset:62464
	ds_read_b128 v[30:33], v84 offset:63488
	ds_read_b128 v[158:161], v84 offset:64512
	v_fmac_f32_e32 v59, v20, v34
	v_fmac_f32_e32 v40, v20, v35
	s_waitcnt lgkmcnt(3)
	v_fmac_f32_e32 v156, v21, v22
	s_waitcnt lgkmcnt(1)
	v_fmac_f32_e32 v59, v21, v32
	v_fmac_f32_e32 v40, v21, v33
	s_waitcnt lgkmcnt(0)
	v_fmac_f32_e32 v3, v21, v160
	v_fmac_f32_e32 v1, v21, v161
	v_fmac_f32_e32 v155, v21, v23
	v_fmac_f32_e32 v67, v21, v24
	v_fmac_f32_e32 v65, v21, v25
	v_fmac_f32_e32 v77, v21, v26
	v_fmac_f32_e32 v76, v21, v27
	v_fmac_f32_e32 v63, v21, v28
	v_fmac_f32_e32 v61, v21, v29
	v_fmac_f32_e32 v75, v21, v30
	v_fmac_f32_e32 v74, v21, v31
	v_fmac_f32_e32 v71, v21, v158
	v_fmac_f32_e32 v69, v21, v159
	ds_read_b128 v[20:23], v86
	ds_read_b128 v[24:27], v87
	ds_read_b128 v[28:31], v88
	ds_read_b128 v[32:35], v89
	s_waitcnt lgkmcnt(3)
	v_fmac_f32_e32 v156, v18, v20
	v_fmac_f32_e32 v155, v18, v21
	v_fmac_f32_e32 v67, v18, v22
	v_fmac_f32_e32 v65, v18, v23
	s_waitcnt lgkmcnt(2)
	v_fmac_f32_e32 v77, v18, v24
	v_fmac_f32_e32 v76, v18, v25
	v_fmac_f32_e32 v63, v18, v26
	v_fmac_f32_e32 v61, v18, v27
	s_waitcnt lgkmcnt(1)
	v_fmac_f32_e32 v75, v18, v28
	v_fmac_f32_e32 v74, v18, v29
	v_fmac_f32_e32 v59, v18, v30
	v_fmac_f32_e32 v40, v18, v31
	s_waitcnt lgkmcnt(0)
	v_fmac_f32_e32 v71, v18, v32
	v_fmac_f32_e32 v69, v18, v33
	v_fmac_f32_e32 v3, v18, v34
	ds_read_b128 v[20:23], v90
	v_fmac_f32_e32 v1, v18, v35
	ds_read_b128 v[24:27], v91
	ds_read_b128 v[28:31], v92
	ds_read_b128 v[32:35], v93
	s_waitcnt lgkmcnt(3)
	v_fmac_f32_e32 v156, v19, v20
	v_fmac_f32_e32 v155, v19, v21
	v_fmac_f32_e32 v67, v19, v22
	v_fmac_f32_e32 v65, v19, v23
	s_waitcnt lgkmcnt(2)
	v_fmac_f32_e32 v77, v19, v24
	v_fmac_f32_e32 v76, v19, v25
	v_fmac_f32_e32 v63, v19, v26
	v_fmac_f32_e32 v61, v19, v27
	s_waitcnt lgkmcnt(1)
	v_fmac_f32_e32 v75, v19, v28
	v_fmac_f32_e32 v74, v19, v29
	v_fmac_f32_e32 v59, v19, v30
	v_fmac_f32_e32 v40, v19, v31
	s_waitcnt lgkmcnt(0)
	v_fmac_f32_e32 v71, v19, v32
	v_fmac_f32_e32 v69, v19, v33
	v_fmac_f32_e32 v3, v19, v34
	ds_read_b128 v[20:23], v94
	v_fmac_f32_e32 v1, v19, v35
	ds_read_b128 v[24:27], v95
	ds_read_b128 v[28:31], v96
	ds_read_b128 v[32:35], v97
	s_waitcnt lgkmcnt(3)
	v_fmac_f32_e32 v156, v16, v20
	v_fmac_f32_e32 v155, v16, v21
	v_fmac_f32_e32 v67, v16, v22
	v_fmac_f32_e32 v65, v16, v23
	s_waitcnt lgkmcnt(2)
	v_fmac_f32_e32 v77, v16, v24
	v_fmac_f32_e32 v76, v16, v25
	v_fmac_f32_e32 v63, v16, v26
	v_fmac_f32_e32 v61, v16, v27
	s_waitcnt lgkmcnt(1)
	v_fmac_f32_e32 v75, v16, v28
	v_fmac_f32_e32 v74, v16, v29
	v_fmac_f32_e32 v59, v16, v30
	v_fmac_f32_e32 v40, v16, v31
	s_waitcnt lgkmcnt(0)
	v_fmac_f32_e32 v71, v16, v32
	v_fmac_f32_e32 v69, v16, v33
	ds_read_b128 v[18:21], v98
	ds_read_b128 v[22:25], v99
	ds_read_b128 v[26:29], v100
	ds_read_b128 v[30:33], v101
	v_fmac_f32_e32 v3, v16, v34
	v_fmac_f32_e32 v1, v16, v35
	s_waitcnt lgkmcnt(2)
	v_fmac_f32_e32 v77, v17, v22
	s_waitcnt lgkmcnt(1)
	v_fmac_f32_e32 v59, v17, v28
	v_fmac_f32_e32 v40, v17, v29
	s_waitcnt lgkmcnt(0)
	v_fmac_f32_e32 v3, v17, v32
	v_fmac_f32_e32 v1, v17, v33
	v_fmac_f32_e32 v156, v17, v18
	v_fmac_f32_e32 v155, v17, v19
	v_fmac_f32_e32 v67, v17, v20
	v_fmac_f32_e32 v65, v17, v21
	v_fmac_f32_e32 v76, v17, v23
	v_fmac_f32_e32 v63, v17, v24
	v_fmac_f32_e32 v61, v17, v25
	v_fmac_f32_e32 v75, v17, v26
	v_fmac_f32_e32 v74, v17, v27
	v_fmac_f32_e32 v71, v17, v30
	v_fmac_f32_e32 v69, v17, v31
	ds_read_b128 v[16:19], v102
	ds_read_b128 v[20:23], v103
	ds_read_b128 v[24:27], v104
	ds_read_b128 v[28:31], v105
	s_waitcnt lgkmcnt(3)
	v_fmac_f32_e32 v156, v14, v16
	v_fmac_f32_e32 v155, v14, v17
	v_fmac_f32_e32 v67, v14, v18
	v_fmac_f32_e32 v65, v14, v19
	s_waitcnt lgkmcnt(2)
	v_fmac_f32_e32 v77, v14, v20
	v_fmac_f32_e32 v76, v14, v21
	v_fmac_f32_e32 v63, v14, v22
	v_fmac_f32_e32 v61, v14, v23
	s_waitcnt lgkmcnt(1)
	v_fmac_f32_e32 v75, v14, v24
	v_fmac_f32_e32 v74, v14, v25
	v_fmac_f32_e32 v59, v14, v26
	v_fmac_f32_e32 v40, v14, v27
	s_waitcnt lgkmcnt(0)
; template <bool COMBINE, bool ROUTE, bool FINAL, bool OUT8 = false, bool DUMMY = false> ...
;     ...
; #pragma unroll
;                 for (int j = 0; j < 8; ++j) {
; #pragma unroll
;                     for (int cc = 0; cc < 4; ++cc) {
;                         const float hv = xv[j][cc];
;                         const f32x4 w0 = WT[((j * 4 + cc) * 4 + 0) * 64 + lane], w1 = WT[((j * 4 + cc) * 4 + 1) * 64 + lane], w2 = WT[((j * 4 + cc) * 4 + 2) * 64 + lane], w3 = WT[((j * 4 + cc) * 4 + 3) * 64 + lane];
;                         lg[0] += hv * w0.x; lg[1] += hv * w0.y; lg[2] += hv * w0.z; lg[3] += hv * w0.w;
;                         lg[4] += hv * w1.x; lg[5] += hv * w1.y; lg[6] += hv * w1.z; lg[7] += hv * w1.w;
;                         lg[8] += hv * w2.x; lg[9] += hv * w2.y; lg[10] += hv * w2.z; lg[11] += hv * w2.w;
;                         lg[12] += hv * w3.x; lg[13] += hv * w3.y; lg[14] += hv * w3.z; lg[15] += hv * w3.w;
;                     }
	v_fmac_f32_e32 v71, v14, v28
	v_fmac_f32_e32 v69, v14, v29
	v_fmac_f32_e32 v3, v14, v30
	ds_read_b128 v[16:19], v106
	v_fmac_f32_e32 v1, v14, v31
	ds_read_b128 v[20:23], v107
	ds_read_b128 v[24:27], v108
	ds_read_b128 v[28:31], v109
	s_waitcnt lgkmcnt(3)
	v_fmac_f32_e32 v156, v15, v16
	v_fmac_f32_e32 v155, v15, v17
	v_fmac_f32_e32 v67, v15, v18
	v_fmac_f32_e32 v65, v15, v19
	s_waitcnt lgkmcnt(2)
	v_fmac_f32_e32 v77, v15, v20
	v_fmac_f32_e32 v76, v15, v21
	v_fmac_f32_e32 v63, v15, v22
	v_fmac_f32_e32 v61, v15, v23
	s_waitcnt lgkmcnt(1)
	v_fmac_f32_e32 v75, v15, v24
	v_fmac_f32_e32 v74, v15, v25
	v_fmac_f32_e32 v59, v15, v26
	v_fmac_f32_e32 v40, v15, v27
	s_waitcnt lgkmcnt(0)
	v_fmac_f32_e32 v71, v15, v28
	v_fmac_f32_e32 v69, v15, v29
	v_fmac_f32_e32 v3, v15, v30
	ds_read_b128 v[16:19], v110
	v_fmac_f32_e32 v1, v15, v31
	ds_read_b128 v[20:23], v111
	ds_read_b128 v[24:27], v112
	ds_read_b128 v[28:31], v113
	s_waitcnt lgkmcnt(3)
	v_fmac_f32_e32 v156, v12, v16
	v_fmac_f32_e32 v155, v12, v17
	v_fmac_f32_e32 v67, v12, v18
	v_fmac_f32_e32 v65, v12, v19
	s_waitcnt lgkmcnt(2)
	v_fmac_f32_e32 v77, v12, v20
	v_fmac_f32_e32 v76, v12, v21
	v_fmac_f32_e32 v63, v12, v22
	v_fmac_f32_e32 v61, v12, v23
	s_waitcnt lgkmcnt(1)
	v_fmac_f32_e32 v75, v12, v24
	v_fmac_f32_e32 v74, v12, v25
	v_fmac_f32_e32 v59, v12, v26
	v_fmac_f32_e32 v40, v12, v27
	s_waitcnt lgkmcnt(0)
	v_fmac_f32_e32 v71, v12, v28
	v_fmac_f32_e32 v69, v12, v29
	ds_read_b128 v[14:17], v114
	ds_read_b128 v[18:21], v115
	ds_read_b128 v[22:25], v116
	ds_read_b128 v[26:29], v117
	v_fmac_f32_e32 v3, v12, v30
	v_fmac_f32_e32 v1, v12, v31
	s_waitcnt lgkmcnt(2)
	v_fmac_f32_e32 v77, v13, v18
	s_waitcnt lgkmcnt(1)
	v_fmac_f32_e32 v59, v13, v24
	v_fmac_f32_e32 v40, v13, v25
	s_waitcnt lgkmcnt(0)
	v_fmac_f32_e32 v3, v13, v28
	v_fmac_f32_e32 v1, v13, v29
	v_fmac_f32_e32 v156, v13, v14
	v_fmac_f32_e32 v155, v13, v15
	v_fmac_f32_e32 v67, v13, v16
	v_fmac_f32_e32 v65, v13, v17
	v_fmac_f32_e32 v76, v13, v19
	v_fmac_f32_e32 v63, v13, v20
	v_fmac_f32_e32 v61, v13, v21
	v_fmac_f32_e32 v75, v13, v22
	v_fmac_f32_e32 v74, v13, v23
	v_fmac_f32_e32 v71, v13, v26
	v_fmac_f32_e32 v69, v13, v27
	ds_read_b128 v[12:15], v118
	ds_read_b128 v[16:19], v119
	ds_read_b128 v[20:23], v120
	ds_read_b128 v[24:27], v121
	s_waitcnt lgkmcnt(3)
	v_fmac_f32_e32 v156, v10, v12
	v_fmac_f32_e32 v155, v10, v13
	v_fmac_f32_e32 v67, v10, v14
	v_fmac_f32_e32 v65, v10, v15
	s_waitcnt lgkmcnt(2)
	v_fmac_f32_e32 v77, v10, v16
	v_fmac_f32_e32 v76, v10, v17
	v_fmac_f32_e32 v63, v10, v18
	v_fmac_f32_e32 v61, v10, v19
	s_waitcnt lgkmcnt(1)
	v_fmac_f32_e32 v75, v10, v20
	v_fmac_f32_e32 v74, v10, v21
	v_fmac_f32_e32 v59, v10, v22
	v_fmac_f32_e32 v40, v10, v23
	s_waitcnt lgkmcnt(0)
	v_fmac_f32_e32 v71, v10, v24
	v_fmac_f32_e32 v69, v10, v25
	v_fmac_f32_e32 v3, v10, v26
	ds_read_b128 v[12:15], v122
	v_fmac_f32_e32 v1, v10, v27
	ds_read_b128 v[16:19], v123
	ds_read_b128 v[20:23], v124
	ds_read_b128 v[24:27], v125
	s_waitcnt lgkmcnt(3)
	v_fmac_f32_e32 v156, v11, v12
	v_fmac_f32_e32 v155, v11, v13
	v_fmac_f32_e32 v67, v11, v14
	v_fmac_f32_e32 v65, v11, v15
	s_waitcnt lgkmcnt(2)
	v_fmac_f32_e32 v77, v11, v16
	v_fmac_f32_e32 v76, v11, v17
	v_fmac_f32_e32 v63, v11, v18
	v_fmac_f32_e32 v61, v11, v19
	s_waitcnt lgkmcnt(1)
	v_fmac_f32_e32 v75, v11, v20
	v_fmac_f32_e32 v74, v11, v21
	v_fmac_f32_e32 v59, v11, v22
	v_fmac_f32_e32 v40, v11, v23
	s_waitcnt lgkmcnt(0)
	v_fmac_f32_e32 v71, v11, v24
	v_fmac_f32_e32 v69, v11, v25
	v_fmac_f32_e32 v3, v11, v26
	ds_read_b128 v[12:15], v126
	v_fmac_f32_e32 v1, v11, v27
	ds_read_b128 v[16:19], v127
	ds_read_b128 v[20:23], v128
	ds_read_b128 v[24:27], v129
	s_waitcnt lgkmcnt(3)
	v_fmac_f32_e32 v156, v8, v12
	v_fmac_f32_e32 v155, v8, v13
	v_fmac_f32_e32 v67, v8, v14
	v_fmac_f32_e32 v65, v8, v15
	s_waitcnt lgkmcnt(2)
	v_fmac_f32_e32 v77, v8, v16
	v_fmac_f32_e32 v76, v8, v17
	v_fmac_f32_e32 v63, v8, v18
	v_fmac_f32_e32 v61, v8, v19
	s_waitcnt lgkmcnt(1)
	v_fmac_f32_e32 v75, v8, v20
	v_fmac_f32_e32 v74, v8, v21
	v_fmac_f32_e32 v59, v8, v22
	v_fmac_f32_e32 v40, v8, v23
	s_waitcnt lgkmcnt(0)
	v_fmac_f32_e32 v71, v8, v24
	v_fmac_f32_e32 v69, v8, v25
	ds_read_b128 v[10:13], v130
	ds_read_b128 v[14:17], v131
	ds_read_b128 v[18:21], v132
	ds_read_b128 v[22:25], v133
	v_fmac_f32_e32 v3, v8, v26
	v_fmac_f32_e32 v1, v8, v27
	s_waitcnt lgkmcnt(2)
	v_fmac_f32_e32 v77, v9, v14
	s_waitcnt lgkmcnt(1)
	v_fmac_f32_e32 v59, v9, v20
	v_fmac_f32_e32 v40, v9, v21
	s_waitcnt lgkmcnt(0)
	v_fmac_f32_e32 v3, v9, v24
	v_fmac_f32_e32 v1, v9, v25
	v_fmac_f32_e32 v156, v9, v10
	v_fmac_f32_e32 v155, v9, v11
	v_fmac_f32_e32 v67, v9, v12
	v_fmac_f32_e32 v65, v9, v13
	v_fmac_f32_e32 v76, v9, v15
	v_fmac_f32_e32 v63, v9, v16
	v_fmac_f32_e32 v61, v9, v17
	v_fmac_f32_e32 v75, v9, v18
	v_fmac_f32_e32 v74, v9, v19
	v_fmac_f32_e32 v71, v9, v22
	v_fmac_f32_e32 v69, v9, v23
	ds_read_b128 v[8:11], v134
	ds_read_b128 v[12:15], v135
	ds_read_b128 v[16:19], v136
	ds_read_b128 v[20:23], v137
	s_waitcnt lgkmcnt(3)
	v_fmac_f32_e32 v65, v6, v11
	v_fmac_f32_e32 v67, v6, v10
	v_mov_b32_e32 v10, v8
	s_waitcnt lgkmcnt(0)
	v_fmac_f32_e32 v3, v6, v22
	v_fmac_f32_e32 v1, v6, v23
	ds_read_b128 v[22:25], v138
	ds_read_b128 v[26:29], v139
	ds_read_b128 v[30:33], v140
	ds_read_b128 v[158:161], v141
	v_fmac_f32_e32 v63, v6, v14
	s_waitcnt lgkmcnt(3)
	v_mov_b32_e32 v11, v22
	v_mov_b32_e32 v22, v9
	v_pk_mul_f32 v[8:9], v[6:7], v[22:23]
	v_pk_mul_f32 v[10:11], v[6:7], v[10:11]
	v_add_f32_e32 v8, v155, v8
	v_add_f32_e32 v155, v8, v9
	v_mov_b32_e32 v8, v12
	s_waitcnt lgkmcnt(2)
; template <bool COMBINE, bool ROUTE, bool FINAL, bool OUT8 = false, bool DUMMY = false> ...
;     ...
; #pragma unroll
;                 for (int j = 0; j < 8; ++j) {
; #pragma unroll
;                     for (int cc = 0; cc < 4; ++cc) {
;                         const float hv = xv[j][cc];
;                         const f32x4 w0 = WT[((j * 4 + cc) * 4 + 0) * 64 + lane], w1 = WT[((j * 4 + cc) * 4 + 1) * 64 + lane], w2 = WT[((j * 4 + cc) * 4 + 2) * 64 + lane], w3 = WT[((j * 4 + cc) * 4 + 3) * 64 + lane];
;                         lg[0] += hv * w0.x; lg[1] += hv * w0.y; lg[2] += hv * w0.z; lg[3] += hv * w0.w;
;                         lg[4] += hv * w1.x; lg[5] += hv * w1.y; lg[6] += hv * w1.z; lg[7] += hv * w1.w;
;                         lg[8] += hv * w2.x; lg[9] += hv * w2.y; lg[10] += hv * w2.z; lg[11] += hv * w2.w;
;                         lg[12] += hv * w3.x; lg[13] += hv * w3.y; lg[14] += hv * w3.z; lg[15] += hv * w3.w;
;                     }
;                     __builtin_amdgcn_sched_barrier(0);
;                 }
;                 float sc_[16], sel[16];
; #pragma unroll
;                 for (int e = 0; e < 16; ++e) { lg[e] = wave_sum(lg[e]); sc_[e] = 1.f / (1.f + expf(-lg[e])); sel[e] = sc_[e] + rb[e]; }
	v_mov_b32_e32 v9, v26
	v_pk_mul_f32 v[8:9], v[6:7], v[8:9]
	v_mov_b32_e32 v26, v13
	v_add_f32_e32 v8, v77, v8
	v_add_f32_e32 v77, v8, v9
	v_pk_mul_f32 v[8:9], v[6:7], v[26:27]
	v_add_f32_e32 v0, v156, v10
	v_add_f32_e32 v8, v76, v8
	v_add_f32_e32 v76, v8, v9
	v_mov_b32_e32 v8, v16
	s_waitcnt lgkmcnt(1)
	v_mov_b32_e32 v9, v30
	v_pk_mul_f32 v[8:9], v[6:7], v[8:9]
	v_mov_b32_e32 v30, v17
	v_add_f32_e32 v8, v75, v8
	v_add_f32_e32 v156, v8, v9
	v_pk_mul_f32 v[8:9], v[6:7], v[30:31]
	v_fmac_f32_e32 v61, v6, v15
	v_add_f32_e32 v8, v74, v8
	v_add_f32_e32 v157, v8, v9
	v_mov_b32_e32 v8, v20
	s_waitcnt lgkmcnt(0)
	v_mov_b32_e32 v9, v158
	v_pk_mul_f32 v[8:9], v[6:7], v[8:9]
	v_mov_b32_e32 v158, v21
	v_add_f32_e32 v8, v71, v8
	v_add_f32_e32 v71, v8, v9
	v_pk_mul_f32 v[8:9], v[6:7], v[158:159]
	v_fmac_f32_e32 v59, v6, v18
	v_fmac_f32_e32 v40, v6, v19
	v_add_f32_e32 v6, v69, v8
	v_add_f32_e32 v0, v0, v11
	v_fmac_f32_e32 v67, v7, v24
	v_fmac_f32_e32 v65, v7, v25
	v_fmac_f32_e32 v63, v7, v28
	v_fmac_f32_e32 v61, v7, v29
	v_fmac_f32_e32 v59, v7, v32
	v_fmac_f32_e32 v40, v7, v33
	v_add_f32_e32 v69, v6, v9
	v_fmac_f32_e32 v3, v7, v160
	v_fmac_f32_e32 v1, v7, v161
	ds_read_b128 v[6:9], v142
	ds_read_b128 v[10:13], v143
	ds_read_b128 v[14:17], v144
	ds_read_b128 v[18:21], v145
	ds_read_b128 v[22:25], v146
	ds_read_b128 v[26:29], v147
	ds_read_b128 v[30:33], v148
	ds_read_b128 v[72:75], v149
	s_waitcnt lgkmcnt(7)
	v_mov_b32_e32 v34, v6
	s_waitcnt lgkmcnt(3)
	v_mov_b32_e32 v35, v22
	v_mov_b32_e32 v22, v7
	v_pk_mul_f32 v[6:7], v[4:5], v[22:23]
	v_pk_mul_f32 v[34:35], v[4:5], v[34:35]
	v_add_f32_e32 v6, v155, v6
	v_add_f32_e32 v0, v0, v34
	v_add_f32_e32 v34, v6, v7
	v_mov_b32_e32 v6, v8
	v_mov_b32_e32 v7, v24
	v_pk_mul_f32 v[6:7], v[4:5], v[6:7]
	v_mov_b32_e32 v24, v9
	v_add_f32_e32 v6, v67, v6
	v_add_f32_e32 v8, v6, v7
	v_pk_mul_f32 v[6:7], v[4:5], v[24:25]
	v_add_f32_e32 v0, v0, v35
	v_add_f32_e32 v6, v65, v6
	v_add_f32_e32 v9, v6, v7
	v_mov_b32_e32 v6, v10
	s_waitcnt lgkmcnt(2)
	v_mov_b32_e32 v7, v26
	v_pk_mul_f32 v[6:7], v[4:5], v[6:7]
	v_mov_b32_e32 v26, v11
	v_add_f32_e32 v6, v77, v6
	v_add_f32_e32 v35, v6, v7
	v_pk_mul_f32 v[6:7], v[4:5], v[26:27]
	s_nop 0
	v_add_f32_e32 v6, v76, v6
	v_add_f32_e32 v65, v6, v7
	v_mov_b32_e32 v6, v12
	v_mov_b32_e32 v7, v28
	v_pk_mul_f32 v[6:7], v[4:5], v[6:7]
	v_mov_b32_e32 v28, v13
	v_add_f32_e32 v6, v63, v6
	v_add_f32_e32 v63, v6, v7
	v_pk_mul_f32 v[6:7], v[4:5], v[28:29]
	s_nop 0
	v_add_f32_e32 v6, v61, v6
	v_add_f32_e32 v61, v6, v7
	v_mov_b32_e32 v6, v14
	s_waitcnt lgkmcnt(1)
	v_mov_b32_e32 v7, v30
	v_pk_mul_f32 v[6:7], v[4:5], v[6:7]
	v_mov_b32_e32 v30, v15
	v_add_f32_e32 v6, v156, v6
	v_add_f32_e32 v27, v6, v7
	v_pk_mul_f32 v[6:7], v[4:5], v[30:31]
	s_nop 0
	v_add_f32_e32 v6, v157, v6
	v_add_f32_e32 v26, v6, v7
	v_mov_b32_e32 v6, v16
	v_mov_b32_e32 v7, v32
	v_pk_mul_f32 v[6:7], v[4:5], v[6:7]
	v_mov_b32_e32 v32, v17
	v_add_f32_e32 v6, v59, v6
	v_add_f32_e32 v25, v6, v7
	v_pk_mul_f32 v[6:7], v[4:5], v[32:33]
	s_nop 0
	v_add_f32_e32 v6, v40, v6
	v_add_f32_e32 v23, v6, v7
	v_mov_b32_e32 v6, v18
	s_waitcnt lgkmcnt(0)
	v_mov_b32_e32 v7, v72
	v_pk_mul_f32 v[6:7], v[4:5], v[6:7]
	v_mov_b32_e32 v72, v19
	v_add_f32_e32 v6, v71, v6
	v_add_f32_e32 v24, v6, v7
	v_pk_mul_f32 v[6:7], v[4:5], v[72:73]
	s_nop 0
	v_add_f32_e32 v6, v69, v6
	v_add_f32_e32 v22, v6, v7
	v_mov_b32_e32 v6, v20
	v_mov_b32_e32 v7, v74
	v_mov_b32_e32 v74, v21
	v_pk_mul_f32 v[6:7], v[4:5], v[6:7]
	v_pk_mul_f32 v[4:5], v[4:5], v[74:75]
	v_add_f32_e32 v3, v3, v6
	v_add_f32_e32 v1, v1, v4
	v_add_f32_e32 v3, v3, v7
	v_add_f32_e32 v1, v1, v5
	ds_bpermute_b32 v4, v78, v0
	ds_bpermute_b32 v5, v78, v34
	global_load_dwordx4 v[16:19], v41, s[42:43]
	s_waitcnt lgkmcnt(1)
	v_add_f32_e32 v0, v0, v4
	s_waitcnt lgkmcnt(0)
	v_add_f32_e32 v4, v34, v5
	ds_bpermute_b32 v5, v79, v0
	ds_bpermute_b32 v6, v79, v4
	s_waitcnt lgkmcnt(1)
	v_add_f32_e32 v0, v0, v5
	s_waitcnt lgkmcnt(0)
	v_add_f32_e32 v4, v4, v6
	ds_bpermute_b32 v5, v80, v0
	ds_bpermute_b32 v6, v80, v4
	s_waitcnt lgkmcnt(1)
	v_add_f32_e32 v0, v0, v5
	s_waitcnt lgkmcnt(0)
	v_add_f32_e32 v4, v4, v6
	ds_bpermute_b32 v5, v81, v0
	ds_bpermute_b32 v6, v81, v4
	s_waitcnt lgkmcnt(1)
	v_add_f32_e32 v0, v0, v5
	s_waitcnt lgkmcnt(0)
	v_add_f32_e32 v4, v4, v6
	ds_bpermute_b32 v5, v82, v0
	ds_bpermute_b32 v6, v82, v4
	s_waitcnt lgkmcnt(1)
	v_add_f32_e32 v0, v0, v5
	s_waitcnt lgkmcnt(0)
	v_add_f32_e32 v4, v4, v6
	ds_bpermute_b32 v5, v83, v0
	ds_bpermute_b32 v6, v83, v4
	s_waitcnt lgkmcnt(1)
	v_add_f32_e32 v0, v0, v5
	s_waitcnt lgkmcnt(0)
	v_add_f32_e32 v5, v4, v6
	v_mul_f32_e32 v4, 0xbfb8aa3b, v0
	v_fma_f32 v7, v0, s58, -v4
	v_rndne_f32_e32 v10, v4
	v_mul_f32_e32 v6, 0xbfb8aa3b, v5
	v_fmac_f32_e32 v7, 0xb2a5705f, v0
	v_sub_f32_e32 v4, v4, v10
	v_fma_f32 v11, v5, s58, -v6
	v_rndne_f32_e32 v12, v6
	v_add_f32_e32 v4, v4, v7
	v_cvt_i32_f32_e32 v10, v10
	v_fmac_f32_e32 v11, 0xb2a5705f, v5
	v_sub_f32_e32 v6, v6, v12
	v_exp_f32_e32 v4, v4
	v_add_f32_e32 v6, v6, v11
	v_cvt_i32_f32_e32 v12, v12
	v_exp_f32_e32 v6, v6
	ds_bpermute_b32 v7, v78, v8
	v_ldexp_f32 v4, v4, v10
	v_cmp_nlt_f32_e32 vcc, s59, v0
	v_ldexp_f32 v6, v6, v12
	global_load_dwordx4 v[12:15], v41, s[42:43] offset:16
	v_cndmask_b32_e32 v4, 0, v4, vcc
	v_cmp_ngt_f32_e32 vcc, s61, v0
	s_waitcnt lgkmcnt(0)
	v_add_f32_e32 v7, v8, v7
	ds_bpermute_b32 v8, v79, v7
	v_cndmask_b32_e32 v4, v152, v4, vcc
	v_cmp_nlt_f32_e32 vcc, s59, v5
	s_waitcnt lgkmcnt(0)
	v_add_f32_e32 v7, v7, v8
	v_cndmask_b32_e32 v0, 0, v6, vcc
	v_cmp_ngt_f32_e32 vcc, s61, v5
	ds_bpermute_b32 v8, v80, v7
	s_waitcnt lgkmcnt(0)
; template <bool COMBINE, bool ROUTE, bool FINAL, bool OUT8 = false, bool DUMMY = false> ...
;     ...
;                 float sc_[16], sel[16];
; #pragma unroll
;                 for (int e = 0; e < 16; ++e) { lg[e] = wave_sum(lg[e]); sc_[e] = 1.f / (1.f + expf(-lg[e])); sel[e] = sc_[e] + rb[e]; }
	v_add_f32_e32 v7, v7, v8
	v_cndmask_b32_e32 v5, v152, v0, vcc
	v_pk_add_f32 v[4:5], v[4:5], 1.0 op_sel_hi:[1,0]
	ds_bpermute_b32 v8, v81, v7
	v_div_scale_f32 v0, s[6:7], v5, v5, 1.0
	v_rcp_f32_e32 v6, v0
	s_nop 0
	v_fma_f32 v10, -v0, v6, 1.0
	v_fmac_f32_e32 v6, v10, v6
	v_div_scale_f32 v10, vcc, 1.0, v5, 1.0
	v_mul_f32_e32 v11, v10, v6
	v_fma_f32 v20, -v0, v11, v10
	v_fmac_f32_e32 v11, v20, v6
	v_fma_f32 v0, -v0, v11, v10
	v_div_scale_f32 v10, s[6:7], v4, v4, 1.0
	v_rcp_f32_e32 v20, v10
	v_div_fmas_f32 v0, v0, v6, v11
	v_div_fixup_f32 v21, v0, v5, 1.0
	v_div_scale_f32 v6, vcc, 1.0, v4, 1.0
	v_fma_f32 v0, -v10, v20, 1.0
	v_fmac_f32_e32 v20, v0, v20
	s_waitcnt lgkmcnt(0)
	v_add_f32_e32 v0, v7, v8
	ds_bpermute_b32 v5, v82, v0
	v_mul_f32_e32 v7, v6, v20
	v_fma_f32 v8, -v10, v7, v6
	v_fmac_f32_e32 v7, v8, v20
	v_fma_f32 v6, -v10, v7, v6
	s_waitcnt lgkmcnt(0)
	v_add_f32_e32 v0, v0, v5
	ds_bpermute_b32 v5, v83, v0
	ds_bpermute_b32 v10, v78, v9
	v_div_fmas_f32 v6, v6, v20, v7
	v_div_fixup_f32 v20, v6, v4, 1.0
	s_waitcnt vmcnt(1)
	v_pk_add_f32 v[16:17], v[16:17], v[20:21]
	s_waitcnt lgkmcnt(1)
	v_add_f32_e32 v0, v0, v5
	v_mul_f32_e32 v5, 0xbfb8aa3b, v0
	v_fma_f32 v7, v0, s58, -v5
	v_rndne_f32_e32 v8, v5
	v_fmac_f32_e32 v7, 0xb2a5705f, v0
	v_sub_f32_e32 v5, v5, v8
	s_waitcnt lgkmcnt(0)
	v_add_f32_e32 v30, v9, v10
	v_add_f32_e32 v5, v5, v7
	ds_bpermute_b32 v31, v79, v30
	v_exp_f32_e32 v28, v5
	v_cvt_i32_f32_e32 v29, v8
	v_cmp_nlt_f32_e32 vcc, s59, v0
	global_load_dwordx4 v[4:7], v41, s[42:43] offset:48
	global_load_dwordx4 v[8:11], v41, s[42:43] offset:32
	v_ldexp_f32 v28, v28, v29
	s_waitcnt lgkmcnt(0)
	v_add_f32_e32 v29, v30, v31
	ds_bpermute_b32 v30, v80, v29
	v_cndmask_b32_e32 v28, 0, v28, vcc
	v_cmp_ngt_f32_e32 vcc, s61, v0
	s_nop 1
	v_cndmask_b32_e32 v0, v152, v28, vcc
	s_waitcnt lgkmcnt(0)
	v_add_f32_e32 v28, v29, v30
	ds_bpermute_b32 v29, v81, v28
	v_add_f32_e32 v0, 1.0, v0
	v_div_scale_f32 v30, s[6:7], v0, v0, 1.0
	v_rcp_f32_e32 v31, v30
	s_waitcnt lgkmcnt(0)
	v_add_f32_e32 v28, v28, v29
	ds_bpermute_b32 v29, v82, v28
	v_fma_f32 v32, -v30, v31, 1.0
	v_fmac_f32_e32 v31, v32, v31
	v_div_scale_f32 v32, vcc, 1.0, v0, 1.0
	s_waitcnt lgkmcnt(0)
	v_add_f32_e32 v28, v28, v29
	ds_bpermute_b32 v29, v83, v28
	v_mul_f32_e32 v33, v32, v31
	v_fma_f32 v34, -v30, v33, v32
	v_fmac_f32_e32 v33, v34, v31
	v_fma_f32 v30, -v30, v33, v32
	s_waitcnt lgkmcnt(0)
	v_add_f32_e32 v28, v28, v29
	v_mul_f32_e32 v29, 0xbfb8aa3b, v28
	v_fma_f32 v32, v28, s58, -v29
	v_rndne_f32_e32 v34, v29
	v_fmac_f32_e32 v32, 0xb2a5705f, v28
	v_sub_f32_e32 v29, v29, v34
	v_add_f32_e32 v29, v29, v32
	v_cvt_i32_f32_e32 v32, v34
	ds_bpermute_b32 v34, v78, v35
	v_div_fmas_f32 v30, v30, v31, v33
	v_exp_f32_e32 v29, v29
	v_div_fixup_f32 v0, v30, v0, 1.0
	v_cmp_nlt_f32_e32 vcc, s59, v28
	s_waitcnt lgkmcnt(0)
	v_add_f32_e32 v30, v35, v34
	ds_bpermute_b32 v31, v79, v30
	v_ldexp_f32 v29, v29, v32
	v_cndmask_b32_e32 v29, 0, v29, vcc
	v_cmp_ngt_f32_e32 vcc, s61, v28
	v_add_f32_e32 v67, v18, v0
	ds_bpermute_b32 v18, v78, v65
	v_cndmask_b32_e32 v28, v152, v29, vcc
	s_waitcnt lgkmcnt(1)
	v_add_f32_e32 v29, v30, v31
	ds_bpermute_b32 v30, v80, v29
	v_add_f32_e32 v31, 1.0, v28
	v_div_scale_f32 v28, s[6:7], v31, v31, 1.0
	v_rcp_f32_e32 v32, v28
	s_waitcnt lgkmcnt(0)
	v_add_f32_e32 v29, v29, v30
	ds_bpermute_b32 v30, v81, v29
	v_add_f32_e32 v18, v65, v18
	v_fma_f32 v33, -v28, v32, 1.0
	v_fmac_f32_e32 v32, v33, v32
	ds_bpermute_b32 v33, v79, v18
	s_waitcnt lgkmcnt(1)
	v_add_f32_e32 v29, v29, v30
	ds_bpermute_b32 v30, v82, v29
	v_div_scale_f32 v34, vcc, 1.0, v31, 1.0
	s_waitcnt lgkmcnt(1)
	v_add_f32_e32 v18, v18, v33
	ds_bpermute_b32 v33, v80, v18
	s_waitcnt lgkmcnt(1)
	v_add_f32_e32 v29, v29, v30
	ds_bpermute_b32 v30, v83, v29
	v_mul_f32_e32 v35, v34, v32
	v_fma_f32 v40, -v28, v35, v34
	s_waitcnt lgkmcnt(1)
	v_add_f32_e32 v18, v18, v33
	v_fmac_f32_e32 v35, v40, v32
	s_waitcnt lgkmcnt(0)
	v_add_f32_e32 v29, v29, v30
	ds_bpermute_b32 v30, v81, v18
	v_mul_f32_e32 v33, 0xbfb8aa3b, v29
	v_fma_f32 v40, v29, s58, -v33
	v_rndne_f32_e32 v59, v33
	v_fmac_f32_e32 v40, 0xb2a5705f, v29
	s_waitcnt lgkmcnt(0)
	v_add_f32_e32 v18, v18, v30
	ds_bpermute_b32 v30, v82, v18
	v_sub_f32_e32 v33, v33, v59
	v_add_f32_e32 v33, v33, v40
	v_exp_f32_e32 v33, v33
	v_cvt_i32_f32_e32 v40, v59
	s_waitcnt lgkmcnt(0)
	v_add_f32_e32 v18, v18, v30
	ds_bpermute_b32 v30, v83, v18
	v_fma_f32 v28, -v28, v35, v34
	v_div_fmas_f32 v32, v28, v32, v35
	v_ldexp_f32 v28, v33, v40
	v_cmp_nlt_f32_e32 vcc, s59, v29
	s_waitcnt lgkmcnt(0)
	v_add_f32_e32 v18, v18, v30
	v_mul_f32_e32 v30, 0xbfb8aa3b, v18
	v_fma_f32 v33, v18, s58, -v30
	v_rndne_f32_e32 v34, v30
	v_fmac_f32_e32 v33, 0xb2a5705f, v18
	v_sub_f32_e32 v30, v30, v34
	v_add_f32_e32 v30, v30, v33
	v_exp_f32_e32 v30, v30
	v_cvt_i32_f32_e32 v33, v34
	v_cndmask_b32_e32 v28, 0, v28, vcc
	v_cmp_ngt_f32_e32 vcc, s61, v29
	ds_bpermute_b32 v40, v78, v61
	v_ldexp_f32 v29, v30, v33
	v_cndmask_b32_e32 v28, v152, v28, vcc
	v_cmp_nlt_f32_e32 vcc, s59, v18
	s_nop 1
	v_cndmask_b32_e32 v29, 0, v29, vcc
	v_cmp_ngt_f32_e32 vcc, s61, v18
	ds_bpermute_b32 v18, v78, v63
	s_waitcnt lgkmcnt(0)
	v_add_f32_e32 v18, v63, v18
	v_cndmask_b32_e32 v29, v152, v29, vcc
	v_pk_add_f32 v[28:29], v[28:29], 1.0 op_sel_hi:[1,0]
	ds_bpermute_b32 v34, v79, v18
	v_div_scale_f32 v30, s[6:7], v29, v29, 1.0
	v_rcp_f32_e32 v33, v30
	v_div_fixup_f32 v63, v32, v31, 1.0
	v_add_f32_e32 v65, v19, v63
	s_waitcnt lgkmcnt(0)
	v_add_f32_e32 v18, v18, v34
	v_fma_f32 v19, -v30, v33, 1.0
	v_fmac_f32_e32 v33, v19, v33
	ds_bpermute_b32 v19, v80, v18
	v_div_scale_f32 v31, vcc, 1.0, v29, 1.0
	v_mul_f32_e32 v32, v31, v33
	v_fma_f32 v34, -v30, v32, v31
	s_waitcnt lgkmcnt(0)
; template <bool COMBINE, bool ROUTE, bool FINAL, bool OUT8 = false, bool DUMMY = false> ...
;     ...
;                 float sc_[16], sel[16];
; #pragma unroll
;                 for (int e = 0; e < 16; ++e) { lg[e] = wave_sum(lg[e]); sc_[e] = 1.f / (1.f + expf(-lg[e])); sel[e] = sc_[e] + rb[e]; }
	v_add_f32_e32 v18, v18, v19
	ds_bpermute_b32 v19, v81, v18
	v_fmac_f32_e32 v32, v34, v33
	v_fma_f32 v30, -v30, v32, v31
	v_div_scale_f32 v31, s[6:7], v28, v28, 1.0
	s_waitcnt lgkmcnt(0)
	v_add_f32_e32 v18, v18, v19
	ds_bpermute_b32 v35, v82, v18
	v_div_fmas_f32 v19, v30, v33, v32
	v_rcp_f32_e32 v34, v31
	v_div_fixup_f32 v19, v19, v29, 1.0
	s_waitcnt lgkmcnt(0)
	v_add_f32_e32 v18, v18, v35
	ds_bpermute_b32 v30, v83, v18
	v_fma_f32 v29, -v31, v34, 1.0
	v_fmac_f32_e32 v34, v29, v34
	v_div_scale_f32 v29, vcc, 1.0, v28, 1.0
	s_waitcnt lgkmcnt(0)
	v_add_f32_e32 v18, v18, v30
	v_mul_f32_e32 v30, 0xbfb8aa3b, v18
	v_fma_f32 v33, v18, s58, -v30
	v_rndne_f32_e32 v35, v30
	v_fmac_f32_e32 v33, 0xb2a5705f, v18
	v_sub_f32_e32 v30, v30, v35
	v_add_f32_e32 v30, v30, v33
	v_cvt_i32_f32_e32 v33, v35
	v_add_f32_e32 v35, v61, v40
	ds_bpermute_b32 v40, v79, v35
	v_mul_f32_e32 v32, v29, v34
	v_exp_f32_e32 v30, v30
	v_fma_f32 v59, -v31, v32, v29
	v_fmac_f32_e32 v32, v59, v34
	v_fma_f32 v29, -v31, v32, v29
	s_waitcnt lgkmcnt(0)
	v_add_f32_e32 v31, v35, v40
	v_ldexp_f32 v30, v30, v33
	ds_bpermute_b32 v33, v80, v31
	v_cmp_nlt_f32_e64 s[6:7], s59, v18
	s_nop 1
	v_cndmask_b32_e64 v30, 0, v30, s[6:7]
	v_cmp_ngt_f32_e64 s[6:7], s61, v18
	s_nop 1
	v_cndmask_b32_e64 v18, v152, v30, s[6:7]
	s_waitcnt lgkmcnt(0)
	v_add_f32_e32 v30, v31, v33
	ds_bpermute_b32 v31, v81, v30
	v_add_f32_e32 v33, 1.0, v18
	v_div_fmas_f32 v18, v29, v34, v32
	v_div_fixup_f32 v18, v18, v28, 1.0
	s_waitcnt vmcnt(2)
	v_pk_add_f32 v[72:73], v[12:13], v[18:19]
	s_waitcnt lgkmcnt(0)
	v_add_f32_e32 v30, v30, v31
	ds_bpermute_b32 v31, v82, v30
	v_div_scale_f32 v35, s[6:7], v33, v33, 1.0
	v_rcp_f32_e32 v40, v35
	v_cmp_nlg_f32_e64 s[12:13], s62, v72
	s_waitcnt lgkmcnt(0)
	v_add_f32_e32 v13, v30, v31
	ds_bpermute_b32 v28, v83, v13
	v_fma_f32 v12, -v35, v40, 1.0
	v_fmac_f32_e32 v40, v12, v40
	v_div_scale_f32 v12, vcc, 1.0, v33, 1.0
	s_waitcnt lgkmcnt(0)
	v_add_f32_e32 v13, v13, v28
	v_mul_f32_e32 v28, 0xbfb8aa3b, v13
	v_fma_f32 v30, v13, s58, -v28
	v_rndne_f32_e32 v31, v28
	v_fmac_f32_e32 v30, 0xb2a5705f, v13
	v_sub_f32_e32 v28, v28, v31
	v_add_f32_e32 v28, v28, v30
	v_mul_f32_e32 v29, v12, v40
	v_exp_f32_e32 v28, v28
	v_cvt_i32_f32_e32 v30, v31
	v_fma_f32 v31, -v35, v29, v12
	v_fmac_f32_e32 v29, v31, v40
	v_fma_f32 v12, -v35, v29, v12
	v_ldexp_f32 v28, v28, v30
	v_cmp_nlt_f32_e64 s[6:7], s59, v13
	v_div_fmas_f32 v12, v12, v40, v29
	v_div_fixup_f32 v32, v12, v33, 1.0
	v_cndmask_b32_e64 v28, 0, v28, s[6:7]
	v_cmp_ngt_f32_e64 s[6:7], s61, v13
	v_add_f32_e32 v61, v14, v32
	ds_bpermute_b32 v14, v78, v27
	v_cndmask_b32_e64 v13, v152, v28, s[6:7]
	v_add_f32_e32 v13, 1.0, v13
	v_div_scale_f32 v28, s[6:7], v13, v13, 1.0
	v_rcp_f32_e32 v30, v28
	s_waitcnt lgkmcnt(0)
	v_add_f32_e32 v14, v27, v14
	ds_bpermute_b32 v27, v79, v14
	ds_bpermute_b32 v33, v78, v26
	v_fma_f32 v12, -v28, v30, 1.0
	v_fmac_f32_e32 v30, v12, v30
	v_div_scale_f32 v12, vcc, 1.0, v13, 1.0
	v_mul_f32_e32 v29, v12, v30
	v_fma_f32 v31, -v28, v29, v12
	v_fmac_f32_e32 v29, v31, v30
	s_waitcnt lgkmcnt(1)
	v_add_f32_e32 v14, v14, v27
	s_waitcnt lgkmcnt(0)
	v_add_f32_e32 v26, v26, v33
	v_fma_f32 v12, -v28, v29, v12
	ds_bpermute_b32 v27, v80, v14
	ds_bpermute_b32 v28, v79, v26
	v_div_fmas_f32 v12, v12, v30, v29
	v_div_fixup_f32 v34, v12, v13, 1.0
	v_add_f32_e32 v69, v15, v34
	s_waitcnt lgkmcnt(1)
	v_add_f32_e32 v12, v14, v27
	s_waitcnt lgkmcnt(0)
	v_add_f32_e32 v14, v26, v28
	ds_bpermute_b32 v13, v81, v12
	ds_bpermute_b32 v26, v80, v14
	ds_bpermute_b32 v15, v78, v25
	v_cmp_gt_f32_e32 vcc, v17, v16
	v_cmp_nlg_f32_e64 s[6:7], s62, v16
	s_waitcnt lgkmcnt(2)
	v_add_f32_e32 v12, v12, v13
	s_waitcnt lgkmcnt(1)
	v_add_f32_e32 v14, v14, v26
	s_waitcnt lgkmcnt(0)
	v_add_f32_e32 v25, v25, v15
	ds_bpermute_b32 v13, v82, v12
	ds_bpermute_b32 v26, v81, v14
	ds_bpermute_b32 v27, v79, v25
	s_waitcnt lgkmcnt(2)
	v_add_f32_e32 v15, v12, v13
	s_waitcnt lgkmcnt(1)
	v_add_f32_e32 v12, v14, v26
	s_waitcnt lgkmcnt(0)
	v_add_f32_e32 v14, v25, v27
	ds_bpermute_b32 v26, v78, v24
	ds_bpermute_b32 v13, v78, v23
	ds_bpermute_b32 v25, v80, v14
	ds_bpermute_b32 v27, v82, v12
	ds_bpermute_b32 v35, v83, v15
	s_waitcnt lgkmcnt(4)
	v_add_f32_e32 v24, v24, v26
	s_waitcnt lgkmcnt(3)
	v_add_f32_e32 v13, v23, v13
	s_waitcnt lgkmcnt(2)
	v_add_f32_e32 v14, v14, v25
	ds_bpermute_b32 v25, v79, v24
	ds_bpermute_b32 v23, v79, v13
	s_waitcnt lgkmcnt(3)
	v_add_f32_e32 v40, v12, v27
	ds_bpermute_b32 v26, v81, v14
	ds_bpermute_b32 v59, v83, v40
	s_waitcnt lgkmcnt(3)
	v_add_f32_e32 v12, v24, v25
	s_waitcnt lgkmcnt(2)
	v_add_f32_e32 v13, v13, v23
	ds_bpermute_b32 v24, v80, v12
	ds_bpermute_b32 v23, v80, v13
	s_waitcnt lgkmcnt(3)
; template <bool COMBINE, bool ROUTE, bool FINAL, bool OUT8 = false, bool DUMMY = false> ...
;     ...
;                 for (int e = 0; e < 16; ++e) { lg[e] = wave_sum(lg[e]); sc_[e] = 1.f / (1.f + expf(-lg[e])); sel[e] = sc_[e] + rb[e]; }
;                 float gsv[4], gw1[4], gw2[4]; int gi1[4], gi2[4];
; #pragma unroll
;                 for (int gq = 0; gq < 4; ++gq) {
;                     float m1 = sel[4 * gq]; int i1 = 0; float s1 = sc_[4 * gq];
; #pragma unroll
;                     for (int i = 1; i < 4; ++i) if (sel[4 * gq + i] > m1) { m1 = sel[4 * gq + i]; i1 = i; s1 = sc_[4 * gq + i]; }
;                     float m2 = -INFINITY; int i2 = 0; float s2 = 0.f;
; #pragma unroll
;                     for (int i = 0; i < 4; ++i) if (i != i1 && sel[4 * gq + i] > m2) { m2 = sel[4 * gq + i]; i2 = i; s2 = sc_[4 * gq + i]; }
;                     gsv[gq] = m1 + m2; gi1[gq] = 4 * gq + i1; gi2[gq] = 4 * gq + i2; gw1[gq] = s1; gw2[gq] = s2;
;                 }
;                 float bv = gsv[0]; int e0 = gi1[0], e1 = gi2[0]; float w0 = gw1[0], w1 = gw2[0];
; #pragma unroll
;                 for (int gq = 1; gq < 4; ++gq) if (gsv[gq] > bv) { bv = gsv[gq]; e0 = gi1[gq]; e1 = gi2[gq]; w0 = gw1[gq]; w1 = gw2[gq]; }
	v_add_f32_e32 v14, v14, v26
	ds_bpermute_b32 v25, v82, v14
	s_waitcnt lgkmcnt(2)
	v_add_f32_e32 v12, v12, v24
	s_waitcnt lgkmcnt(1)
	v_add_f32_e32 v13, v13, v23
	ds_bpermute_b32 v24, v81, v12
	ds_bpermute_b32 v23, v81, v13
	s_waitcnt lgkmcnt(2)
	v_add_f32_e32 v14, v14, v25
	ds_bpermute_b32 v33, v83, v14
	s_waitcnt lgkmcnt(2)
	v_add_f32_e32 v12, v12, v24
	s_waitcnt lgkmcnt(1)
	v_add_f32_e32 v13, v13, v23
	ds_bpermute_b32 v24, v82, v12
	ds_bpermute_b32 v23, v82, v13
	s_waitcnt lgkmcnt(1)
	v_add_f32_e32 v26, v12, v24
	ds_bpermute_b32 v12, v78, v3
	s_waitcnt lgkmcnt(1)
	v_add_f32_e32 v30, v13, v23
	ds_bpermute_b32 v13, v78, v22
	ds_bpermute_b32 v23, v78, v1
	ds_bpermute_b32 v31, v83, v30
	s_waitcnt lgkmcnt(3)
	v_add_f32_e32 v3, v3, v12
	ds_bpermute_b32 v12, v79, v3
	s_waitcnt lgkmcnt(3)
	v_add_f32_e32 v13, v22, v13
	s_waitcnt lgkmcnt(2)
	v_add_f32_e32 v1, v1, v23
	ds_bpermute_b32 v22, v79, v13
	ds_bpermute_b32 v23, v79, v1
	s_waitcnt lgkmcnt(2)
	v_add_f32_e32 v3, v3, v12
	ds_bpermute_b32 v12, v80, v3
	ds_bpermute_b32 v27, v83, v26
	s_waitcnt lgkmcnt(3)
	v_add_f32_e32 v13, v13, v22
	s_waitcnt lgkmcnt(2)
	v_add_f32_e32 v1, v1, v23
	ds_bpermute_b32 v22, v80, v13
	ds_bpermute_b32 v23, v80, v1
	s_waitcnt lgkmcnt(3)
	v_add_f32_e32 v3, v3, v12
	ds_bpermute_b32 v12, v81, v3
	s_waitcnt lgkmcnt(2)
	v_add_f32_e32 v13, v13, v22
	s_waitcnt lgkmcnt(1)
	v_add_f32_e32 v1, v1, v23
	ds_bpermute_b32 v22, v81, v13
	ds_bpermute_b32 v23, v81, v1
	s_waitcnt lgkmcnt(2)
	v_add_f32_e32 v3, v3, v12
	ds_bpermute_b32 v12, v82, v3
	s_waitcnt lgkmcnt(2)
	v_add_f32_e32 v13, v13, v22
	s_waitcnt lgkmcnt(1)
	v_add_f32_e32 v1, v1, v23
	ds_bpermute_b32 v22, v82, v13
	ds_bpermute_b32 v23, v82, v1
	s_waitcnt lgkmcnt(2)
	v_add_f32_e32 v24, v3, v12
	v_cndmask_b32_e32 v12, v16, v17, vcc
	v_cndmask_b32_e64 v3, 0, 1, vcc
	s_waitcnt lgkmcnt(1)
	v_add_f32_e32 v28, v13, v22
	s_waitcnt lgkmcnt(0)
	v_add_f32_e32 v22, v1, v23
	v_cndmask_b32_e32 v1, v20, v21, vcc
	v_cmp_gt_f32_e32 vcc, v67, v12
	ds_bpermute_b32 v29, v83, v28
	ds_bpermute_b32 v25, v83, v24
	v_cndmask_b32_e32 v12, v12, v67, vcc
	v_cndmask_b32_e32 v1, v1, v0, vcc
	v_cndmask_b32_e64 v13, v3, 2, vcc
	v_cmp_ngt_f32_e32 vcc, v65, v12
	ds_bpermute_b32 v23, v83, v22
	s_nop 0
	v_cndmask_b32_e32 v71, v65, v12, vcc
	v_cndmask_b32_e32 v12, 3, v13, vcc
	v_cmp_eq_u32_e64 s[8:9], 0, v12
	s_or_b64 s[6:7], s[8:9], s[6:7]
	v_cndmask_b32_e32 v3, v63, v1, vcc
	v_cndmask_b32_e64 v1, v16, v153, s[6:7]
	v_cndmask_b32_e64 v13, v20, 0, s[6:7]
	v_cmp_ne_u32_e64 s[6:7], 1, v12
	v_cmp_gt_f32_e64 s[8:9], v17, v1
	s_and_b64 s[6:7], s[6:7], s[8:9]
	v_cndmask_b32_e64 v1, v1, v17, s[6:7]
	v_cndmask_b32_e64 v16, 0, 1, s[6:7]
	v_cndmask_b32_e64 v13, v13, v21, s[6:7]
	v_cmp_ne_u32_e64 s[6:7], 2, v12
	v_cmp_gt_f32_e64 s[8:9], v67, v1
	s_and_b64 s[6:7], s[6:7], s[8:9]
	v_cndmask_b32_e64 v1, v1, v67, s[6:7]
	v_cndmask_b32_e64 v16, v16, 2, s[6:7]
	v_cndmask_b32_e64 v0, v13, v0, s[6:7]
	v_cmp_gt_f32_e64 s[6:7], v65, v1
	s_and_b64 vcc, vcc, s[6:7]
	v_cndmask_b32_e32 v17, v1, v65, vcc
	v_cndmask_b32_e64 v1, v16, 3, vcc
	v_cndmask_b32_e32 v13, v0, v63, vcc
	v_cmp_gt_f32_e32 vcc, v73, v72
	v_add_f32_e32 v16, v71, v17
	s_nop 0
	v_cndmask_b32_e32 v17, v72, v73, vcc
	v_cmp_gt_f32_e64 s[6:7], v61, v17
	v_cndmask_b32_e64 v0, 0, 1, vcc
	s_nop 0
	v_cndmask_b32_e64 v20, v17, v61, s[6:7]
	v_cndmask_b32_e64 v0, v0, 2, s[6:7]
	v_cmp_ngt_f32_e64 s[8:9], v69, v20
	s_nop 1
	v_cndmask_b32_e64 v17, 3, v0, s[8:9]
	v_cmp_eq_u32_e64 s[10:11], 0, v17
	s_or_b64 s[10:11], s[10:11], s[12:13]
	v_cndmask_b32_e64 v0, v69, v20, s[8:9]
	v_cndmask_b32_e64 v20, v72, v153, s[10:11]
	v_cmp_ne_u32_e64 s[12:13], 1, v17
	v_cmp_gt_f32_e64 s[14:15], v73, v20
	s_and_b64 s[12:13], s[12:13], s[14:15]
	v_cndmask_b32_e64 v20, v20, v73, s[12:13]
	v_cmp_ne_u32_e64 s[14:15], 2, v17
	v_cmp_gt_f32_e64 s[16:17], v61, v20
	s_and_b64 s[14:15], s[14:15], s[16:17]
	v_cndmask_b32_e64 v20, v20, v61, s[14:15]
	v_cmp_gt_f32_e64 s[16:17], v69, v20
	s_and_b64 s[16:17], s[8:9], s[16:17]
	s_nop 0
	v_cndmask_b32_e64 v20, v20, v69, s[16:17]
	v_add_f32_e32 v20, v0, v20
	v_cmp_gt_f32_e64 s[18:19], v20, v16
	s_and_saveexec_b64 s[56:57], s[18:19]
	s_cbranch_execz .LBB0_525
	v_cndmask_b32_e64 v0, 4, 5, s[12:13]
	v_cndmask_b32_e64 v0, v0, 6, s[14:15]
	v_cndmask_b32_e64 v1, v0, 7, s[16:17]
	v_cndmask_b32_e64 v0, v18, 0, s[10:11]
	v_cndmask_b32_e64 v0, v0, v19, s[12:13]
	v_cndmask_b32_e64 v0, v0, v32, s[14:15]
	v_cndmask_b32_e64 v13, v0, v34, s[16:17]
	v_cndmask_b32_e32 v0, v18, v19, vcc
	v_cndmask_b32_e64 v0, v0, v32, s[6:7]
	v_or_b32_e32 v12, 4, v17
	v_cndmask_b32_e64 v3, v34, v0, s[8:9]
	v_mov_b32_e32 v16, v20

; template <bool COMBINE, bool ROUTE, bool FINAL, bool OUT8 = false, bool DUMMY = false> ...
;     ...
;         float ss = 0.f;
; #pragma unroll
;         for (int j = 0; j < 8; ++j) ss += xv[j].x * xv[j].x + xv[j].y * xv[j].y + xv[j].z * xv[j].z + xv[j].w * xv[j].w;
;         ss = wave_sum(ss);
;         const float rstd = 1.0f / sqrtf(ss * (1.f / D) + EPS);
;         if (FINAL) {
; #pragma unroll
;             for (int j = 0; j < 8; ++j) { const int c = 4 * lane + 256 * j; const f32x4 gv = *(const f32x4*)(g + c); *(f32x4*)(fout + (size_t)m * D + c) = xv[j] * rstd * gv; }
;         } else {
;             const float* sh = modl + (size_t)b * 12288 + sh_off; const float* sc = modl + (size_t)b * 12288 + sc_off;
; #pragma unroll
;             for (int j = 0; j < 8; ++j) {
;                 const int c = 4 * lane + 256 * j;
;                 const f32x4 gv = *(const f32x4*)(g + c), shv = *(const f32x4*)(sh + c), scv = *(const f32x4*)(sc + c);
.LBB0_1109:
	s_waitcnt vmcnt(7)
	v_mul_f32_e32 v0, v33, v33
	s_waitcnt vmcnt(6)
	v_mul_f32_e32 v1, v29, v29
	v_fmac_f32_e32 v0, v32, v32
	v_fmac_f32_e32 v1, v28, v28
	v_fmac_f32_e32 v0, v34, v34
	v_fmac_f32_e32 v1, v30, v30
	v_fmac_f32_e32 v0, v35, v35
	v_fmac_f32_e32 v1, v31, v31
	v_add_f32_e32 v0, v0, v1
	s_waitcnt vmcnt(5)
	v_mul_f32_e32 v1, v25, v25
	v_fmac_f32_e32 v1, v24, v24
	v_fmac_f32_e32 v1, v26, v26
	v_fmac_f32_e32 v1, v27, v27
	v_add_f32_e32 v0, v0, v1
	s_waitcnt vmcnt(4)
	v_mul_f32_e32 v1, v21, v21
	v_fmac_f32_e32 v1, v20, v20
	v_fmac_f32_e32 v1, v22, v22
	v_fmac_f32_e32 v1, v23, v23
	v_add_f32_e32 v0, v0, v1
	s_waitcnt vmcnt(3)
	v_mul_f32_e32 v1, v17, v17
	v_fmac_f32_e32 v1, v16, v16
	v_fmac_f32_e32 v1, v18, v18
	v_fmac_f32_e32 v1, v19, v19
	v_add_f32_e32 v0, v0, v1
	s_waitcnt vmcnt(2)
	v_mul_f32_e32 v1, v13, v13
	v_fmac_f32_e32 v1, v12, v12
	v_fmac_f32_e32 v1, v14, v14
	v_fmac_f32_e32 v1, v15, v15
	s_waitcnt vmcnt(1)
	v_mov_b32_e32 v74, v9
	s_waitcnt vmcnt(0)
	v_mov_b32_e32 v75, v5
	v_add_f32_e32 v59, v0, v1
	v_mov_b32_e32 v0, v8
	v_mov_b32_e32 v1, v4
	v_pk_mul_f32 v[74:75], v[74:75], v[74:75]
	v_lshl_add_u64 v[76:77], v[72:73], 0, s[52:53]
	v_pk_fma_f32 v[0:1], v[0:1], v[0:1], v[74:75]
	v_mov_b32_e32 v74, v10
	v_mov_b32_e32 v75, v6
	v_pk_fma_f32 v[0:1], v[74:75], v[74:75], v[0:1]
	v_mov_b32_e32 v74, v11
	v_mov_b32_e32 v75, v7
	v_pk_fma_f32 v[0:1], v[74:75], v[74:75], v[0:1]
	v_lshl_add_u64 v[74:75], v[72:73], 0, s[50:51]
	v_lshl_add_u64 v[72:73], v[74:75], 0, v[40:41]
	v_lshl_add_u64 v[158:159], v[76:77], 0, v[40:41]
	global_load_dwordx4 v[150:153], v[44:45], off
	global_load_dwordx4 v[154:157], v[72:73], off
	s_nop 0
	global_load_dwordx4 v[158:161], v[158:159], off
	global_load_dwordx4 v[162:165], v[44:45], off offset:1024
	v_mov_b32_e32 v166, v58
	v_mov_b32_e32 v167, 0
	v_lshl_add_u64 v[166:167], v[76:77], 0, v[166:167]
	global_load_dwordx4 v[166:169], v[166:167], off
	v_mov_b32_e32 v170, v58
	v_mov_b32_e32 v171, 0
	v_lshl_add_u64 v[170:171], v[74:75], 0, v[170:171]
	global_load_dwordx4 v[170:173], v[170:171], off
	global_load_dwordx4 v[174:177], v[44:45], off offset:2048
	v_mov_b32_e32 v178, v60
	v_mov_b32_e32 v179, 0
	v_lshl_add_u64 v[178:179], v[76:77], 0, v[178:179]
	global_load_dwordx4 v[178:181], v[178:179], off
	v_mov_b32_e32 v188, v60
	v_mov_b32_e32 v189, 0
	v_lshl_add_u64 v[188:189], v[74:75], 0, v[188:189]
	global_load_dwordx4 v[188:191], v[188:189], off
	global_load_dwordx4 v[192:195], v[44:45], off offset:3072
	v_mov_b32_e32 v196, v62
	v_mov_b32_e32 v197, 0
	v_lshl_add_u64 v[196:197], v[76:77], 0, v[196:197]
	global_load_dwordx4 v[196:199], v[196:197], off
	v_mov_b32_e32 v200, v62
	v_mov_b32_e32 v201, 0
	v_lshl_add_u64 v[200:201], v[74:75], 0, v[200:201]
	global_load_dwordx4 v[200:203], v[200:201], off
	global_load_dwordx4 v[204:207], v[46:47], off
	v_mov_b32_e32 v208, v64
	v_mov_b32_e32 v209, 0
	v_lshl_add_u64 v[208:209], v[76:77], 0, v[208:209]
	global_load_dwordx4 v[208:211], v[208:209], off
	v_mov_b32_e32 v212, v64
	v_mov_b32_e32 v213, 0
	v_lshl_add_u64 v[212:213], v[74:75], 0, v[212:213]
	global_load_dwordx4 v[212:215], v[212:213], off
	global_load_dwordx4 v[216:219], v[48:49], off
	v_mov_b32_e32 v220, v66
	v_mov_b32_e32 v221, 0
	v_lshl_add_u64 v[220:221], v[76:77], 0, v[220:221]
	global_load_dwordx4 v[220:223], v[220:221], off
	v_mov_b32_e32 v224, v66
	v_mov_b32_e32 v225, 0
	v_lshl_add_u64 v[224:225], v[74:75], 0, v[224:225]
	global_load_dwordx4 v[224:227], v[224:225], off
	global_load_dwordx4 v[228:231], v[50:51], off
	v_mov_b32_e32 v246, v68
	v_mov_b32_e32 v247, 0
	v_lshl_add_u64 v[246:247], v[76:77], 0, v[246:247]
	global_load_dwordx4 v[246:249], v[246:247], off
	v_mov_b32_e32 v250, v68
	v_mov_b32_e32 v251, 0
	v_lshl_add_u64 v[250:251], v[74:75], 0, v[250:251]
	global_load_dwordx4 v[250:253], v[250:251], off
	global_load_dwordx4 v[232:235], v[52:53], off
	v_mov_b32_e32 v236, v70
	v_mov_b32_e32 v237, 0
	v_lshl_add_u64 v[236:237], v[74:75], 0, v[236:237]
	global_load_dwordx4 v[236:239], v[236:237], off
	v_mov_b32_e32 v242, v70
	v_mov_b32_e32 v243, 0
	v_lshl_add_u64 v[242:243], v[76:77], 0, v[242:243]
	global_load_dwordx4 v[242:245], v[242:243], off
	v_add_f32_e32 v0, v59, v0
	v_add_f32_e32 v0, v0, v1
	ds_bpermute_b32 v1, v182, v0
	v_mov_b32_e32 v65, v41
	v_mov_b32_e32 v67, v41
	v_mov_b32_e32 v69, v41
	v_mov_b32_e32 v71, v41
	s_waitcnt lgkmcnt(0)
	v_add_f32_e32 v0, v0, v1
	ds_bpermute_b32 v1, v183, v0
	s_waitcnt lgkmcnt(0)
	v_add_f32_e32 v0, v0, v1
	ds_bpermute_b32 v1, v184, v0
	s_waitcnt lgkmcnt(0)
	v_add_f32_e32 v0, v0, v1
	ds_bpermute_b32 v1, v185, v0
	s_waitcnt lgkmcnt(0)
	v_add_f32_e32 v0, v0, v1
	ds_bpermute_b32 v1, v186, v0
	s_waitcnt lgkmcnt(0)
	v_add_f32_e32 v0, v0, v1
	ds_bpermute_b32 v1, v187, v0
	s_waitcnt lgkmcnt(0)
	v_add_f32_e32 v0, v0, v1
	v_fmamk_f32 v0, v0, 0x3a000000, v39
	v_mul_f32_e32 v1, 0x4f800000, v0
	v_cmp_gt_f32_e32 vcc, s3, v0
	s_waitcnt vmcnt(0)
; __device__ __forceinline__ unsigned pk2(float a, float b) { f32x2 v = {a, b}; bf16x2_t r = __builtin_convertvector(v, bf16x2_t); return __builtin_bit_cast(unsigned, r); }
; __device__ __forceinline__ unsigned pk4_fp8(float a, float b, float c, float d) { unsigned w = 0u; w = __builtin_amdgcn_cvt_pk_fp8_f32(a, b, w, false); w = __builtin_amdgcn_cvt_pk_fp8_f32(c, d, w, true); return w; }
; template <bool COMBINE, bool ROUTE, bool FINAL, bool OUT8 = false, bool DUMMY = false> ...
;     ...
;         const float rstd = 1.0f / sqrtf(ss * (1.f / D) + EPS);
;         if (FINAL) {
; #pragma unroll
;             for (int j = 0; j < 8; ++j) { const int c = 4 * lane + 256 * j; const f32x4 gv = *(const f32x4*)(g + c); *(f32x4*)(fout + (size_t)m * D + c) = xv[j] * rstd * gv; }
;         } else {
;             const float* sh = modl + (size_t)b * 12288 + sh_off; const float* sc = modl + (size_t)b * 12288 + sc_off;
; #pragma unroll
;             for (int j = 0; j < 8; ++j) {
;                 const int c = 4 * lane + 256 * j;
;                 const f32x4 gv = *(const f32x4*)(g + c), shv = *(const f32x4*)(sh + c), scv = *(const f32x4*)(sc + c);
;                 xv[j] = xv[j] * rstd * gv * (1.f + scv) + shv;
;                 if (OUT8) *(unsigned*)((unsigned char*)hout + (size_t)m * D + c) = pk4_fp8(xv[j].x * F8_SA, xv[j].y * F8_SA, xv[j].z * F8_SA, xv[j].w * F8_SA);
;                 else { u32x2 o; o.x = pk2(xv[j].x, xv[j].y); o.y = pk2(xv[j].z, xv[j].w); *(u32x2*)(hout + (size_t)m * D + c) = o; }
;             }
	v_pk_add_f32 v[72:73], v[158:159], 1.0 op_sel_hi:[1,0]
	v_cndmask_b32_e32 v0, v0, v1, vcc
	v_sqrt_f32_e32 v1, v0
	s_nop 0
	v_add_u32_e32 v40, -1, v1
	v_fma_f32 v59, -v40, v1, v0
	v_cmp_ge_f32_e64 s[8:9], 0, v59
	v_add_u32_e32 v59, 1, v1
	s_nop 0
	v_cndmask_b32_e64 v40, v1, v40, s[8:9]
	v_fma_f32 v1, -v59, v1, v0
	v_cmp_lt_f32_e64 s[8:9], 0, v1
	s_nop 1
	v_cndmask_b32_e64 v1, v40, v59, s[8:9]
	v_mul_f32_e32 v40, 0x37800000, v1
	v_cndmask_b32_e32 v1, v1, v40, vcc
	v_cmp_class_f32_e32 vcc, v0, v144
	s_nop 1
	v_cndmask_b32_e32 v0, v1, v0, vcc
	v_div_scale_f32 v1, s[8:9], v0, v0, 1.0
	v_rcp_f32_e32 v40, v1
	s_nop 0
	v_fma_f32 v59, -v1, v40, 1.0
	v_fmac_f32_e32 v40, v59, v40
	v_div_scale_f32 v59, vcc, 1.0, v0, 1.0
	v_mul_f32_e32 v61, v59, v40
	v_fma_f32 v63, -v1, v61, v59
	v_fmac_f32_e32 v61, v63, v40
	v_fma_f32 v1, -v1, v61, v59
	v_div_fmas_f32 v1, v1, v40, v61
	v_div_fixup_f32 v40, v1, v0, 1.0
	v_pk_mul_f32 v[32:33], v[32:33], v[40:41] op_sel_hi:[1,0]
	v_mov_b32_e32 v59, v41
	v_pk_mul_f32 v[32:33], v[150:151], v[32:33]
	v_pk_mul_f32 v[0:1], v[34:35], v[40:41] op_sel_hi:[1,0]
	v_pk_fma_f32 v[72:73], v[72:73], v[32:33], v[154:155]
	v_pk_mul_f32 v[0:1], v[152:153], v[0:1]
	v_mul_f32_e32 v32, 0x41800000, v72
	v_mul_f32_e32 v33, 0x41800000, v73
	v_cvt_pk_fp8_f32 v59, v32, v33
	v_pk_add_f32 v[34:35], v[160:161], 1.0 op_sel_hi:[1,0]
	v_pk_mul_f32 v[28:29], v[28:29], v[40:41] op_sel_hi:[1,0]
	v_pk_fma_f32 v[32:33], v[34:35], v[0:1], v[156:157]
	v_mov_b32_e32 v61, v41
	v_mul_f32_e32 v0, 0x41800000, v32
	v_mul_f32_e32 v1, 0x41800000, v33
	v_cvt_pk_fp8_f32 v59, v0, v1 op_sel:[0,0,1]
	v_lshlrev_b64 v[0:1], 11, v[2:3]
	v_lshl_add_u64 v[34:35], v[56:57], 0, v[0:1]
	v_mov_b32_e32 v3, v41
	global_store_dword v[34:35], v59, off
	v_mov_b32_e32 v59, v41
	v_lshl_add_u64 v[0:1], v[76:77], 0, v[58:59]
	v_lshl_add_u64 v[0:1], v[74:75], 0, v[58:59]
	v_pk_mul_f32 v[0:1], v[30:31], v[40:41] op_sel_hi:[1,0]
	v_pk_mul_f32 v[24:25], v[24:25], v[40:41] op_sel_hi:[1,0]
	v_mov_b32_e32 v63, v41
	v_pk_mul_f32 v[20:21], v[20:21], v[40:41] op_sel_hi:[1,0]
	v_pk_mul_f32 v[16:17], v[16:17], v[40:41] op_sel_hi:[1,0]
	v_pk_mul_f32 v[12:13], v[12:13], v[40:41] op_sel_hi:[1,0]
	v_pk_mul_f32 v[8:9], v[8:9], v[40:41] op_sel_hi:[1,0]
	v_pk_mul_f32 v[6:7], v[6:7], v[40:41] op_sel_hi:[1,0]
	v_pk_mul_f32 v[4:5], v[4:5], v[40:41] op_sel_hi:[1,0]
	v_pk_mul_f32 v[28:29], v[162:163], v[28:29]
	v_pk_add_f32 v[30:31], v[166:167], 1.0 op_sel_hi:[1,0]
	v_pk_mul_f32 v[0:1], v[164:165], v[0:1]
	v_pk_fma_f32 v[30:31], v[30:31], v[28:29], v[170:171]
	v_pk_add_f32 v[150:151], v[168:169], 1.0 op_sel_hi:[1,0]
	v_mul_f32_e32 v28, 0x41800000, v30
	v_mul_f32_e32 v29, 0x41800000, v31
	v_cvt_pk_fp8_f32 v3, v28, v29
	v_pk_fma_f32 v[28:29], v[150:151], v[0:1], v[172:173]
	s_nop 0
	v_mul_f32_e32 v0, 0x41800000, v28
	v_mul_f32_e32 v1, 0x41800000, v29
	v_cvt_pk_fp8_f32 v3, v0, v1 op_sel:[0,0,1]
	v_lshl_add_u64 v[0:1], v[76:77], 0, v[60:61]
	global_store_dword v[34:35], v3, off offset:256
	v_lshl_add_u64 v[0:1], v[74:75], 0, v[60:61]
	v_pk_mul_f32 v[0:1], v[26:27], v[40:41] op_sel_hi:[1,0]
	v_mov_b32_e32 v3, v41
	v_pk_mul_f32 v[24:25], v[174:175], v[24:25]
	v_pk_add_f32 v[26:27], v[178:179], 1.0 op_sel_hi:[1,0]
	v_pk_mul_f32 v[0:1], v[176:177], v[0:1]
	v_pk_fma_f32 v[26:27], v[24:25], v[26:27], v[188:189]
	v_pk_add_f32 v[150:151], v[180:181], 1.0 op_sel_hi:[1,0]
	v_mul_f32_e32 v24, 0x41800000, v26
	v_mul_f32_e32 v25, 0x41800000, v27
	v_cvt_pk_fp8_f32 v3, v24, v25
	v_pk_fma_f32 v[24:25], v[0:1], v[150:151], v[190:191]
	s_nop 0
	v_mul_f32_e32 v0, 0x41800000, v24
	v_mul_f32_e32 v1, 0x41800000, v25
	v_cvt_pk_fp8_f32 v3, v0, v1 op_sel:[0,0,1]
	v_lshl_add_u64 v[0:1], v[76:77], 0, v[62:63]
	global_store_dword v[34:35], v3, off offset:512
	v_lshl_add_u64 v[0:1], v[74:75], 0, v[62:63]
	v_pk_mul_f32 v[0:1], v[22:23], v[40:41] op_sel_hi:[1,0]
	v_mov_b32_e32 v3, v41
	v_pk_mul_f32 v[20:21], v[20:21], v[192:193]
	v_pk_add_f32 v[22:23], v[196:197], 1.0 op_sel_hi:[1,0]
	v_pk_mul_f32 v[0:1], v[0:1], v[194:195]
	v_pk_fma_f32 v[22:23], v[20:21], v[22:23], v[200:201]
	v_pk_add_f32 v[150:151], v[198:199], 1.0 op_sel_hi:[1,0]
	v_mul_f32_e32 v20, 0x41800000, v22
	v_mul_f32_e32 v21, 0x41800000, v23
	v_cvt_pk_fp8_f32 v3, v20, v21
	v_pk_fma_f32 v[20:21], v[0:1], v[150:151], v[202:203]
	s_nop 0
	v_mul_f32_e32 v0, 0x41800000, v20
	v_mul_f32_e32 v1, 0x41800000, v21
	v_cvt_pk_fp8_f32 v3, v0, v1 op_sel:[0,0,1]
	v_lshl_add_u64 v[0:1], v[76:77], 0, v[64:65]
	global_store_dword v[34:35], v3, off offset:768
	v_lshl_add_u64 v[0:1], v[74:75], 0, v[64:65]
	v_pk_mul_f32 v[0:1], v[18:19], v[40:41] op_sel_hi:[1,0]
	v_mov_b32_e32 v3, v41
	v_pk_mul_f32 v[16:17], v[16:17], v[204:205]
	v_pk_add_f32 v[18:19], v[208:209], 1.0 op_sel_hi:[1,0]
	v_pk_mul_f32 v[0:1], v[0:1], v[206:207]
	v_pk_fma_f32 v[18:19], v[16:17], v[18:19], v[212:213]
	v_pk_add_f32 v[150:151], v[210:211], 1.0 op_sel_hi:[1,0]
	v_mul_f32_e32 v16, 0x41800000, v18
	v_mul_f32_e32 v17, 0x41800000, v19
	v_cvt_pk_fp8_f32 v3, v16, v17
	v_pk_fma_f32 v[16:17], v[0:1], v[150:151], v[214:215]
	s_nop 0
	v_mul_f32_e32 v0, 0x41800000, v16
	v_mul_f32_e32 v1, 0x41800000, v17
	v_cvt_pk_fp8_f32 v3, v0, v1 op_sel:[0,0,1]
	v_lshl_add_u64 v[0:1], v[76:77], 0, v[66:67]
	global_store_dword v[34:35], v3, off offset:1024
	v_lshl_add_u64 v[0:1], v[74:75], 0, v[66:67]
	v_pk_mul_f32 v[0:1], v[14:15], v[40:41] op_sel_hi:[1,0]
	v_mov_b32_e32 v3, v41
	v_pk_mul_f32 v[12:13], v[12:13], v[216:217]
	v_pk_add_f32 v[14:15], v[220:221], 1.0 op_sel_hi:[1,0]
	v_pk_mul_f32 v[0:1], v[0:1], v[218:219]
	v_pk_fma_f32 v[14:15], v[12:13], v[14:15], v[224:225]
	v_pk_add_f32 v[150:151], v[222:223], 1.0 op_sel_hi:[1,0]
	v_mul_f32_e32 v12, 0x41800000, v14
; __device__ __forceinline__ unsigned pk2(float a, float b) { f32x2 v = {a, b}; bf16x2_t r = __builtin_convertvector(v, bf16x2_t); return __builtin_bit_cast(unsigned, r); }
; __device__ __forceinline__ unsigned pk4_fp8(float a, float b, float c, float d) { unsigned w = 0u; w = __builtin_amdgcn_cvt_pk_fp8_f32(a, b, w, false); w = __builtin_amdgcn_cvt_pk_fp8_f32(c, d, w, true); return w; }
; template <bool COMBINE, bool ROUTE, bool FINAL, bool OUT8 = false, bool DUMMY = false> ...
;     ...
;             const float* sh = modl + (size_t)b * 12288 + sh_off; const float* sc = modl + (size_t)b * 12288 + sc_off;
; #pragma unroll
;             for (int j = 0; j < 8; ++j) {
;                 const int c = 4 * lane + 256 * j;
;                 const f32x4 gv = *(const f32x4*)(g + c), shv = *(const f32x4*)(sh + c), scv = *(const f32x4*)(sc + c);
;                 xv[j] = xv[j] * rstd * gv * (1.f + scv) + shv;
;                 if (OUT8) *(unsigned*)((unsigned char*)hout + (size_t)m * D + c) = pk4_fp8(xv[j].x * F8_SA, xv[j].y * F8_SA, xv[j].z * F8_SA, xv[j].w * F8_SA);
;                 else { u32x2 o; o.x = pk2(xv[j].x, xv[j].y); o.y = pk2(xv[j].z, xv[j].w); *(u32x2*)(hout + (size_t)m * D + c) = o; }
;             }
;             if (ROUTE) {
;                 float lg[16];
; #pragma unroll
;                 for (int e = 0; e < 16; ++e) lg[e] = 0.f;
; #pragma unroll
;                 for (int j = 0; j < 8; ++j) {
; #pragma unroll
;                     for (int cc = 0; cc < 4; ++cc) {
;                         const float hv = xv[j][cc];
;                         const f32x4 w0 = WT[((j * 4 + cc) * 4 + 0) * 64 + lane], w1 = WT[((j * 4 + cc) * 4 + 1) * 64 + lane], w2 = WT[((j * 4 + cc) * 4 + 2) * 64 + lane], w3 = WT[((j * 4 + cc) * 4 + 3) * 64 + lane];
;                         lg[0] += hv * w0.x; lg[1] += hv * w0.y; lg[2] += hv * w0.z; lg[3] += hv * w0.w;
;                         lg[4] += hv * w1.x; lg[5] += hv * w1.y; lg[6] += hv * w1.z; lg[7] += hv * w1.w;
;                         lg[8] += hv * w2.x; lg[9] += hv * w2.y; lg[10] += hv * w2.z; lg[11] += hv * w2.w;
;                         lg[12] += hv * w3.x; lg[13] += hv * w3.y; lg[14] += hv * w3.z; lg[15] += hv * w3.w;
	v_mul_f32_e32 v13, 0x41800000, v15
	v_cvt_pk_fp8_f32 v3, v12, v13
	v_pk_fma_f32 v[12:13], v[0:1], v[150:151], v[226:227]
	s_nop 0
	v_mul_f32_e32 v0, 0x41800000, v12
	v_mul_f32_e32 v1, 0x41800000, v13
	v_cvt_pk_fp8_f32 v3, v0, v1 op_sel:[0,0,1]
	v_lshl_add_u64 v[0:1], v[76:77], 0, v[68:69]
	global_store_dword v[34:35], v3, off offset:1280
	v_lshl_add_u64 v[0:1], v[74:75], 0, v[68:69]
	v_pk_mul_f32 v[0:1], v[10:11], v[40:41] op_sel_hi:[1,0]
	v_mov_b32_e32 v3, v41
	v_pk_mul_f32 v[8:9], v[8:9], v[228:229]
	v_pk_add_f32 v[10:11], v[246:247], 1.0 op_sel_hi:[1,0]
	v_pk_mul_f32 v[0:1], v[0:1], v[230:231]
	v_pk_fma_f32 v[10:11], v[8:9], v[10:11], v[250:251]
	v_pk_add_f32 v[150:151], v[248:249], 1.0 op_sel_hi:[1,0]
	v_mul_f32_e32 v8, 0x41800000, v10
	v_mul_f32_e32 v9, 0x41800000, v11
	v_cvt_pk_fp8_f32 v3, v8, v9
	v_pk_fma_f32 v[8:9], v[0:1], v[150:151], v[252:253]
	v_mov_b32_e32 v151, v41
	v_mul_f32_e32 v0, 0x41800000, v8
	v_mul_f32_e32 v1, 0x41800000, v9
	v_cvt_pk_fp8_f32 v3, v0, v1 op_sel:[0,0,1]
	v_lshl_add_u64 v[0:1], v[74:75], 0, v[70:71]
	v_lshl_add_u64 v[74:75], v[76:77], 0, v[70:71]
	global_store_dword v[34:35], v3, off offset:1536
	ds_read_b128 v[74:77], v78
	ds_read_b128 v[164:167], v78 offset:1024
	ds_read_b128 v[168:171], v78 offset:2048
	ds_read_b128 v[172:175], v78 offset:3072
	ds_read_b128 v[176:179], v78 offset:4096
	ds_read_b128 v[188:191], v78 offset:5120
	ds_read_b128 v[192:195], v78 offset:6144
	ds_read_b128 v[196:199], v78 offset:7168
	ds_read_b128 v[200:203], v78 offset:8192
	ds_read_b128 v[204:207], v78 offset:9216
	ds_read_b128 v[208:211], v78 offset:10240
	ds_read_b128 v[212:215], v78 offset:11264
	ds_read_b128 v[216:219], v78 offset:12288
	ds_read_b128 v[220:223], v78 offset:13312
	ds_read_b128 v[224:227], v78 offset:14336
	ds_read_b128 v[228:231], v78 offset:15360
	s_waitcnt lgkmcnt(14)
	v_fma_f32 v150, v72, v74, 0
	v_fma_f32 v149, v72, v75, 0
	v_fma_f32 v67, v72, v76, 0
	v_fma_f32 v65, v72, v77, 0
	v_fma_f32 v77, v72, v164, 0
	v_fma_f32 v76, v72, v165, 0
	v_fma_f32 v63, v72, v166, 0
	v_fma_f32 v61, v72, v167, 0
	s_waitcnt lgkmcnt(13)
	v_fma_f32 v75, v72, v168, 0
	v_fma_f32 v74, v72, v169, 0
	v_fma_f32 v59, v72, v170, 0
	v_fma_f32 v40, v72, v171, 0
	s_waitcnt lgkmcnt(12)
	v_fma_f32 v71, v72, v172, 0
	v_fma_f32 v69, v72, v173, 0
	v_fma_f32 v3, v72, v174, 0
	v_fma_f32 v1, v72, v175, 0
	s_waitcnt lgkmcnt(11)
	v_fmac_f32_e32 v150, v73, v176
	v_fmac_f32_e32 v149, v73, v177
	v_fmac_f32_e32 v67, v73, v178
	v_fmac_f32_e32 v65, v73, v179
	s_waitcnt lgkmcnt(10)
	v_fmac_f32_e32 v77, v73, v188
	v_fmac_f32_e32 v76, v73, v189
	v_fmac_f32_e32 v63, v73, v190
	v_fmac_f32_e32 v61, v73, v191
	s_waitcnt lgkmcnt(9)
	v_fmac_f32_e32 v75, v73, v192
	v_fmac_f32_e32 v74, v73, v193
	v_fmac_f32_e32 v59, v73, v194
	v_fmac_f32_e32 v40, v73, v195
	s_waitcnt lgkmcnt(8)
	v_fmac_f32_e32 v71, v73, v196
	v_fmac_f32_e32 v69, v73, v197
	v_fmac_f32_e32 v3, v73, v198
	v_fmac_f32_e32 v1, v73, v199
	s_waitcnt lgkmcnt(7)
	v_fmac_f32_e32 v150, v32, v200
	v_fmac_f32_e32 v149, v32, v201
	v_fmac_f32_e32 v67, v32, v202
	v_fmac_f32_e32 v65, v32, v203
	s_waitcnt lgkmcnt(6)
	v_fmac_f32_e32 v77, v32, v204
	v_fmac_f32_e32 v76, v32, v205
	v_fmac_f32_e32 v63, v32, v206
	v_fmac_f32_e32 v61, v32, v207
	s_waitcnt lgkmcnt(5)
	v_fmac_f32_e32 v75, v32, v208
	v_fmac_f32_e32 v74, v32, v209
	v_fmac_f32_e32 v59, v32, v210
	v_fmac_f32_e32 v40, v32, v211
	s_waitcnt lgkmcnt(4)
	v_fmac_f32_e32 v71, v32, v212
	v_fmac_f32_e32 v69, v32, v213
	v_fmac_f32_e32 v3, v32, v214
	v_fmac_f32_e32 v1, v32, v215
	s_waitcnt lgkmcnt(1)
	v_fmac_f32_e32 v59, v33, v226
	v_fmac_f32_e32 v40, v33, v227
	s_waitcnt lgkmcnt(0)
	v_fmac_f32_e32 v3, v33, v230
	v_fmac_f32_e32 v1, v33, v231
	v_fmac_f32_e32 v150, v33, v216
	v_fmac_f32_e32 v149, v33, v217
	v_fmac_f32_e32 v67, v33, v218
	v_fmac_f32_e32 v65, v33, v219
	v_fmac_f32_e32 v77, v33, v220
	v_fmac_f32_e32 v76, v33, v221
	v_fmac_f32_e32 v63, v33, v222
	v_fmac_f32_e32 v61, v33, v223
	v_fmac_f32_e32 v75, v33, v224
	v_fmac_f32_e32 v74, v33, v225
	v_fmac_f32_e32 v71, v33, v228
	v_fmac_f32_e32 v69, v33, v229
	v_pk_mul_f32 v[4:5], v[4:5], v[232:233]
	v_pk_mul_f32 v[72:73], v[6:7], v[234:235]
	v_pk_add_f32 v[6:7], v[242:243], 1.0 op_sel_hi:[1,0]
	v_pk_add_f32 v[152:153], v[244:245], 1.0 op_sel_hi:[1,0]
	v_pk_fma_f32 v[6:7], v[4:5], v[6:7], v[236:237]
	s_nop 0
	v_mul_f32_e32 v0, 0x41800000, v6
	v_mul_f32_e32 v4, 0x41800000, v7
	v_cvt_pk_fp8_f32 v151, v0, v4
	v_pk_fma_f32 v[4:5], v[72:73], v[152:153], v[238:239]
	s_nop 0
	v_mul_f32_e32 v0, 0x41800000, v4
	v_mul_f32_e32 v32, 0x41800000, v5
	v_cvt_pk_fp8_f32 v151, v0, v32 op_sel:[0,0,1]
	global_store_dword v[34:35], v151, off offset:1792
	ds_read_b128 v[32:35], v78 offset:16384
	ds_read_b128 v[152:155], v78 offset:17408
	ds_read_b128 v[156:159], v78 offset:18432
	ds_read_b128 v[160:163], v78 offset:19456
	s_waitcnt lgkmcnt(3)
	v_fmac_f32_e32 v150, v30, v32
	v_fmac_f32_e32 v149, v30, v33
	v_fmac_f32_e32 v67, v30, v34
	v_fmac_f32_e32 v65, v30, v35
	s_waitcnt lgkmcnt(2)
	v_fmac_f32_e32 v77, v30, v152
	v_fmac_f32_e32 v76, v30, v153
	v_fmac_f32_e32 v63, v30, v154
	v_fmac_f32_e32 v61, v30, v155
	s_waitcnt lgkmcnt(1)
	v_fmac_f32_e32 v75, v30, v156
	v_fmac_f32_e32 v74, v30, v157
	v_fmac_f32_e32 v59, v30, v158
	v_fmac_f32_e32 v40, v30, v159
	s_waitcnt lgkmcnt(0)
	v_fmac_f32_e32 v71, v30, v160
	v_fmac_f32_e32 v69, v30, v161
	v_fmac_f32_e32 v3, v30, v162
	ds_read_b128 v[32:35], v78 offset:20480
	v_fmac_f32_e32 v1, v30, v163
	ds_read_b128 v[152:155], v78 offset:21504
	ds_read_b128 v[156:159], v78 offset:22528
	ds_read_b128 v[160:163], v78 offset:23552
	s_waitcnt lgkmcnt(3)
; template <bool COMBINE, bool ROUTE, bool FINAL, bool OUT8 = false, bool DUMMY = false> ...
;     ...
;                 for (int j = 0; j < 8; ++j) {
; #pragma unroll
;                     for (int cc = 0; cc < 4; ++cc) {
;                         const float hv = xv[j][cc];
;                         const f32x4 w0 = WT[((j * 4 + cc) * 4 + 0) * 64 + lane], w1 = WT[((j * 4 + cc) * 4 + 1) * 64 + lane], w2 = WT[((j * 4 + cc) * 4 + 2) * 64 + lane], w3 = WT[((j * 4 + cc) * 4 + 3) * 64 + lane];
;                         lg[0] += hv * w0.x; lg[1] += hv * w0.y; lg[2] += hv * w0.z; lg[3] += hv * w0.w;
;                         lg[4] += hv * w1.x; lg[5] += hv * w1.y; lg[6] += hv * w1.z; lg[7] += hv * w1.w;
;                         lg[8] += hv * w2.x; lg[9] += hv * w2.y; lg[10] += hv * w2.z; lg[11] += hv * w2.w;
;                         lg[12] += hv * w3.x; lg[13] += hv * w3.y; lg[14] += hv * w3.z; lg[15] += hv * w3.w;
;                     }
	v_fmac_f32_e32 v150, v31, v32
	v_fmac_f32_e32 v149, v31, v33
	v_fmac_f32_e32 v67, v31, v34
	v_fmac_f32_e32 v65, v31, v35
	s_waitcnt lgkmcnt(2)
	v_fmac_f32_e32 v77, v31, v152
	v_fmac_f32_e32 v76, v31, v153
	v_fmac_f32_e32 v63, v31, v154
	v_fmac_f32_e32 v61, v31, v155
	s_waitcnt lgkmcnt(1)
	v_fmac_f32_e32 v75, v31, v156
	v_fmac_f32_e32 v74, v31, v157
	v_fmac_f32_e32 v59, v31, v158
	v_fmac_f32_e32 v40, v31, v159
	s_waitcnt lgkmcnt(0)
	v_fmac_f32_e32 v71, v31, v160
	v_fmac_f32_e32 v69, v31, v161
	v_fmac_f32_e32 v3, v31, v162
	ds_read_b128 v[32:35], v78 offset:24576
	v_fmac_f32_e32 v1, v31, v163
	ds_read_b128 v[152:155], v78 offset:25600
	ds_read_b128 v[156:159], v78 offset:26624
	ds_read_b128 v[160:163], v78 offset:27648
	s_waitcnt lgkmcnt(3)
	v_fmac_f32_e32 v150, v28, v32
	v_fmac_f32_e32 v149, v28, v33
	s_waitcnt lgkmcnt(2)
	v_fmac_f32_e32 v77, v28, v152
	v_fmac_f32_e32 v76, v28, v153
	v_fmac_f32_e32 v63, v28, v154
	v_fmac_f32_e32 v61, v28, v155
	s_waitcnt lgkmcnt(1)
	v_fmac_f32_e32 v75, v28, v156
	v_fmac_f32_e32 v74, v28, v157
	v_fmac_f32_e32 v59, v28, v158
	v_fmac_f32_e32 v40, v28, v159
	s_waitcnt lgkmcnt(0)
	v_fmac_f32_e32 v71, v28, v160
	v_fmac_f32_e32 v69, v28, v161
	v_fmac_f32_e32 v3, v28, v162
	ds_read_b128 v[30:33], v78 offset:28672
	v_fmac_f32_e32 v1, v28, v163
	ds_read_b128 v[152:155], v78 offset:29696
	ds_read_b128 v[156:159], v78 offset:30720
	ds_read_b128 v[160:163], v78 offset:31744
	v_fmac_f32_e32 v67, v28, v34
	v_fmac_f32_e32 v65, v28, v35
	s_waitcnt lgkmcnt(3)
	v_fmac_f32_e32 v150, v29, v30
	s_waitcnt lgkmcnt(1)
	v_fmac_f32_e32 v59, v29, v158
	v_fmac_f32_e32 v40, v29, v159
	s_waitcnt lgkmcnt(0)
	v_fmac_f32_e32 v3, v29, v162
	v_fmac_f32_e32 v1, v29, v163
	v_fmac_f32_e32 v149, v29, v31
	v_fmac_f32_e32 v67, v29, v32
	v_fmac_f32_e32 v65, v29, v33
	v_fmac_f32_e32 v77, v29, v152
	v_fmac_f32_e32 v76, v29, v153
	v_fmac_f32_e32 v63, v29, v154
	v_fmac_f32_e32 v61, v29, v155
	v_fmac_f32_e32 v75, v29, v156
	v_fmac_f32_e32 v74, v29, v157
	v_fmac_f32_e32 v71, v29, v160
	v_fmac_f32_e32 v69, v29, v161
	ds_read_b128 v[28:31], v78 offset:32768
	ds_read_b128 v[32:35], v78 offset:33792
	ds_read_b128 v[152:155], v78 offset:34816
	ds_read_b128 v[156:159], v78 offset:35840
	s_waitcnt lgkmcnt(3)
	v_fmac_f32_e32 v150, v26, v28
	v_fmac_f32_e32 v149, v26, v29
	v_fmac_f32_e32 v67, v26, v30
	v_fmac_f32_e32 v65, v26, v31
	s_waitcnt lgkmcnt(2)
	v_fmac_f32_e32 v77, v26, v32
	v_fmac_f32_e32 v76, v26, v33
	v_fmac_f32_e32 v63, v26, v34
	v_fmac_f32_e32 v61, v26, v35
	s_waitcnt lgkmcnt(1)
	v_fmac_f32_e32 v75, v26, v152
	v_fmac_f32_e32 v74, v26, v153
	v_fmac_f32_e32 v59, v26, v154
	v_fmac_f32_e32 v40, v26, v155
	s_waitcnt lgkmcnt(0)
	v_fmac_f32_e32 v71, v26, v156
	v_fmac_f32_e32 v69, v26, v157
	v_fmac_f32_e32 v3, v26, v158
	ds_read_b128 v[28:31], v78 offset:36864
	v_fmac_f32_e32 v1, v26, v159
	ds_read_b128 v[32:35], v78 offset:37888
	ds_read_b128 v[152:155], v78 offset:38912
	ds_read_b128 v[156:159], v78 offset:39936
	s_waitcnt lgkmcnt(3)
	v_fmac_f32_e32 v150, v27, v28
	v_fmac_f32_e32 v149, v27, v29
	v_fmac_f32_e32 v67, v27, v30
	v_fmac_f32_e32 v65, v27, v31
	s_waitcnt lgkmcnt(2)
	v_fmac_f32_e32 v77, v27, v32
	v_fmac_f32_e32 v76, v27, v33
	v_fmac_f32_e32 v63, v27, v34
	v_fmac_f32_e32 v61, v27, v35
	s_waitcnt lgkmcnt(1)
	v_fmac_f32_e32 v75, v27, v152
	v_fmac_f32_e32 v74, v27, v153
	v_fmac_f32_e32 v59, v27, v154
	v_fmac_f32_e32 v40, v27, v155
	s_waitcnt lgkmcnt(0)
	v_fmac_f32_e32 v71, v27, v156
	v_fmac_f32_e32 v69, v27, v157
	v_fmac_f32_e32 v3, v27, v158
	ds_read_b128 v[28:31], v78 offset:40960
	v_fmac_f32_e32 v1, v27, v159
	ds_read_b128 v[32:35], v78 offset:41984
	ds_read_b128 v[152:155], v78 offset:43008
	ds_read_b128 v[156:159], v78 offset:44032
	s_waitcnt lgkmcnt(3)
	v_fmac_f32_e32 v150, v24, v28
	v_fmac_f32_e32 v149, v24, v29
	v_fmac_f32_e32 v67, v24, v30
	v_fmac_f32_e32 v65, v24, v31
	s_waitcnt lgkmcnt(2)
	v_fmac_f32_e32 v77, v24, v32
	v_fmac_f32_e32 v76, v24, v33
	s_waitcnt lgkmcnt(1)
	v_fmac_f32_e32 v75, v24, v152
	v_fmac_f32_e32 v74, v24, v153
	v_fmac_f32_e32 v59, v24, v154
	v_fmac_f32_e32 v40, v24, v155
	s_waitcnt lgkmcnt(0)
	v_fmac_f32_e32 v71, v24, v156
	v_fmac_f32_e32 v69, v24, v157
	v_fmac_f32_e32 v3, v24, v158
	ds_read_b128 v[26:29], v78 offset:45056
	v_fmac_f32_e32 v1, v24, v159
	ds_read_b128 v[30:33], v78 offset:46080
	ds_read_b128 v[152:155], v78 offset:47104
	ds_read_b128 v[156:159], v78 offset:48128
	v_fmac_f32_e32 v63, v24, v34
	v_fmac_f32_e32 v61, v24, v35
	s_waitcnt lgkmcnt(3)
	v_fmac_f32_e32 v150, v25, v26
	s_waitcnt lgkmcnt(1)
	v_fmac_f32_e32 v59, v25, v154
	v_fmac_f32_e32 v40, v25, v155
	s_waitcnt lgkmcnt(0)
	v_fmac_f32_e32 v3, v25, v158
	v_fmac_f32_e32 v1, v25, v159
	v_fmac_f32_e32 v149, v25, v27
	v_fmac_f32_e32 v67, v25, v28
	v_fmac_f32_e32 v65, v25, v29
	v_fmac_f32_e32 v77, v25, v30
	v_fmac_f32_e32 v76, v25, v31
	v_fmac_f32_e32 v63, v25, v32
	v_fmac_f32_e32 v61, v25, v33
	v_fmac_f32_e32 v75, v25, v152
	v_fmac_f32_e32 v74, v25, v153
	v_fmac_f32_e32 v71, v25, v156
	v_fmac_f32_e32 v69, v25, v157
	ds_read_b128 v[24:27], v78 offset:49152
	ds_read_b128 v[28:31], v78 offset:50176
	ds_read_b128 v[32:35], v78 offset:51200
	ds_read_b128 v[152:155], v78 offset:52224
	s_waitcnt lgkmcnt(3)
	v_fmac_f32_e32 v150, v22, v24
	v_fmac_f32_e32 v149, v22, v25
	v_fmac_f32_e32 v67, v22, v26
	v_fmac_f32_e32 v65, v22, v27
	s_waitcnt lgkmcnt(2)
	v_fmac_f32_e32 v77, v22, v28
	v_fmac_f32_e32 v76, v22, v29
	v_fmac_f32_e32 v63, v22, v30
	v_fmac_f32_e32 v61, v22, v31
	s_waitcnt lgkmcnt(1)
	v_fmac_f32_e32 v75, v22, v32
	v_fmac_f32_e32 v74, v22, v33
	v_fmac_f32_e32 v59, v22, v34
	v_fmac_f32_e32 v40, v22, v35
	s_waitcnt lgkmcnt(0)
; template <bool COMBINE, bool ROUTE, bool FINAL, bool OUT8 = false, bool DUMMY = false> ...
;     ...
;                 for (int j = 0; j < 8; ++j) {
; #pragma unroll
;                     for (int cc = 0; cc < 4; ++cc) {
;                         const float hv = xv[j][cc];
;                         const f32x4 w0 = WT[((j * 4 + cc) * 4 + 0) * 64 + lane], w1 = WT[((j * 4 + cc) * 4 + 1) * 64 + lane], w2 = WT[((j * 4 + cc) * 4 + 2) * 64 + lane], w3 = WT[((j * 4 + cc) * 4 + 3) * 64 + lane];
;                         lg[0] += hv * w0.x; lg[1] += hv * w0.y; lg[2] += hv * w0.z; lg[3] += hv * w0.w;
;                         lg[4] += hv * w1.x; lg[5] += hv * w1.y; lg[6] += hv * w1.z; lg[7] += hv * w1.w;
;                         lg[8] += hv * w2.x; lg[9] += hv * w2.y; lg[10] += hv * w2.z; lg[11] += hv * w2.w;
;                         lg[12] += hv * w3.x; lg[13] += hv * w3.y; lg[14] += hv * w3.z; lg[15] += hv * w3.w;
;                     }
	v_fmac_f32_e32 v71, v22, v152
	v_fmac_f32_e32 v69, v22, v153
	v_fmac_f32_e32 v3, v22, v154
	ds_read_b128 v[24:27], v78 offset:53248
	v_fmac_f32_e32 v1, v22, v155
	ds_read_b128 v[28:31], v78 offset:54272
	ds_read_b128 v[32:35], v78 offset:55296
	ds_read_b128 v[152:155], v78 offset:56320
	s_waitcnt lgkmcnt(3)
	v_fmac_f32_e32 v150, v23, v24
	v_fmac_f32_e32 v149, v23, v25
	v_fmac_f32_e32 v67, v23, v26
	v_fmac_f32_e32 v65, v23, v27
	s_waitcnt lgkmcnt(2)
	v_fmac_f32_e32 v77, v23, v28
	v_fmac_f32_e32 v76, v23, v29
	v_fmac_f32_e32 v63, v23, v30
	v_fmac_f32_e32 v61, v23, v31
	s_waitcnt lgkmcnt(1)
	v_fmac_f32_e32 v75, v23, v32
	v_fmac_f32_e32 v74, v23, v33
	v_fmac_f32_e32 v59, v23, v34
	v_fmac_f32_e32 v40, v23, v35
	s_waitcnt lgkmcnt(0)
	v_fmac_f32_e32 v71, v23, v152
	v_fmac_f32_e32 v69, v23, v153
	v_fmac_f32_e32 v3, v23, v154
	ds_read_b128 v[24:27], v78 offset:57344
	v_fmac_f32_e32 v1, v23, v155
	ds_read_b128 v[28:31], v78 offset:58368
	ds_read_b128 v[32:35], v78 offset:59392
	ds_read_b128 v[152:155], v78 offset:60416
	s_waitcnt lgkmcnt(3)
	v_fmac_f32_e32 v150, v20, v24
	v_fmac_f32_e32 v149, v20, v25
	v_fmac_f32_e32 v67, v20, v26
	v_fmac_f32_e32 v65, v20, v27
	s_waitcnt lgkmcnt(2)
	v_fmac_f32_e32 v77, v20, v28
	v_fmac_f32_e32 v76, v20, v29
	v_fmac_f32_e32 v63, v20, v30
	v_fmac_f32_e32 v61, v20, v31
	s_waitcnt lgkmcnt(1)
	v_fmac_f32_e32 v75, v20, v32
	v_fmac_f32_e32 v74, v20, v33
	s_waitcnt lgkmcnt(0)
	v_fmac_f32_e32 v71, v20, v152
	v_fmac_f32_e32 v69, v20, v153
	v_fmac_f32_e32 v3, v20, v154
	ds_read_b128 v[22:25], v78 offset:61440
	v_fmac_f32_e32 v1, v20, v155
	ds_read_b128 v[26:29], v78 offset:62464
	ds_read_b128 v[30:33], v78 offset:63488
	ds_read_b128 v[152:155], v78 offset:64512
	v_fmac_f32_e32 v59, v20, v34
	v_fmac_f32_e32 v40, v20, v35
	s_waitcnt lgkmcnt(3)
	v_fmac_f32_e32 v150, v21, v22
	s_waitcnt lgkmcnt(1)
	v_fmac_f32_e32 v59, v21, v32
	v_fmac_f32_e32 v40, v21, v33
	s_waitcnt lgkmcnt(0)
	v_fmac_f32_e32 v3, v21, v154
	v_fmac_f32_e32 v1, v21, v155
	v_fmac_f32_e32 v149, v21, v23
	v_fmac_f32_e32 v67, v21, v24
	v_fmac_f32_e32 v65, v21, v25
	v_fmac_f32_e32 v77, v21, v26
	v_fmac_f32_e32 v76, v21, v27
	v_fmac_f32_e32 v63, v21, v28
	v_fmac_f32_e32 v61, v21, v29
	v_fmac_f32_e32 v75, v21, v30
	v_fmac_f32_e32 v74, v21, v31
	v_fmac_f32_e32 v71, v21, v152
	v_fmac_f32_e32 v69, v21, v153
	ds_read_b128 v[20:23], v80
	ds_read_b128 v[24:27], v81
	ds_read_b128 v[28:31], v82
	ds_read_b128 v[32:35], v83
	s_waitcnt lgkmcnt(3)
	v_fmac_f32_e32 v150, v18, v20
	v_fmac_f32_e32 v149, v18, v21
	v_fmac_f32_e32 v67, v18, v22
	v_fmac_f32_e32 v65, v18, v23
	s_waitcnt lgkmcnt(2)
	v_fmac_f32_e32 v77, v18, v24
	v_fmac_f32_e32 v76, v18, v25
	v_fmac_f32_e32 v63, v18, v26
	v_fmac_f32_e32 v61, v18, v27
	s_waitcnt lgkmcnt(1)
	v_fmac_f32_e32 v75, v18, v28
	v_fmac_f32_e32 v74, v18, v29
	v_fmac_f32_e32 v59, v18, v30
	v_fmac_f32_e32 v40, v18, v31
	s_waitcnt lgkmcnt(0)
	v_fmac_f32_e32 v71, v18, v32
	v_fmac_f32_e32 v69, v18, v33
	v_fmac_f32_e32 v3, v18, v34
	ds_read_b128 v[20:23], v84
	v_fmac_f32_e32 v1, v18, v35
	ds_read_b128 v[24:27], v85
	ds_read_b128 v[28:31], v86
	ds_read_b128 v[32:35], v87
	s_waitcnt lgkmcnt(3)
	v_fmac_f32_e32 v150, v19, v20
	v_fmac_f32_e32 v149, v19, v21
	v_fmac_f32_e32 v67, v19, v22
	v_fmac_f32_e32 v65, v19, v23
	s_waitcnt lgkmcnt(2)
	v_fmac_f32_e32 v77, v19, v24
	v_fmac_f32_e32 v76, v19, v25
	v_fmac_f32_e32 v63, v19, v26
	v_fmac_f32_e32 v61, v19, v27
	s_waitcnt lgkmcnt(1)
	v_fmac_f32_e32 v75, v19, v28
	v_fmac_f32_e32 v74, v19, v29
	v_fmac_f32_e32 v59, v19, v30
	v_fmac_f32_e32 v40, v19, v31
	s_waitcnt lgkmcnt(0)
	v_fmac_f32_e32 v71, v19, v32
	v_fmac_f32_e32 v69, v19, v33
	v_fmac_f32_e32 v3, v19, v34
	ds_read_b128 v[20:23], v88
	v_fmac_f32_e32 v1, v19, v35
	ds_read_b128 v[24:27], v89
	ds_read_b128 v[28:31], v90
	ds_read_b128 v[32:35], v91
	s_waitcnt lgkmcnt(3)
	v_fmac_f32_e32 v150, v16, v20
	v_fmac_f32_e32 v149, v16, v21
	v_fmac_f32_e32 v67, v16, v22
	v_fmac_f32_e32 v65, v16, v23
	s_waitcnt lgkmcnt(2)
	v_fmac_f32_e32 v77, v16, v24
	v_fmac_f32_e32 v76, v16, v25
	v_fmac_f32_e32 v63, v16, v26
	v_fmac_f32_e32 v61, v16, v27
	s_waitcnt lgkmcnt(1)
	v_fmac_f32_e32 v75, v16, v28
	v_fmac_f32_e32 v74, v16, v29
	v_fmac_f32_e32 v59, v16, v30
	v_fmac_f32_e32 v40, v16, v31
	s_waitcnt lgkmcnt(0)
	v_fmac_f32_e32 v71, v16, v32
	v_fmac_f32_e32 v69, v16, v33
	ds_read_b128 v[18:21], v92
	ds_read_b128 v[22:25], v93
	ds_read_b128 v[26:29], v94
	ds_read_b128 v[30:33], v95
	v_fmac_f32_e32 v3, v16, v34
	v_fmac_f32_e32 v1, v16, v35
	s_waitcnt lgkmcnt(2)
	v_fmac_f32_e32 v77, v17, v22
	s_waitcnt lgkmcnt(1)
	v_fmac_f32_e32 v59, v17, v28
	v_fmac_f32_e32 v40, v17, v29
	s_waitcnt lgkmcnt(0)
	v_fmac_f32_e32 v3, v17, v32
	v_fmac_f32_e32 v1, v17, v33
	v_fmac_f32_e32 v150, v17, v18
	v_fmac_f32_e32 v149, v17, v19
	v_fmac_f32_e32 v67, v17, v20
	v_fmac_f32_e32 v65, v17, v21
	v_fmac_f32_e32 v76, v17, v23
	v_fmac_f32_e32 v63, v17, v24
	v_fmac_f32_e32 v61, v17, v25
	v_fmac_f32_e32 v75, v17, v26
	v_fmac_f32_e32 v74, v17, v27
	v_fmac_f32_e32 v71, v17, v30
	v_fmac_f32_e32 v69, v17, v31
	ds_read_b128 v[16:19], v96
	ds_read_b128 v[20:23], v97
	ds_read_b128 v[24:27], v98
	ds_read_b128 v[28:31], v99
	s_waitcnt lgkmcnt(3)
	v_fmac_f32_e32 v150, v14, v16
	v_fmac_f32_e32 v149, v14, v17
	v_fmac_f32_e32 v67, v14, v18
	v_fmac_f32_e32 v65, v14, v19
	s_waitcnt lgkmcnt(2)
	v_fmac_f32_e32 v77, v14, v20
	v_fmac_f32_e32 v76, v14, v21
	v_fmac_f32_e32 v63, v14, v22
	v_fmac_f32_e32 v61, v14, v23
	s_waitcnt lgkmcnt(1)
	v_fmac_f32_e32 v75, v14, v24
	v_fmac_f32_e32 v74, v14, v25
	v_fmac_f32_e32 v59, v14, v26
	v_fmac_f32_e32 v40, v14, v27
	s_waitcnt lgkmcnt(0)
; template <bool COMBINE, bool ROUTE, bool FINAL, bool OUT8 = false, bool DUMMY = false> ...
;     ...
;                 for (int j = 0; j < 8; ++j) {
; #pragma unroll
;                     for (int cc = 0; cc < 4; ++cc) {
;                         const float hv = xv[j][cc];
;                         const f32x4 w0 = WT[((j * 4 + cc) * 4 + 0) * 64 + lane], w1 = WT[((j * 4 + cc) * 4 + 1) * 64 + lane], w2 = WT[((j * 4 + cc) * 4 + 2) * 64 + lane], w3 = WT[((j * 4 + cc) * 4 + 3) * 64 + lane];
;                         lg[0] += hv * w0.x; lg[1] += hv * w0.y; lg[2] += hv * w0.z; lg[3] += hv * w0.w;
;                         lg[4] += hv * w1.x; lg[5] += hv * w1.y; lg[6] += hv * w1.z; lg[7] += hv * w1.w;
;                         lg[8] += hv * w2.x; lg[9] += hv * w2.y; lg[10] += hv * w2.z; lg[11] += hv * w2.w;
;                         lg[12] += hv * w3.x; lg[13] += hv * w3.y; lg[14] += hv * w3.z; lg[15] += hv * w3.w;
;                     }
	v_fmac_f32_e32 v71, v14, v28
	v_fmac_f32_e32 v69, v14, v29
	v_fmac_f32_e32 v3, v14, v30
	ds_read_b128 v[16:19], v100
	v_fmac_f32_e32 v1, v14, v31
	ds_read_b128 v[20:23], v101
	ds_read_b128 v[24:27], v102
	ds_read_b128 v[28:31], v103
	s_waitcnt lgkmcnt(3)
	v_fmac_f32_e32 v150, v15, v16
	v_fmac_f32_e32 v149, v15, v17
	v_fmac_f32_e32 v67, v15, v18
	v_fmac_f32_e32 v65, v15, v19
	s_waitcnt lgkmcnt(2)
	v_fmac_f32_e32 v77, v15, v20
	v_fmac_f32_e32 v76, v15, v21
	v_fmac_f32_e32 v63, v15, v22
	v_fmac_f32_e32 v61, v15, v23
	s_waitcnt lgkmcnt(1)
	v_fmac_f32_e32 v75, v15, v24
	v_fmac_f32_e32 v74, v15, v25
	v_fmac_f32_e32 v59, v15, v26
	v_fmac_f32_e32 v40, v15, v27
	s_waitcnt lgkmcnt(0)
	v_fmac_f32_e32 v71, v15, v28
	v_fmac_f32_e32 v69, v15, v29
	v_fmac_f32_e32 v3, v15, v30
	ds_read_b128 v[16:19], v104
	v_fmac_f32_e32 v1, v15, v31
	ds_read_b128 v[20:23], v105
	ds_read_b128 v[24:27], v106
	ds_read_b128 v[28:31], v107
	s_waitcnt lgkmcnt(3)
	v_fmac_f32_e32 v150, v12, v16
	v_fmac_f32_e32 v149, v12, v17
	v_fmac_f32_e32 v67, v12, v18
	v_fmac_f32_e32 v65, v12, v19
	s_waitcnt lgkmcnt(2)
	v_fmac_f32_e32 v77, v12, v20
	v_fmac_f32_e32 v76, v12, v21
	v_fmac_f32_e32 v63, v12, v22
	v_fmac_f32_e32 v61, v12, v23
	s_waitcnt lgkmcnt(1)
	v_fmac_f32_e32 v75, v12, v24
	v_fmac_f32_e32 v74, v12, v25
	v_fmac_f32_e32 v59, v12, v26
	v_fmac_f32_e32 v40, v12, v27
	s_waitcnt lgkmcnt(0)
	v_fmac_f32_e32 v71, v12, v28
	v_fmac_f32_e32 v69, v12, v29
	ds_read_b128 v[14:17], v108
	ds_read_b128 v[18:21], v109
	ds_read_b128 v[22:25], v110
	ds_read_b128 v[26:29], v111
	v_fmac_f32_e32 v3, v12, v30
	v_fmac_f32_e32 v1, v12, v31
	s_waitcnt lgkmcnt(2)
	v_fmac_f32_e32 v77, v13, v18
	s_waitcnt lgkmcnt(1)
	v_fmac_f32_e32 v59, v13, v24
	v_fmac_f32_e32 v40, v13, v25
	s_waitcnt lgkmcnt(0)
	v_fmac_f32_e32 v3, v13, v28
	v_fmac_f32_e32 v1, v13, v29
	v_fmac_f32_e32 v150, v13, v14
	v_fmac_f32_e32 v149, v13, v15
	v_fmac_f32_e32 v67, v13, v16
	v_fmac_f32_e32 v65, v13, v17
	v_fmac_f32_e32 v76, v13, v19
	v_fmac_f32_e32 v63, v13, v20
	v_fmac_f32_e32 v61, v13, v21
	v_fmac_f32_e32 v75, v13, v22
	v_fmac_f32_e32 v74, v13, v23
	v_fmac_f32_e32 v71, v13, v26
	v_fmac_f32_e32 v69, v13, v27
	ds_read_b128 v[12:15], v112
	ds_read_b128 v[16:19], v113
	ds_read_b128 v[20:23], v114
	ds_read_b128 v[24:27], v115
	s_waitcnt lgkmcnt(3)
	v_fmac_f32_e32 v150, v10, v12
	v_fmac_f32_e32 v149, v10, v13
	v_fmac_f32_e32 v67, v10, v14
	v_fmac_f32_e32 v65, v10, v15
	s_waitcnt lgkmcnt(2)
	v_fmac_f32_e32 v77, v10, v16
	v_fmac_f32_e32 v76, v10, v17
	v_fmac_f32_e32 v63, v10, v18
	v_fmac_f32_e32 v61, v10, v19
	s_waitcnt lgkmcnt(1)
	v_fmac_f32_e32 v75, v10, v20
	v_fmac_f32_e32 v74, v10, v21
	v_fmac_f32_e32 v59, v10, v22
	v_fmac_f32_e32 v40, v10, v23
	s_waitcnt lgkmcnt(0)
	v_fmac_f32_e32 v71, v10, v24
	v_fmac_f32_e32 v69, v10, v25
	v_fmac_f32_e32 v3, v10, v26
	ds_read_b128 v[12:15], v116
	v_fmac_f32_e32 v1, v10, v27
	ds_read_b128 v[16:19], v117
	ds_read_b128 v[20:23], v118
	ds_read_b128 v[24:27], v119
	s_waitcnt lgkmcnt(3)
	v_fmac_f32_e32 v150, v11, v12
	v_fmac_f32_e32 v149, v11, v13
	v_fmac_f32_e32 v67, v11, v14
	v_fmac_f32_e32 v65, v11, v15
	s_waitcnt lgkmcnt(2)
	v_fmac_f32_e32 v77, v11, v16
	v_fmac_f32_e32 v76, v11, v17
	v_fmac_f32_e32 v63, v11, v18
	v_fmac_f32_e32 v61, v11, v19
	s_waitcnt lgkmcnt(1)
	v_fmac_f32_e32 v75, v11, v20
	v_fmac_f32_e32 v74, v11, v21
	v_fmac_f32_e32 v59, v11, v22
	v_fmac_f32_e32 v40, v11, v23
	s_waitcnt lgkmcnt(0)
	v_fmac_f32_e32 v71, v11, v24
	v_fmac_f32_e32 v69, v11, v25
	v_fmac_f32_e32 v3, v11, v26
	ds_read_b128 v[12:15], v120
	v_fmac_f32_e32 v1, v11, v27
	ds_read_b128 v[16:19], v121
	ds_read_b128 v[20:23], v122
	ds_read_b128 v[24:27], v123
	s_waitcnt lgkmcnt(3)
	v_fmac_f32_e32 v150, v8, v12
	v_fmac_f32_e32 v149, v8, v13
	v_fmac_f32_e32 v67, v8, v14
	v_fmac_f32_e32 v65, v8, v15
	s_waitcnt lgkmcnt(2)
	v_fmac_f32_e32 v77, v8, v16
	v_fmac_f32_e32 v76, v8, v17
	v_fmac_f32_e32 v63, v8, v18
	v_fmac_f32_e32 v61, v8, v19
	s_waitcnt lgkmcnt(1)
	v_fmac_f32_e32 v75, v8, v20
	v_fmac_f32_e32 v74, v8, v21
	v_fmac_f32_e32 v59, v8, v22
	v_fmac_f32_e32 v40, v8, v23
	s_waitcnt lgkmcnt(0)
	v_fmac_f32_e32 v71, v8, v24
	v_fmac_f32_e32 v69, v8, v25
	ds_read_b128 v[10:13], v124
	ds_read_b128 v[14:17], v125
	ds_read_b128 v[18:21], v126
	ds_read_b128 v[22:25], v127
	v_fmac_f32_e32 v3, v8, v26
	v_fmac_f32_e32 v1, v8, v27
	s_waitcnt lgkmcnt(2)
	v_fmac_f32_e32 v77, v9, v14
	s_waitcnt lgkmcnt(1)
	v_fmac_f32_e32 v59, v9, v20
	v_fmac_f32_e32 v40, v9, v21
	s_waitcnt lgkmcnt(0)
	v_fmac_f32_e32 v3, v9, v24
	v_fmac_f32_e32 v1, v9, v25
	v_fmac_f32_e32 v150, v9, v10
	v_fmac_f32_e32 v149, v9, v11
	v_fmac_f32_e32 v67, v9, v12
	v_fmac_f32_e32 v65, v9, v13
	v_fmac_f32_e32 v76, v9, v15
	v_fmac_f32_e32 v63, v9, v16
	v_fmac_f32_e32 v61, v9, v17
	v_fmac_f32_e32 v75, v9, v18
	v_fmac_f32_e32 v74, v9, v19
	v_fmac_f32_e32 v71, v9, v22
	v_fmac_f32_e32 v69, v9, v23
	ds_read_b128 v[8:11], v128
	ds_read_b128 v[12:15], v129
	ds_read_b128 v[16:19], v130
	ds_read_b128 v[20:23], v131
	s_waitcnt lgkmcnt(3)
	v_fmac_f32_e32 v65, v6, v11
	v_fmac_f32_e32 v67, v6, v10
	v_mov_b32_e32 v10, v8
	s_waitcnt lgkmcnt(0)
	v_fmac_f32_e32 v3, v6, v22
	v_fmac_f32_e32 v1, v6, v23
	ds_read_b128 v[22:25], v132
	ds_read_b128 v[26:29], v133
	ds_read_b128 v[30:33], v134
	ds_read_b128 v[152:155], v135
	v_fmac_f32_e32 v63, v6, v14
	s_waitcnt lgkmcnt(3)
	v_mov_b32_e32 v11, v22
	v_mov_b32_e32 v22, v9
	v_pk_mul_f32 v[8:9], v[6:7], v[22:23]
	v_pk_mul_f32 v[10:11], v[6:7], v[10:11]
	v_add_f32_e32 v8, v149, v8
	v_add_f32_e32 v149, v8, v9
	v_mov_b32_e32 v8, v12
	s_waitcnt lgkmcnt(2)
; template <bool COMBINE, bool ROUTE, bool FINAL, bool OUT8 = false, bool DUMMY = false> ...
;     ...
;                         const f32x4 w0 = WT[((j * 4 + cc) * 4 + 0) * 64 + lane], w1 = WT[((j * 4 + cc) * 4 + 1) * 64 + lane], w2 = WT[((j * 4 + cc) * 4 + 2) * 64 + lane], w3 = WT[((j * 4 + cc) * 4 + 3) * 64 + lane];
;                         lg[0] += hv * w0.x; lg[1] += hv * w0.y; lg[2] += hv * w0.z; lg[3] += hv * w0.w;
;                         lg[4] += hv * w1.x; lg[5] += hv * w1.y; lg[6] += hv * w1.z; lg[7] += hv * w1.w;
;                         lg[8] += hv * w2.x; lg[9] += hv * w2.y; lg[10] += hv * w2.z; lg[11] += hv * w2.w;
;                         lg[12] += hv * w3.x; lg[13] += hv * w3.y; lg[14] += hv * w3.z; lg[15] += hv * w3.w;
;                     }
;                     __builtin_amdgcn_sched_barrier(0);
;                 }
;                 float sc_[16], sel[16];
; #pragma unroll
;                 for (int e = 0; e < 16; ++e) { lg[e] = wave_sum(lg[e]); sc_[e] = 1.f / (1.f + expf(-lg[e])); sel[e] = sc_[e] + rb[e]; }
	v_mov_b32_e32 v9, v26
	v_pk_mul_f32 v[8:9], v[6:7], v[8:9]
	v_mov_b32_e32 v26, v13
	v_add_f32_e32 v8, v77, v8
	v_add_f32_e32 v77, v8, v9
	v_pk_mul_f32 v[8:9], v[6:7], v[26:27]
	v_add_f32_e32 v0, v150, v10
	v_add_f32_e32 v8, v76, v8
	v_add_f32_e32 v76, v8, v9
	v_mov_b32_e32 v8, v16
	s_waitcnt lgkmcnt(1)
	v_mov_b32_e32 v9, v30
	v_pk_mul_f32 v[8:9], v[6:7], v[8:9]
	v_mov_b32_e32 v30, v17
	v_add_f32_e32 v8, v75, v8
	v_add_f32_e32 v150, v8, v9
	v_pk_mul_f32 v[8:9], v[6:7], v[30:31]
	v_fmac_f32_e32 v61, v6, v15
	v_add_f32_e32 v8, v74, v8
	v_add_f32_e32 v151, v8, v9
	v_mov_b32_e32 v8, v20
	s_waitcnt lgkmcnt(0)
	v_mov_b32_e32 v9, v152
	v_pk_mul_f32 v[8:9], v[6:7], v[8:9]
	v_mov_b32_e32 v152, v21
	v_add_f32_e32 v8, v71, v8
	v_add_f32_e32 v71, v8, v9
	v_pk_mul_f32 v[8:9], v[6:7], v[152:153]
	v_fmac_f32_e32 v59, v6, v18
	v_fmac_f32_e32 v40, v6, v19
	v_add_f32_e32 v6, v69, v8
	v_add_f32_e32 v0, v0, v11
	v_fmac_f32_e32 v67, v7, v24
	v_fmac_f32_e32 v65, v7, v25
	v_fmac_f32_e32 v63, v7, v28
	v_fmac_f32_e32 v61, v7, v29
	v_fmac_f32_e32 v59, v7, v32
	v_fmac_f32_e32 v40, v7, v33
	v_add_f32_e32 v69, v6, v9
	v_fmac_f32_e32 v3, v7, v154
	v_fmac_f32_e32 v1, v7, v155
	ds_read_b128 v[6:9], v136
	ds_read_b128 v[10:13], v137
	ds_read_b128 v[14:17], v138
	ds_read_b128 v[18:21], v139
	ds_read_b128 v[22:25], v140
	ds_read_b128 v[26:29], v141
	ds_read_b128 v[30:33], v142
	ds_read_b128 v[72:75], v143
	s_waitcnt lgkmcnt(7)
	v_mov_b32_e32 v34, v6
	s_waitcnt lgkmcnt(3)
	v_mov_b32_e32 v35, v22
	v_mov_b32_e32 v22, v7
	v_pk_mul_f32 v[6:7], v[4:5], v[22:23]
	v_pk_mul_f32 v[34:35], v[4:5], v[34:35]
	v_add_f32_e32 v6, v149, v6
	v_add_f32_e32 v0, v0, v34
	v_add_f32_e32 v34, v6, v7
	v_mov_b32_e32 v6, v8
	v_mov_b32_e32 v7, v24
	v_pk_mul_f32 v[6:7], v[4:5], v[6:7]
	v_mov_b32_e32 v24, v9
	v_add_f32_e32 v6, v67, v6
	v_add_f32_e32 v8, v6, v7
	v_pk_mul_f32 v[6:7], v[4:5], v[24:25]
	v_add_f32_e32 v0, v0, v35
	v_add_f32_e32 v6, v65, v6
	v_add_f32_e32 v9, v6, v7
	v_mov_b32_e32 v6, v10
	s_waitcnt lgkmcnt(2)
	v_mov_b32_e32 v7, v26
	v_pk_mul_f32 v[6:7], v[4:5], v[6:7]
	v_mov_b32_e32 v26, v11
	v_add_f32_e32 v6, v77, v6
	v_add_f32_e32 v35, v6, v7
	v_pk_mul_f32 v[6:7], v[4:5], v[26:27]
	s_nop 0
	v_add_f32_e32 v6, v76, v6
	v_add_f32_e32 v65, v6, v7
	v_mov_b32_e32 v6, v12
	v_mov_b32_e32 v7, v28
	v_pk_mul_f32 v[6:7], v[4:5], v[6:7]
	v_mov_b32_e32 v28, v13
	v_add_f32_e32 v6, v63, v6
	v_add_f32_e32 v63, v6, v7
	v_pk_mul_f32 v[6:7], v[4:5], v[28:29]
	s_nop 0
	v_add_f32_e32 v6, v61, v6
	v_add_f32_e32 v61, v6, v7
	v_mov_b32_e32 v6, v14
	s_waitcnt lgkmcnt(1)
	v_mov_b32_e32 v7, v30
	v_pk_mul_f32 v[6:7], v[4:5], v[6:7]
	v_mov_b32_e32 v30, v15
	v_add_f32_e32 v6, v150, v6
	v_add_f32_e32 v27, v6, v7
	v_pk_mul_f32 v[6:7], v[4:5], v[30:31]
	s_nop 0
	v_add_f32_e32 v6, v151, v6
	v_add_f32_e32 v26, v6, v7
	v_mov_b32_e32 v6, v16
	v_mov_b32_e32 v7, v32
	v_pk_mul_f32 v[6:7], v[4:5], v[6:7]
	v_mov_b32_e32 v32, v17
	v_add_f32_e32 v6, v59, v6
	v_add_f32_e32 v25, v6, v7
	v_pk_mul_f32 v[6:7], v[4:5], v[32:33]
	s_nop 0
	v_add_f32_e32 v6, v40, v6
	v_add_f32_e32 v23, v6, v7
	v_mov_b32_e32 v6, v18
	s_waitcnt lgkmcnt(0)
	v_mov_b32_e32 v7, v72
	v_pk_mul_f32 v[6:7], v[4:5], v[6:7]
	v_mov_b32_e32 v72, v19
	v_add_f32_e32 v6, v71, v6
	v_add_f32_e32 v24, v6, v7
	v_pk_mul_f32 v[6:7], v[4:5], v[72:73]
	s_nop 0
	v_add_f32_e32 v6, v69, v6
	v_add_f32_e32 v22, v6, v7
	v_mov_b32_e32 v6, v20
	v_mov_b32_e32 v7, v74
	v_mov_b32_e32 v74, v21
	v_pk_mul_f32 v[6:7], v[4:5], v[6:7]
	v_pk_mul_f32 v[4:5], v[4:5], v[74:75]
	v_add_f32_e32 v3, v3, v6
	v_add_f32_e32 v1, v1, v4
	v_add_f32_e32 v3, v3, v7
	v_add_f32_e32 v1, v1, v5
	ds_bpermute_b32 v4, v182, v0
	ds_bpermute_b32 v5, v182, v34
	global_load_dwordx4 v[16:19], v41, s[42:43]
	s_waitcnt lgkmcnt(1)
	v_add_f32_e32 v0, v0, v4
	s_waitcnt lgkmcnt(0)
	v_add_f32_e32 v4, v34, v5
	ds_bpermute_b32 v5, v183, v0
	ds_bpermute_b32 v6, v183, v4
	s_waitcnt lgkmcnt(1)
	v_add_f32_e32 v0, v0, v5
	s_waitcnt lgkmcnt(0)
	v_add_f32_e32 v4, v4, v6
	ds_bpermute_b32 v5, v184, v0
	ds_bpermute_b32 v6, v184, v4
	s_waitcnt lgkmcnt(1)
	v_add_f32_e32 v0, v0, v5
	s_waitcnt lgkmcnt(0)
	v_add_f32_e32 v4, v4, v6
	ds_bpermute_b32 v5, v185, v0
	ds_bpermute_b32 v6, v185, v4
	s_waitcnt lgkmcnt(1)
	v_add_f32_e32 v0, v0, v5
	s_waitcnt lgkmcnt(0)
	v_add_f32_e32 v4, v4, v6
	ds_bpermute_b32 v5, v186, v0
	ds_bpermute_b32 v6, v186, v4
	s_waitcnt lgkmcnt(1)
	v_add_f32_e32 v0, v0, v5
	s_waitcnt lgkmcnt(0)
	v_add_f32_e32 v4, v4, v6
	ds_bpermute_b32 v5, v187, v0
	ds_bpermute_b32 v6, v187, v4
	s_waitcnt lgkmcnt(1)
	v_add_f32_e32 v0, v0, v5
	s_waitcnt lgkmcnt(0)
	v_add_f32_e32 v5, v4, v6
	v_mul_f32_e32 v4, 0xbfb8aa3b, v0
	v_fma_f32 v7, v0, s4, -v4
	v_rndne_f32_e32 v10, v4
	v_mul_f32_e32 v6, 0xbfb8aa3b, v5
	v_fmac_f32_e32 v7, 0xb2a5705f, v0
	v_sub_f32_e32 v4, v4, v10
	v_fma_f32 v11, v5, s4, -v6
	v_rndne_f32_e32 v12, v6
	v_add_f32_e32 v4, v4, v7
	v_cvt_i32_f32_e32 v10, v10
	v_fmac_f32_e32 v11, 0xb2a5705f, v5
	v_sub_f32_e32 v6, v6, v12
	v_exp_f32_e32 v4, v4
	v_add_f32_e32 v6, v6, v11
	v_cvt_i32_f32_e32 v12, v12
	v_exp_f32_e32 v6, v6
	ds_bpermute_b32 v7, v182, v8
	v_ldexp_f32 v4, v4, v10
	v_cmp_nlt_f32_e32 vcc, s5, v0
	v_ldexp_f32 v6, v6, v12
	global_load_dwordx4 v[12:15], v41, s[42:43] offset:16
	v_cndmask_b32_e32 v4, 0, v4, vcc
	v_cmp_ngt_f32_e32 vcc, s56, v0
	s_waitcnt lgkmcnt(0)
	v_add_f32_e32 v7, v8, v7
	ds_bpermute_b32 v8, v183, v7
	v_cndmask_b32_e32 v4, v146, v4, vcc
	v_cmp_nlt_f32_e32 vcc, s5, v5
	s_waitcnt lgkmcnt(0)
	v_add_f32_e32 v7, v7, v8
	v_cndmask_b32_e32 v0, 0, v6, vcc
	v_cmp_ngt_f32_e32 vcc, s56, v5
	ds_bpermute_b32 v8, v184, v7
	s_waitcnt lgkmcnt(0)
; template <bool COMBINE, bool ROUTE, bool FINAL, bool OUT8 = false, bool DUMMY = false> ...
;     ...
;                 for (int e = 0; e < 16; ++e) { lg[e] = wave_sum(lg[e]); sc_[e] = 1.f / (1.f + expf(-lg[e])); sel[e] = sc_[e] + rb[e]; }
	v_add_f32_e32 v7, v7, v8
	v_cndmask_b32_e32 v5, v146, v0, vcc
	v_pk_add_f32 v[4:5], v[4:5], 1.0 op_sel_hi:[1,0]
	ds_bpermute_b32 v8, v185, v7
	v_div_scale_f32 v0, s[8:9], v5, v5, 1.0
	v_rcp_f32_e32 v6, v0
	s_nop 0
	v_fma_f32 v10, -v0, v6, 1.0
	v_fmac_f32_e32 v6, v10, v6
	v_div_scale_f32 v10, vcc, 1.0, v5, 1.0
	v_mul_f32_e32 v11, v10, v6
	v_fma_f32 v20, -v0, v11, v10
	v_fmac_f32_e32 v11, v20, v6
	v_fma_f32 v0, -v0, v11, v10
	v_div_scale_f32 v10, s[8:9], v4, v4, 1.0
	v_rcp_f32_e32 v20, v10
	v_div_fmas_f32 v0, v0, v6, v11
	v_div_fixup_f32 v21, v0, v5, 1.0
	v_div_scale_f32 v6, vcc, 1.0, v4, 1.0
	v_fma_f32 v0, -v10, v20, 1.0
	v_fmac_f32_e32 v20, v0, v20
	s_waitcnt lgkmcnt(0)
	v_add_f32_e32 v0, v7, v8
	ds_bpermute_b32 v5, v186, v0
	v_mul_f32_e32 v7, v6, v20
	v_fma_f32 v8, -v10, v7, v6
	v_fmac_f32_e32 v7, v8, v20
	v_fma_f32 v6, -v10, v7, v6
	s_waitcnt lgkmcnt(0)
	v_add_f32_e32 v0, v0, v5
	ds_bpermute_b32 v5, v187, v0
	ds_bpermute_b32 v10, v182, v9
	v_div_fmas_f32 v6, v6, v20, v7
	v_div_fixup_f32 v20, v6, v4, 1.0
	s_waitcnt vmcnt(1)
	v_pk_add_f32 v[16:17], v[16:17], v[20:21]
	s_waitcnt lgkmcnt(1)
	v_add_f32_e32 v0, v0, v5
	v_mul_f32_e32 v5, 0xbfb8aa3b, v0
	v_fma_f32 v7, v0, s4, -v5
	v_rndne_f32_e32 v8, v5
	v_fmac_f32_e32 v7, 0xb2a5705f, v0
	v_sub_f32_e32 v5, v5, v8
	s_waitcnt lgkmcnt(0)
	v_add_f32_e32 v30, v9, v10
	v_add_f32_e32 v5, v5, v7
	ds_bpermute_b32 v31, v183, v30
	v_exp_f32_e32 v28, v5
	v_cvt_i32_f32_e32 v29, v8
	v_cmp_nlt_f32_e32 vcc, s5, v0
	global_load_dwordx4 v[4:7], v41, s[42:43] offset:48
	global_load_dwordx4 v[8:11], v41, s[42:43] offset:32
	v_ldexp_f32 v28, v28, v29
	s_waitcnt lgkmcnt(0)
	v_add_f32_e32 v29, v30, v31
	ds_bpermute_b32 v30, v184, v29
	v_cndmask_b32_e32 v28, 0, v28, vcc
	v_cmp_ngt_f32_e32 vcc, s56, v0
	s_nop 1
	v_cndmask_b32_e32 v0, v146, v28, vcc
	s_waitcnt lgkmcnt(0)
	v_add_f32_e32 v28, v29, v30
	ds_bpermute_b32 v29, v185, v28
	v_add_f32_e32 v0, 1.0, v0
	v_div_scale_f32 v30, s[8:9], v0, v0, 1.0
	v_rcp_f32_e32 v31, v30
	s_waitcnt lgkmcnt(0)
	v_add_f32_e32 v28, v28, v29
	ds_bpermute_b32 v29, v186, v28
	v_fma_f32 v32, -v30, v31, 1.0
	v_fmac_f32_e32 v31, v32, v31
	v_div_scale_f32 v32, vcc, 1.0, v0, 1.0
	s_waitcnt lgkmcnt(0)
	v_add_f32_e32 v28, v28, v29
	ds_bpermute_b32 v29, v187, v28
	v_mul_f32_e32 v33, v32, v31
	v_fma_f32 v34, -v30, v33, v32
	v_fmac_f32_e32 v33, v34, v31
	v_fma_f32 v30, -v30, v33, v32
	s_waitcnt lgkmcnt(0)
	v_add_f32_e32 v28, v28, v29
	v_mul_f32_e32 v29, 0xbfb8aa3b, v28
	v_fma_f32 v32, v28, s4, -v29
	v_rndne_f32_e32 v34, v29
	v_fmac_f32_e32 v32, 0xb2a5705f, v28
	v_sub_f32_e32 v29, v29, v34
	v_add_f32_e32 v29, v29, v32
	v_cvt_i32_f32_e32 v32, v34
	ds_bpermute_b32 v34, v182, v35
	v_div_fmas_f32 v30, v30, v31, v33
	v_exp_f32_e32 v29, v29
	v_div_fixup_f32 v0, v30, v0, 1.0
	v_cmp_nlt_f32_e32 vcc, s5, v28
	s_waitcnt lgkmcnt(0)
	v_add_f32_e32 v30, v35, v34
	ds_bpermute_b32 v31, v183, v30
	v_ldexp_f32 v29, v29, v32
	v_cndmask_b32_e32 v29, 0, v29, vcc
	v_cmp_ngt_f32_e32 vcc, s56, v28
	v_add_f32_e32 v67, v18, v0
	ds_bpermute_b32 v18, v182, v65
	v_cndmask_b32_e32 v28, v146, v29, vcc
	s_waitcnt lgkmcnt(1)
	v_add_f32_e32 v29, v30, v31
	ds_bpermute_b32 v30, v184, v29
	v_add_f32_e32 v31, 1.0, v28
	v_div_scale_f32 v28, s[8:9], v31, v31, 1.0
	v_rcp_f32_e32 v32, v28
	s_waitcnt lgkmcnt(0)
	v_add_f32_e32 v29, v29, v30
	ds_bpermute_b32 v30, v185, v29
	v_add_f32_e32 v18, v65, v18
	v_fma_f32 v33, -v28, v32, 1.0
	v_fmac_f32_e32 v32, v33, v32
	ds_bpermute_b32 v33, v183, v18
	s_waitcnt lgkmcnt(1)
	v_add_f32_e32 v29, v29, v30
	ds_bpermute_b32 v30, v186, v29
	v_div_scale_f32 v34, vcc, 1.0, v31, 1.0
	s_waitcnt lgkmcnt(1)
	v_add_f32_e32 v18, v18, v33
	ds_bpermute_b32 v33, v184, v18
	s_waitcnt lgkmcnt(1)
	v_add_f32_e32 v29, v29, v30
	ds_bpermute_b32 v30, v187, v29
	v_mul_f32_e32 v35, v34, v32
	v_fma_f32 v40, -v28, v35, v34
	s_waitcnt lgkmcnt(1)
	v_add_f32_e32 v18, v18, v33
	v_fmac_f32_e32 v35, v40, v32
	s_waitcnt lgkmcnt(0)
	v_add_f32_e32 v29, v29, v30
	ds_bpermute_b32 v30, v185, v18
	v_mul_f32_e32 v33, 0xbfb8aa3b, v29
	v_fma_f32 v40, v29, s4, -v33
	v_rndne_f32_e32 v59, v33
	v_fmac_f32_e32 v40, 0xb2a5705f, v29
	s_waitcnt lgkmcnt(0)
	v_add_f32_e32 v18, v18, v30
	ds_bpermute_b32 v30, v186, v18
	v_sub_f32_e32 v33, v33, v59
	v_add_f32_e32 v33, v33, v40
	v_exp_f32_e32 v33, v33
	v_cvt_i32_f32_e32 v40, v59
	s_waitcnt lgkmcnt(0)
	v_add_f32_e32 v18, v18, v30
	ds_bpermute_b32 v30, v187, v18
	v_fma_f32 v28, -v28, v35, v34
	v_div_fmas_f32 v32, v28, v32, v35
	v_ldexp_f32 v28, v33, v40
	v_cmp_nlt_f32_e32 vcc, s5, v29
	s_waitcnt lgkmcnt(0)
	v_add_f32_e32 v18, v18, v30
	v_mul_f32_e32 v30, 0xbfb8aa3b, v18
	v_fma_f32 v33, v18, s4, -v30
	v_rndne_f32_e32 v34, v30
	v_fmac_f32_e32 v33, 0xb2a5705f, v18
	v_sub_f32_e32 v30, v30, v34
	v_add_f32_e32 v30, v30, v33
	v_exp_f32_e32 v30, v30
	v_cvt_i32_f32_e32 v33, v34
	v_cndmask_b32_e32 v28, 0, v28, vcc
	v_cmp_ngt_f32_e32 vcc, s56, v29
	ds_bpermute_b32 v40, v182, v61
	v_ldexp_f32 v29, v30, v33
	v_cndmask_b32_e32 v28, v146, v28, vcc
	v_cmp_nlt_f32_e32 vcc, s5, v18
	s_nop 1
	v_cndmask_b32_e32 v29, 0, v29, vcc
	v_cmp_ngt_f32_e32 vcc, s56, v18
	ds_bpermute_b32 v18, v182, v63
	s_waitcnt lgkmcnt(0)
	v_add_f32_e32 v18, v63, v18
	v_cndmask_b32_e32 v29, v146, v29, vcc
	v_pk_add_f32 v[28:29], v[28:29], 1.0 op_sel_hi:[1,0]
	ds_bpermute_b32 v34, v183, v18
	v_div_scale_f32 v30, s[8:9], v29, v29, 1.0
	v_rcp_f32_e32 v33, v30
	v_div_fixup_f32 v63, v32, v31, 1.0
	v_add_f32_e32 v65, v19, v63
	s_waitcnt lgkmcnt(0)
	v_add_f32_e32 v18, v18, v34
	v_fma_f32 v19, -v30, v33, 1.0
	v_fmac_f32_e32 v33, v19, v33
	ds_bpermute_b32 v19, v184, v18
	v_div_scale_f32 v31, vcc, 1.0, v29, 1.0
	v_mul_f32_e32 v32, v31, v33
	v_fma_f32 v34, -v30, v32, v31
	s_waitcnt lgkmcnt(0)
; template <bool COMBINE, bool ROUTE, bool FINAL, bool OUT8 = false, bool DUMMY = false> ...
;     ...
;                 for (int e = 0; e < 16; ++e) { lg[e] = wave_sum(lg[e]); sc_[e] = 1.f / (1.f + expf(-lg[e])); sel[e] = sc_[e] + rb[e]; }
	v_add_f32_e32 v18, v18, v19
	ds_bpermute_b32 v19, v185, v18
	v_fmac_f32_e32 v32, v34, v33
	v_fma_f32 v30, -v30, v32, v31
	v_div_scale_f32 v31, s[8:9], v28, v28, 1.0
	s_waitcnt lgkmcnt(0)
	v_add_f32_e32 v18, v18, v19
	ds_bpermute_b32 v35, v186, v18
	v_div_fmas_f32 v19, v30, v33, v32
	v_rcp_f32_e32 v34, v31
	v_div_fixup_f32 v19, v19, v29, 1.0
	s_waitcnt lgkmcnt(0)
	v_add_f32_e32 v18, v18, v35
	ds_bpermute_b32 v30, v187, v18
	v_fma_f32 v29, -v31, v34, 1.0
	v_fmac_f32_e32 v34, v29, v34
	v_div_scale_f32 v29, vcc, 1.0, v28, 1.0
	s_waitcnt lgkmcnt(0)
	v_add_f32_e32 v18, v18, v30
	v_mul_f32_e32 v30, 0xbfb8aa3b, v18
	v_fma_f32 v33, v18, s4, -v30
	v_rndne_f32_e32 v35, v30
	v_fmac_f32_e32 v33, 0xb2a5705f, v18
	v_sub_f32_e32 v30, v30, v35
	v_add_f32_e32 v30, v30, v33
	v_cvt_i32_f32_e32 v33, v35
	v_add_f32_e32 v35, v61, v40
	ds_bpermute_b32 v40, v183, v35
	v_mul_f32_e32 v32, v29, v34
	v_exp_f32_e32 v30, v30
	v_fma_f32 v59, -v31, v32, v29
	v_fmac_f32_e32 v32, v59, v34
	v_fma_f32 v29, -v31, v32, v29
	s_waitcnt lgkmcnt(0)
	v_add_f32_e32 v31, v35, v40
	v_ldexp_f32 v30, v30, v33
	ds_bpermute_b32 v33, v184, v31
	v_cmp_nlt_f32_e64 s[8:9], s5, v18
	s_nop 1
	v_cndmask_b32_e64 v30, 0, v30, s[8:9]
	v_cmp_ngt_f32_e64 s[8:9], s56, v18
	s_nop 1
	v_cndmask_b32_e64 v18, v146, v30, s[8:9]
	s_waitcnt lgkmcnt(0)
	v_add_f32_e32 v30, v31, v33
	ds_bpermute_b32 v31, v185, v30
	v_add_f32_e32 v33, 1.0, v18
	v_div_fmas_f32 v18, v29, v34, v32
	v_div_fixup_f32 v18, v18, v28, 1.0
	s_waitcnt vmcnt(2)
	v_pk_add_f32 v[72:73], v[12:13], v[18:19]
	s_waitcnt lgkmcnt(0)
	v_add_f32_e32 v30, v30, v31
	ds_bpermute_b32 v31, v186, v30
	v_div_scale_f32 v35, s[8:9], v33, v33, 1.0
	v_rcp_f32_e32 v40, v35
	v_cmp_nlg_f32_e64 s[14:15], s57, v72
	s_waitcnt lgkmcnt(0)
	v_add_f32_e32 v13, v30, v31
	ds_bpermute_b32 v28, v187, v13
	v_fma_f32 v12, -v35, v40, 1.0
	v_fmac_f32_e32 v40, v12, v40
	v_div_scale_f32 v12, vcc, 1.0, v33, 1.0
	s_waitcnt lgkmcnt(0)
	v_add_f32_e32 v13, v13, v28
	v_mul_f32_e32 v28, 0xbfb8aa3b, v13
	v_fma_f32 v30, v13, s4, -v28
	v_rndne_f32_e32 v31, v28
	v_fmac_f32_e32 v30, 0xb2a5705f, v13
	v_sub_f32_e32 v28, v28, v31
	v_add_f32_e32 v28, v28, v30
	v_mul_f32_e32 v29, v12, v40
	v_exp_f32_e32 v28, v28
	v_cvt_i32_f32_e32 v30, v31
	v_fma_f32 v31, -v35, v29, v12
	v_fmac_f32_e32 v29, v31, v40
	v_fma_f32 v12, -v35, v29, v12
	v_ldexp_f32 v28, v28, v30
	v_cmp_nlt_f32_e64 s[8:9], s5, v13
	v_div_fmas_f32 v12, v12, v40, v29
	v_div_fixup_f32 v32, v12, v33, 1.0
	v_cndmask_b32_e64 v28, 0, v28, s[8:9]
	v_cmp_ngt_f32_e64 s[8:9], s56, v13
	v_add_f32_e32 v61, v14, v32
	ds_bpermute_b32 v14, v182, v27
	v_cndmask_b32_e64 v13, v146, v28, s[8:9]
	v_add_f32_e32 v13, 1.0, v13
	v_div_scale_f32 v28, s[8:9], v13, v13, 1.0
	v_rcp_f32_e32 v30, v28
	s_waitcnt lgkmcnt(0)
	v_add_f32_e32 v14, v27, v14
	ds_bpermute_b32 v27, v183, v14
	ds_bpermute_b32 v33, v182, v26
	v_fma_f32 v12, -v28, v30, 1.0
	v_fmac_f32_e32 v30, v12, v30
	v_div_scale_f32 v12, vcc, 1.0, v13, 1.0
	v_mul_f32_e32 v29, v12, v30
	v_fma_f32 v31, -v28, v29, v12
	v_fmac_f32_e32 v29, v31, v30
	s_waitcnt lgkmcnt(1)
	v_add_f32_e32 v14, v14, v27
	s_waitcnt lgkmcnt(0)
	v_add_f32_e32 v26, v26, v33
	v_fma_f32 v12, -v28, v29, v12
	ds_bpermute_b32 v27, v184, v14
	ds_bpermute_b32 v28, v183, v26
	v_div_fmas_f32 v12, v12, v30, v29
	v_div_fixup_f32 v34, v12, v13, 1.0
	v_add_f32_e32 v69, v15, v34
	s_waitcnt lgkmcnt(1)
	v_add_f32_e32 v12, v14, v27
	s_waitcnt lgkmcnt(0)
	v_add_f32_e32 v14, v26, v28
	ds_bpermute_b32 v13, v185, v12
	ds_bpermute_b32 v26, v184, v14
	ds_bpermute_b32 v15, v182, v25
	v_cmp_gt_f32_e32 vcc, v17, v16
	v_cmp_nlg_f32_e64 s[8:9], s57, v16
	s_waitcnt lgkmcnt(2)
	v_add_f32_e32 v12, v12, v13
	s_waitcnt lgkmcnt(1)
	v_add_f32_e32 v14, v14, v26
	s_waitcnt lgkmcnt(0)
	v_add_f32_e32 v25, v25, v15
	ds_bpermute_b32 v13, v186, v12
	ds_bpermute_b32 v26, v185, v14
	ds_bpermute_b32 v27, v183, v25
	s_waitcnt lgkmcnt(2)
	v_add_f32_e32 v15, v12, v13
	s_waitcnt lgkmcnt(1)
	v_add_f32_e32 v12, v14, v26
	s_waitcnt lgkmcnt(0)
	v_add_f32_e32 v14, v25, v27
	ds_bpermute_b32 v26, v182, v24
	ds_bpermute_b32 v13, v182, v23
	ds_bpermute_b32 v25, v184, v14
	ds_bpermute_b32 v27, v186, v12
	ds_bpermute_b32 v35, v187, v15
	s_waitcnt lgkmcnt(4)
	v_add_f32_e32 v24, v24, v26
	s_waitcnt lgkmcnt(3)
	v_add_f32_e32 v13, v23, v13
	s_waitcnt lgkmcnt(2)
	v_add_f32_e32 v14, v14, v25
	ds_bpermute_b32 v25, v183, v24
	ds_bpermute_b32 v23, v183, v13
	s_waitcnt lgkmcnt(3)
	v_add_f32_e32 v40, v12, v27
	ds_bpermute_b32 v26, v185, v14
	ds_bpermute_b32 v59, v187, v40
	s_waitcnt lgkmcnt(3)
	v_add_f32_e32 v12, v24, v25
	s_waitcnt lgkmcnt(2)
	v_add_f32_e32 v13, v13, v23
	ds_bpermute_b32 v24, v184, v12
	ds_bpermute_b32 v23, v184, v13
	s_waitcnt lgkmcnt(3)
; template <bool COMBINE, bool ROUTE, bool FINAL, bool OUT8 = false, bool DUMMY = false> ...
;     ...
;                 for (int e = 0; e < 16; ++e) { lg[e] = wave_sum(lg[e]); sc_[e] = 1.f / (1.f + expf(-lg[e])); sel[e] = sc_[e] + rb[e]; }
;                 float gsv[4], gw1[4], gw2[4]; int gi1[4], gi2[4];
; #pragma unroll
;                 for (int gq = 0; gq < 4; ++gq) {
;                     float m1 = sel[4 * gq]; int i1 = 0; float s1 = sc_[4 * gq];
; #pragma unroll
;                     for (int i = 1; i < 4; ++i) if (sel[4 * gq + i] > m1) { m1 = sel[4 * gq + i]; i1 = i; s1 = sc_[4 * gq + i]; }
;                     float m2 = -INFINITY; int i2 = 0; float s2 = 0.f;
; #pragma unroll
;                     for (int i = 0; i < 4; ++i) if (i != i1 && sel[4 * gq + i] > m2) { m2 = sel[4 * gq + i]; i2 = i; s2 = sc_[4 * gq + i]; }
;                     gsv[gq] = m1 + m2; gi1[gq] = 4 * gq + i1; gi2[gq] = 4 * gq + i2; gw1[gq] = s1; gw2[gq] = s2;
;                 }
;                 float bv = gsv[0]; int e0 = gi1[0], e1 = gi2[0]; float w0 = gw1[0], w1 = gw2[0];
; #pragma unroll
;                 for (int gq = 1; gq < 4; ++gq) if (gsv[gq] > bv) { bv = gsv[gq]; e0 = gi1[gq]; e1 = gi2[gq]; w0 = gw1[gq]; w1 = gw2[gq]; }
	v_add_f32_e32 v14, v14, v26
	ds_bpermute_b32 v25, v186, v14
	s_waitcnt lgkmcnt(2)
	v_add_f32_e32 v12, v12, v24
	s_waitcnt lgkmcnt(1)
	v_add_f32_e32 v13, v13, v23
	ds_bpermute_b32 v24, v185, v12
	ds_bpermute_b32 v23, v185, v13
	s_waitcnt lgkmcnt(2)
	v_add_f32_e32 v14, v14, v25
	ds_bpermute_b32 v33, v187, v14
	s_waitcnt lgkmcnt(2)
	v_add_f32_e32 v12, v12, v24
	s_waitcnt lgkmcnt(1)
	v_add_f32_e32 v13, v13, v23
	ds_bpermute_b32 v24, v186, v12
	ds_bpermute_b32 v23, v186, v13
	s_waitcnt lgkmcnt(1)
	v_add_f32_e32 v26, v12, v24
	ds_bpermute_b32 v12, v182, v3
	s_waitcnt lgkmcnt(1)
	v_add_f32_e32 v30, v13, v23
	ds_bpermute_b32 v13, v182, v22
	ds_bpermute_b32 v23, v182, v1
	ds_bpermute_b32 v31, v187, v30
	s_waitcnt lgkmcnt(3)
	v_add_f32_e32 v3, v3, v12
	ds_bpermute_b32 v12, v183, v3
	s_waitcnt lgkmcnt(3)
	v_add_f32_e32 v13, v22, v13
	s_waitcnt lgkmcnt(2)
	v_add_f32_e32 v1, v1, v23
	ds_bpermute_b32 v22, v183, v13
	ds_bpermute_b32 v23, v183, v1
	s_waitcnt lgkmcnt(2)
	v_add_f32_e32 v3, v3, v12
	ds_bpermute_b32 v12, v184, v3
	ds_bpermute_b32 v27, v187, v26
	s_waitcnt lgkmcnt(3)
	v_add_f32_e32 v13, v13, v22
	s_waitcnt lgkmcnt(2)
	v_add_f32_e32 v1, v1, v23
	ds_bpermute_b32 v22, v184, v13
	ds_bpermute_b32 v23, v184, v1
	s_waitcnt lgkmcnt(3)
	v_add_f32_e32 v3, v3, v12
	ds_bpermute_b32 v12, v185, v3
	s_waitcnt lgkmcnt(2)
	v_add_f32_e32 v13, v13, v22
	s_waitcnt lgkmcnt(1)
	v_add_f32_e32 v1, v1, v23
	ds_bpermute_b32 v22, v185, v13
	ds_bpermute_b32 v23, v185, v1
	s_waitcnt lgkmcnt(2)
	v_add_f32_e32 v3, v3, v12
	ds_bpermute_b32 v12, v186, v3
	s_waitcnt lgkmcnt(2)
	v_add_f32_e32 v13, v13, v22
	s_waitcnt lgkmcnt(1)
	v_add_f32_e32 v1, v1, v23
	ds_bpermute_b32 v22, v186, v13
	ds_bpermute_b32 v23, v186, v1
	s_waitcnt lgkmcnt(2)
	v_add_f32_e32 v24, v3, v12
	v_cndmask_b32_e32 v12, v16, v17, vcc
	v_cndmask_b32_e64 v3, 0, 1, vcc
	s_waitcnt lgkmcnt(1)
	v_add_f32_e32 v28, v13, v22
	s_waitcnt lgkmcnt(0)
	v_add_f32_e32 v22, v1, v23
	v_cndmask_b32_e32 v1, v20, v21, vcc
	v_cmp_gt_f32_e32 vcc, v67, v12
	ds_bpermute_b32 v29, v187, v28
	ds_bpermute_b32 v25, v187, v24
	v_cndmask_b32_e32 v12, v12, v67, vcc
	v_cndmask_b32_e32 v1, v1, v0, vcc
	v_cndmask_b32_e64 v13, v3, 2, vcc
	v_cmp_ngt_f32_e32 vcc, v65, v12
	ds_bpermute_b32 v23, v187, v22
	s_nop 0
	v_cndmask_b32_e32 v71, v65, v12, vcc
	v_cndmask_b32_e32 v12, 3, v13, vcc
	v_cmp_eq_u32_e64 s[10:11], 0, v12
	s_or_b64 s[8:9], s[10:11], s[8:9]
	v_cndmask_b32_e32 v3, v63, v1, vcc
	v_cndmask_b32_e64 v1, v16, v147, s[8:9]
	v_cndmask_b32_e64 v13, v20, 0, s[8:9]
	v_cmp_ne_u32_e64 s[8:9], 1, v12
	v_cmp_gt_f32_e64 s[10:11], v17, v1
	s_and_b64 s[8:9], s[8:9], s[10:11]
	v_cndmask_b32_e64 v1, v1, v17, s[8:9]
	v_cndmask_b32_e64 v16, 0, 1, s[8:9]
	v_cndmask_b32_e64 v13, v13, v21, s[8:9]
	v_cmp_ne_u32_e64 s[8:9], 2, v12
	v_cmp_gt_f32_e64 s[10:11], v67, v1
	s_and_b64 s[8:9], s[8:9], s[10:11]
	v_cndmask_b32_e64 v1, v1, v67, s[8:9]
	v_cndmask_b32_e64 v16, v16, 2, s[8:9]
	v_cndmask_b32_e64 v0, v13, v0, s[8:9]
	v_cmp_gt_f32_e64 s[8:9], v65, v1
	s_and_b64 vcc, vcc, s[8:9]
	v_cndmask_b32_e32 v17, v1, v65, vcc
	v_cndmask_b32_e64 v1, v16, 3, vcc
	v_cndmask_b32_e32 v13, v0, v63, vcc
	v_cmp_gt_f32_e32 vcc, v73, v72
	v_add_f32_e32 v16, v71, v17
	s_nop 0
	v_cndmask_b32_e32 v17, v72, v73, vcc
	v_cmp_gt_f32_e64 s[8:9], v61, v17
	v_cndmask_b32_e64 v0, 0, 1, vcc
	s_nop 0
	v_cndmask_b32_e64 v20, v17, v61, s[8:9]
	v_cndmask_b32_e64 v0, v0, 2, s[8:9]
	v_cmp_ngt_f32_e64 s[10:11], v69, v20
	s_nop 1
	v_cndmask_b32_e64 v17, 3, v0, s[10:11]
	v_cmp_eq_u32_e64 s[12:13], 0, v17
	s_or_b64 s[12:13], s[12:13], s[14:15]
	v_cndmask_b32_e64 v0, v69, v20, s[10:11]
	v_cndmask_b32_e64 v20, v72, v147, s[12:13]
	v_cmp_ne_u32_e64 s[14:15], 1, v17
	v_cmp_gt_f32_e64 s[16:17], v73, v20
	s_and_b64 s[14:15], s[14:15], s[16:17]
	v_cndmask_b32_e64 v20, v20, v73, s[14:15]
	v_cmp_ne_u32_e64 s[16:17], 2, v17
	v_cmp_gt_f32_e64 s[18:19], v61, v20
	s_and_b64 s[16:17], s[16:17], s[18:19]
	v_cndmask_b32_e64 v20, v20, v61, s[16:17]
	v_cmp_gt_f32_e64 s[18:19], v69, v20
	s_and_b64 s[18:19], s[10:11], s[18:19]
	s_nop 0
	v_cndmask_b32_e64 v20, v20, v69, s[18:19]
	v_add_f32_e32 v20, v0, v20
	v_cmp_gt_f32_e64 s[22:23], v20, v16
	s_and_saveexec_b64 s[54:55], s[22:23]
	s_cbranch_execz .LBB0_1111
	v_cndmask_b32_e64 v0, 4, 5, s[14:15]
	v_cndmask_b32_e64 v0, v0, 6, s[16:17]
	v_cndmask_b32_e64 v1, v0, 7, s[18:19]
	v_cndmask_b32_e64 v0, v18, 0, s[12:13]
	v_cndmask_b32_e64 v0, v0, v19, s[14:15]
	v_cndmask_b32_e64 v0, v0, v32, s[16:17]
	v_cndmask_b32_e64 v13, v0, v34, s[18:19]
	v_cndmask_b32_e32 v0, v18, v19, vcc
	v_cndmask_b32_e64 v0, v0, v32, s[8:9]
	v_or_b32_e32 v12, 4, v17
	v_cndmask_b32_e64 v3, v34, v0, s[10:11]
	v_mov_b32_e32 v16, v20
